# GEMM K loops: the per-MFMA-group s_setprio 1/0 toggles removed (192 instructions)
# baseline (speedup 1.0000x reference)
.LBB0_417:
	ds_read_b128 v[130:133], v144
	ds_read_b128 v[134:137], v144 offset:1024
	ds_read_b128 v[150:153], v144 offset:2048
	ds_read_b128 v[154:157], v144 offset:3072
	ds_read_b128 v[158:161], v145
	ds_read_b128 v[162:165], v145 offset:1024
	ds_read_b128 v[166:169], v145 offset:2048
	ds_read_b128 v[170:173], v145 offset:3072
	s_add_i32 s10, s28, 0xfffc0080
	s_cmp_eq_u32 s65, 12
	s_cselect_b32 s68, s5, s10
	s_cselect_b32 s67, s4, s29
	s_or_b32 s66, s68, 0x80
	s_mov_b32 m0, s55
	ds_read_b128 v[174:177], v146
	ds_read_b128 v[178:181], v146 offset:1024
	ds_read_b128 v[182:185], v146 offset:2048
	ds_read_b128 v[186:189], v146 offset:3072
	ds_read_b128 v[190:193], v146 offset:4096
	ds_read_b128 v[194:197], v146 offset:5120
	ds_read_b128 v[198:201], v146 offset:6144
	ds_read_b128 v[202:205], v146 offset:7168
	buffer_load_dwordx4 v139, s[12:15], s28 offen lds
	s_mov_b32 m0, s56
	s_nop 0
	buffer_load_dwordx4 v140, s[12:15], s28 offen lds
	s_waitcnt vmcnt(8)
	s_waitcnt lgkmcnt(0)
	s_barrier
	s_waitcnt lgkmcnt(7)
	v_mfma_i32_16x16x64_i8 v[126:129], v[130:133], v[174:177], v[126:129]
	v_mfma_i32_16x16x64_i8 v[122:125], v[150:153], v[174:177], v[122:125]
	s_waitcnt lgkmcnt(5)
	v_mfma_i32_16x16x64_i8 v[110:113], v[130:133], v[182:185], v[110:113]
	v_mfma_i32_16x16x64_i8 v[106:109], v[150:153], v[182:185], v[106:109]
	s_waitcnt lgkmcnt(3)
	v_mfma_i32_16x16x64_i8 v[94:97], v[130:133], v[190:193], v[94:97]
	v_mfma_i32_16x16x64_i8 v[90:93], v[150:153], v[190:193], v[90:93]
	s_waitcnt lgkmcnt(1)
	v_mfma_i32_16x16x64_i8 v[78:81], v[130:133], v[198:201], v[78:81]
	v_mfma_i32_16x16x64_i8 v[74:77], v[150:153], v[198:201], v[74:77]
	v_mfma_i32_16x16x64_i8 v[126:129], v[134:137], v[178:181], v[126:129]
	v_mfma_i32_16x16x64_i8 v[122:125], v[154:157], v[178:181], v[122:125]
	v_mfma_i32_16x16x64_i8 v[110:113], v[134:137], v[186:189], v[110:113]
	v_mfma_i32_16x16x64_i8 v[106:109], v[154:157], v[186:189], v[106:109]
	v_mfma_i32_16x16x64_i8 v[94:97], v[134:137], v[194:197], v[94:97]
	v_mfma_i32_16x16x64_i8 v[90:93], v[154:157], v[194:197], v[90:93]
	s_waitcnt lgkmcnt(0)
	v_mfma_i32_16x16x64_i8 v[78:81], v[134:137], v[202:205], v[78:81]
	v_mfma_i32_16x16x64_i8 v[74:77], v[154:157], v[202:205], v[74:77]
	v_mfma_i32_16x16x64_i8 v[118:121], v[158:161], v[174:177], v[118:121]
	v_mfma_i32_16x16x64_i8 v[114:117], v[166:169], v[174:177], v[114:117]
	v_mfma_i32_16x16x64_i8 v[102:105], v[158:161], v[182:185], v[102:105]
	v_mfma_i32_16x16x64_i8 v[98:101], v[166:169], v[182:185], v[98:101]
	v_mfma_i32_16x16x64_i8 v[86:89], v[158:161], v[190:193], v[86:89]
	v_mfma_i32_16x16x64_i8 v[82:85], v[166:169], v[190:193], v[82:85]
	v_mfma_i32_16x16x64_i8 v[70:73], v[158:161], v[198:201], v[70:73]
	v_mfma_i32_16x16x64_i8 v[66:69], v[166:169], v[198:201], v[66:69]
	v_mfma_i32_16x16x64_i8 v[118:121], v[162:165], v[178:181], v[118:121]
	v_mfma_i32_16x16x64_i8 v[114:117], v[170:173], v[178:181], v[114:117]
	v_mfma_i32_16x16x64_i8 v[102:105], v[162:165], v[186:189], v[102:105]
	v_mfma_i32_16x16x64_i8 v[98:101], v[170:173], v[186:189], v[98:101]
	v_mfma_i32_16x16x64_i8 v[86:89], v[162:165], v[194:197], v[86:89]
	v_mfma_i32_16x16x64_i8 v[82:85], v[170:173], v[194:197], v[82:85]
	v_mfma_i32_16x16x64_i8 v[70:73], v[162:165], v[202:205], v[70:73]
	v_mfma_i32_16x16x64_i8 v[66:69], v[170:173], v[202:205], v[66:69]
	s_barrier
	s_mov_b32 m0, s33
	s_mov_b32 s10, s14
	s_mov_b32 s11, s15
	ds_read_b128 v[174:177], v146 offset:16384
	ds_read_b128 v[178:181], v146 offset:17408
	ds_read_b128 v[182:185], v146 offset:18432
	ds_read_b128 v[186:189], v146 offset:19456
	ds_read_b128 v[190:193], v146 offset:20480
	ds_read_b128 v[194:197], v146 offset:21504
	ds_read_b128 v[198:201], v146 offset:22528
	ds_read_b128 v[202:205], v146 offset:23552
	buffer_load_dwordx4 v1, s[8:11], s67 offen lds
	s_mov_b32 m0, s34
	s_add_i32 s69, s67, 0x40000
	buffer_load_dwordx4 v138, s[8:11], s67 offen lds
	s_mov_b32 m0, s35
	s_nop 0
	buffer_load_dwordx4 v1, s[8:11], s69 offen lds
	s_mov_b32 m0, s38
	s_nop 0
	buffer_load_dwordx4 v138, s[8:11], s69 offen lds
	s_mov_b32 m0, s31
	s_nop 0
	buffer_load_dwordx4 v139, s[12:15], s68 offen lds
	s_mov_b32 m0, s39
	s_nop 0
	buffer_load_dwordx4 v140, s[12:15], s68 offen lds
	s_waitcnt vmcnt(8)
	s_waitcnt lgkmcnt(0)
	s_barrier
	s_waitcnt lgkmcnt(7)
	v_mfma_i32_16x16x64_i8 v[62:65], v[130:133], v[174:177], v[62:65]
	v_mfma_i32_16x16x64_i8 v[58:61], v[150:153], v[174:177], v[58:61]
	s_waitcnt lgkmcnt(5)
	v_mfma_i32_16x16x64_i8 v[46:49], v[130:133], v[182:185], v[46:49]
	v_mfma_i32_16x16x64_i8 v[42:45], v[150:153], v[182:185], v[42:45]
	s_waitcnt lgkmcnt(3)
	v_mfma_i32_16x16x64_i8 v[30:33], v[130:133], v[190:193], v[30:33]
	v_mfma_i32_16x16x64_i8 v[26:29], v[150:153], v[190:193], v[26:29]
	s_waitcnt lgkmcnt(1)
	v_mfma_i32_16x16x64_i8 v[14:17], v[130:133], v[198:201], v[14:17]
	v_mfma_i32_16x16x64_i8 v[10:13], v[150:153], v[198:201], v[10:13]
	v_mfma_i32_16x16x64_i8 v[62:65], v[134:137], v[178:181], v[62:65]
	v_mfma_i32_16x16x64_i8 v[58:61], v[154:157], v[178:181], v[58:61]
	v_mfma_i32_16x16x64_i8 v[46:49], v[134:137], v[186:189], v[46:49]
	v_mfma_i32_16x16x64_i8 v[42:45], v[154:157], v[186:189], v[42:45]
	v_mfma_i32_16x16x64_i8 v[30:33], v[134:137], v[194:197], v[30:33]
	v_mfma_i32_16x16x64_i8 v[26:29], v[154:157], v[194:197], v[26:29]
	s_waitcnt lgkmcnt(0)
	v_mfma_i32_16x16x64_i8 v[14:17], v[134:137], v[202:205], v[14:17]
	v_mfma_i32_16x16x64_i8 v[10:13], v[154:157], v[202:205], v[10:13]
	v_mfma_i32_16x16x64_i8 v[54:57], v[158:161], v[174:177], v[54:57]
	v_mfma_i32_16x16x64_i8 v[50:53], v[166:169], v[174:177], v[50:53]
	v_mfma_i32_16x16x64_i8 v[38:41], v[158:161], v[182:185], v[38:41]
	v_mfma_i32_16x16x64_i8 v[34:37], v[166:169], v[182:185], v[34:37]
	v_mfma_i32_16x16x64_i8 v[22:25], v[158:161], v[190:193], v[22:25]
	v_mfma_i32_16x16x64_i8 v[18:21], v[166:169], v[190:193], v[18:21]
	v_mfma_i32_16x16x64_i8 v[6:9], v[158:161], v[198:201], v[6:9]
	v_mfma_i32_16x16x64_i8 v[2:5], v[166:169], v[198:201], v[2:5]
	v_mfma_i32_16x16x64_i8 v[54:57], v[162:165], v[178:181], v[54:57]
	v_mfma_i32_16x16x64_i8 v[50:53], v[170:173], v[178:181], v[50:53]
	v_mfma_i32_16x16x64_i8 v[38:41], v[162:165], v[186:189], v[38:41]
	v_mfma_i32_16x16x64_i8 v[34:37], v[170:173], v[186:189], v[34:37]
	v_mfma_i32_16x16x64_i8 v[22:25], v[162:165], v[194:197], v[22:25]
	v_mfma_i32_16x16x64_i8 v[18:21], v[170:173], v[194:197], v[18:21]
	v_mfma_i32_16x16x64_i8 v[6:9], v[162:165], v[202:205], v[6:9]
	v_mfma_i32_16x16x64_i8 v[2:5], v[170:173], v[202:205], v[2:5]
	s_barrier
	ds_read_b128 v[130:133], v147
	ds_read_b128 v[134:137], v147 offset:1024
	ds_read_b128 v[150:153], v147 offset:2048
	ds_read_b128 v[154:157], v147 offset:3072
	ds_read_b128 v[158:161], v148
	ds_read_b128 v[162:165], v148 offset:1024
	ds_read_b128 v[166:169], v148 offset:2048
	ds_read_b128 v[170:173], v148 offset:3072
	s_add_i32 s68, s68, 0x40000
	s_mov_b32 m0, s46
	ds_read_b128 v[174:177], v146 offset:32768
	ds_read_b128 v[178:181], v146 offset:33792
	ds_read_b128 v[182:185], v146 offset:34816
	ds_read_b128 v[186:189], v146 offset:35840
	ds_read_b128 v[190:193], v146 offset:36864
	ds_read_b128 v[194:197], v146 offset:37888
	ds_read_b128 v[198:201], v146 offset:38912
	ds_read_b128 v[202:205], v146 offset:39936
	buffer_load_dwordx4 v139, s[12:15], s68 offen lds
	s_mov_b32 m0, s47
	s_nop 0
	buffer_load_dwordx4 v140, s[12:15], s68 offen lds
	s_waitcnt vmcnt(8)
	s_waitcnt lgkmcnt(0)
	s_barrier
	s_waitcnt lgkmcnt(7)
	v_mfma_i32_16x16x64_i8 v[126:129], v[130:133], v[174:177], v[126:129]
	v_mfma_i32_16x16x64_i8 v[122:125], v[150:153], v[174:177], v[122:125]
	s_waitcnt lgkmcnt(5)
	v_mfma_i32_16x16x64_i8 v[110:113], v[130:133], v[182:185], v[110:113]
	v_mfma_i32_16x16x64_i8 v[106:109], v[150:153], v[182:185], v[106:109]
	s_waitcnt lgkmcnt(3)
	v_mfma_i32_16x16x64_i8 v[94:97], v[130:133], v[190:193], v[94:97]
	v_mfma_i32_16x16x64_i8 v[90:93], v[150:153], v[190:193], v[90:93]
	s_waitcnt lgkmcnt(1)
	v_mfma_i32_16x16x64_i8 v[78:81], v[130:133], v[198:201], v[78:81]
	v_mfma_i32_16x16x64_i8 v[74:77], v[150:153], v[198:201], v[74:77]
	v_mfma_i32_16x16x64_i8 v[126:129], v[134:137], v[178:181], v[126:129]
	v_mfma_i32_16x16x64_i8 v[122:125], v[154:157], v[178:181], v[122:125]
	v_mfma_i32_16x16x64_i8 v[110:113], v[134:137], v[186:189], v[110:113]
	v_mfma_i32_16x16x64_i8 v[106:109], v[154:157], v[186:189], v[106:109]
	v_mfma_i32_16x16x64_i8 v[94:97], v[134:137], v[194:197], v[94:97]
	v_mfma_i32_16x16x64_i8 v[90:93], v[154:157], v[194:197], v[90:93]
	s_waitcnt lgkmcnt(0)
	v_mfma_i32_16x16x64_i8 v[78:81], v[134:137], v[202:205], v[78:81]
	v_mfma_i32_16x16x64_i8 v[74:77], v[154:157], v[202:205], v[74:77]
	v_mfma_i32_16x16x64_i8 v[118:121], v[158:161], v[174:177], v[118:121]
	v_mfma_i32_16x16x64_i8 v[114:117], v[166:169], v[174:177], v[114:117]
	v_mfma_i32_16x16x64_i8 v[102:105], v[158:161], v[182:185], v[102:105]
	v_mfma_i32_16x16x64_i8 v[98:101], v[166:169], v[182:185], v[98:101]
	v_mfma_i32_16x16x64_i8 v[86:89], v[158:161], v[190:193], v[86:89]
	v_mfma_i32_16x16x64_i8 v[82:85], v[166:169], v[190:193], v[82:85]
	v_mfma_i32_16x16x64_i8 v[70:73], v[158:161], v[198:201], v[70:73]
	v_mfma_i32_16x16x64_i8 v[66:69], v[166:169], v[198:201], v[66:69]
	v_mfma_i32_16x16x64_i8 v[118:121], v[162:165], v[178:181], v[118:121]
	v_mfma_i32_16x16x64_i8 v[114:117], v[170:173], v[178:181], v[114:117]
	v_mfma_i32_16x16x64_i8 v[102:105], v[162:165], v[186:189], v[102:105]
	v_mfma_i32_16x16x64_i8 v[98:101], v[170:173], v[186:189], v[98:101]
	v_mfma_i32_16x16x64_i8 v[86:89], v[162:165], v[194:197], v[86:89]
	v_mfma_i32_16x16x64_i8 v[82:85], v[170:173], v[194:197], v[82:85]
	v_mfma_i32_16x16x64_i8 v[70:73], v[162:165], v[202:205], v[70:73]
	v_mfma_i32_16x16x64_i8 v[66:69], v[170:173], v[202:205], v[66:69]
	s_barrier
	s_mov_b32 m0, s48
	s_or_b32 s68, s67, 0x80
	ds_read_b128 v[174:177], v146 offset:49152
	ds_read_b128 v[178:181], v146 offset:50176
	ds_read_b128 v[182:185], v146 offset:51200
	ds_read_b128 v[186:189], v146 offset:52224
	ds_read_b128 v[190:193], v146 offset:53248
	ds_read_b128 v[194:197], v146 offset:54272
	ds_read_b128 v[198:201], v146 offset:55296
	ds_read_b128 v[202:205], v146 offset:56320
	buffer_load_dwordx4 v1, s[8:11], s68 offen lds
	s_mov_b32 m0, s49
	s_add_i32 s67, s67, 0x40080
	buffer_load_dwordx4 v138, s[8:11], s68 offen lds
	s_mov_b32 m0, s52
	s_nop 0
	buffer_load_dwordx4 v1, s[8:11], s67 offen lds
	s_mov_b32 m0, s53
	s_nop 0
	buffer_load_dwordx4 v138, s[8:11], s67 offen lds
	s_mov_b32 m0, s50
	s_nop 0
	buffer_load_dwordx4 v139, s[12:15], s66 offen lds
	s_mov_b32 m0, s51
	s_nop 0
	buffer_load_dwordx4 v140, s[12:15], s66 offen lds
	s_waitcnt vmcnt(8)
	s_waitcnt lgkmcnt(0)
	s_barrier
	s_waitcnt lgkmcnt(7)
	v_mfma_i32_16x16x64_i8 v[62:65], v[130:133], v[174:177], v[62:65]
	v_mfma_i32_16x16x64_i8 v[58:61], v[150:153], v[174:177], v[58:61]
	s_waitcnt lgkmcnt(5)
	v_mfma_i32_16x16x64_i8 v[46:49], v[130:133], v[182:185], v[46:49]
	v_mfma_i32_16x16x64_i8 v[42:45], v[150:153], v[182:185], v[42:45]
	s_waitcnt lgkmcnt(3)
	v_mfma_i32_16x16x64_i8 v[30:33], v[130:133], v[190:193], v[30:33]
	v_mfma_i32_16x16x64_i8 v[26:29], v[150:153], v[190:193], v[26:29]
	s_waitcnt lgkmcnt(1)
	v_mfma_i32_16x16x64_i8 v[14:17], v[130:133], v[198:201], v[14:17]
	v_mfma_i32_16x16x64_i8 v[10:13], v[150:153], v[198:201], v[10:13]
	v_mfma_i32_16x16x64_i8 v[62:65], v[134:137], v[178:181], v[62:65]
	v_mfma_i32_16x16x64_i8 v[58:61], v[154:157], v[178:181], v[58:61]
	v_mfma_i32_16x16x64_i8 v[46:49], v[134:137], v[186:189], v[46:49]
	v_mfma_i32_16x16x64_i8 v[42:45], v[154:157], v[186:189], v[42:45]
	v_mfma_i32_16x16x64_i8 v[30:33], v[134:137], v[194:197], v[30:33]
	v_mfma_i32_16x16x64_i8 v[26:29], v[154:157], v[194:197], v[26:29]
	s_waitcnt lgkmcnt(0)
	v_mfma_i32_16x16x64_i8 v[14:17], v[134:137], v[202:205], v[14:17]
	v_mfma_i32_16x16x64_i8 v[10:13], v[154:157], v[202:205], v[10:13]
	v_mfma_i32_16x16x64_i8 v[54:57], v[158:161], v[174:177], v[54:57]
	v_mfma_i32_16x16x64_i8 v[50:53], v[166:169], v[174:177], v[50:53]
	v_mfma_i32_16x16x64_i8 v[38:41], v[158:161], v[182:185], v[38:41]
	v_mfma_i32_16x16x64_i8 v[34:37], v[166:169], v[182:185], v[34:37]
	v_mfma_i32_16x16x64_i8 v[22:25], v[158:161], v[190:193], v[22:25]
	v_mfma_i32_16x16x64_i8 v[18:21], v[166:169], v[190:193], v[18:21]
	v_mfma_i32_16x16x64_i8 v[6:9], v[158:161], v[198:201], v[6:9]
	v_mfma_i32_16x16x64_i8 v[2:5], v[166:169], v[198:201], v[2:5]
	v_mfma_i32_16x16x64_i8 v[54:57], v[162:165], v[178:181], v[54:57]
	v_mfma_i32_16x16x64_i8 v[50:53], v[170:173], v[178:181], v[50:53]
	v_mfma_i32_16x16x64_i8 v[38:41], v[162:165], v[186:189], v[38:41]
	v_mfma_i32_16x16x64_i8 v[34:37], v[170:173], v[186:189], v[34:37]
	v_mfma_i32_16x16x64_i8 v[22:25], v[162:165], v[194:197], v[22:25]
	v_mfma_i32_16x16x64_i8 v[18:21], v[170:173], v[194:197], v[18:21]
	v_mfma_i32_16x16x64_i8 v[6:9], v[162:165], v[202:205], v[6:9]
	v_mfma_i32_16x16x64_i8 v[2:5], v[170:173], v[202:205], v[2:5]
	s_barrier
	s_add_i32 s65, s65, 2
	s_addk_i32 s28, 0x100
	s_addk_i32 s29, 0x100
	s_cmp_gt_u32 s65, 13
	s_cbranch_scc0 .LBB0_417
	s_and_b64 vcc, exec, s[24:25]
	s_cbranch_vccz .LBB0_420
	s_barrier

.LBB0_489:
	ds_read_b128 v[142:145], v136
	ds_read_b128 v[146:149], v136 offset:1024
	ds_read_b128 v[150:153], v136 offset:2048
	ds_read_b128 v[154:157], v136 offset:3072
	ds_read_b128 v[158:161], v137
	ds_read_b128 v[162:165], v137 offset:1024
	ds_read_b128 v[166:169], v137 offset:2048
	ds_read_b128 v[170:173], v137 offset:3072
	s_add_i32 s6, s67, 0xfffc0080
	s_cmp_eq_u32 s69, 12
	s_cselect_b32 s72, s66, s6
	s_cselect_b32 s71, s65, s68
	s_or_b32 s70, s72, 0x80
	s_mov_b32 m0, s47
	ds_read_b128 v[174:177], v138
	ds_read_b128 v[178:181], v138 offset:1024
	ds_read_b128 v[182:185], v138 offset:2048
	ds_read_b128 v[186:189], v138 offset:3072
	ds_read_b128 v[190:193], v138 offset:4096
	ds_read_b128 v[194:197], v138 offset:5120
	ds_read_b128 v[198:201], v138 offset:6144
	ds_read_b128 v[202:205], v138 offset:7168
	buffer_load_dwordx4 v131, s[8:11], s67 offen lds
	s_mov_b32 m0, s56
	s_nop 0
	buffer_load_dwordx4 v132, s[8:11], s67 offen lds
	s_waitcnt vmcnt(8)
	s_waitcnt lgkmcnt(0)
	s_barrier
	s_waitcnt lgkmcnt(6)
	v_mfma_f32_16x16x128_f8f6f4 v[126:129], v[142:149], v[174:181], v[126:129]
	v_mfma_f32_16x16x128_f8f6f4 v[122:125], v[150:157], v[174:181], v[122:125]
	s_waitcnt lgkmcnt(4)
	v_mfma_f32_16x16x128_f8f6f4 v[110:113], v[142:149], v[182:189], v[110:113]
	v_mfma_f32_16x16x128_f8f6f4 v[106:109], v[150:157], v[182:189], v[106:109]
	s_waitcnt lgkmcnt(2)
	v_mfma_f32_16x16x128_f8f6f4 v[206:209], v[142:149], v[190:197], v[94:97]
	v_mfma_f32_16x16x128_f8f6f4 v[210:213], v[150:157], v[190:197], v[90:93]
	s_waitcnt lgkmcnt(0)
	v_mfma_f32_16x16x128_f8f6f4 v[214:217], v[142:149], v[198:205], v[78:81]
	v_mfma_f32_16x16x128_f8f6f4 v[218:221], v[150:157], v[198:205], v[74:77]
	v_mfma_f32_16x16x128_f8f6f4 v[118:121], v[158:165], v[174:181], v[118:121]
	v_mfma_f32_16x16x128_f8f6f4 v[114:117], v[166:173], v[174:181], v[114:117]
	v_mfma_f32_16x16x128_f8f6f4 v[102:105], v[158:165], v[182:189], v[102:105]
	v_mfma_f32_16x16x128_f8f6f4 v[98:101], v[166:173], v[182:189], v[98:101]
	v_mfma_f32_16x16x128_f8f6f4 v[174:177], v[158:165], v[190:197], v[86:89]
	v_mfma_f32_16x16x128_f8f6f4 v[178:181], v[166:173], v[190:197], v[82:85]
	v_mfma_f32_16x16x128_f8f6f4 v[182:185], v[158:165], v[198:205], v[70:73]
	v_mfma_f32_16x16x128_f8f6f4 v[186:189], v[166:173], v[198:205], v[66:69]
	s_barrier
	s_mov_b32 m0, s23
	s_mov_b32 s6, s10
	s_mov_b32 s7, s11
	s_nop 1
	ds_read_b128 v[66:69], v138 offset:16384
	ds_read_b128 v[70:73], v138 offset:17408
	ds_read_b128 v[74:77], v138 offset:18432
	ds_read_b128 v[78:81], v138 offset:19456
	ds_read_b128 v[82:85], v138 offset:20480
	ds_read_b128 v[86:89], v138 offset:21504
	ds_read_b128 v[90:93], v138 offset:22528
	ds_read_b128 v[94:97], v138 offset:23552
	buffer_load_dwordx4 v1, s[4:7], s71 offen lds
	s_mov_b32 m0, s24
	s_add_i32 s73, s71, 0x40000
	buffer_load_dwordx4 v130, s[4:7], s71 offen lds
	s_mov_b32 m0, s25
	s_nop 0
	buffer_load_dwordx4 v1, s[4:7], s73 offen lds
	s_mov_b32 m0, s26
	s_nop 0
	buffer_load_dwordx4 v130, s[4:7], s73 offen lds
	s_mov_b32 m0, s22
	s_nop 0
	buffer_load_dwordx4 v131, s[8:11], s72 offen lds
	s_mov_b32 m0, s27
	s_nop 0
	buffer_load_dwordx4 v132, s[8:11], s72 offen lds
	s_waitcnt vmcnt(8)
	s_waitcnt lgkmcnt(0)
	s_barrier
	s_waitcnt lgkmcnt(6)
	v_mfma_f32_16x16x128_f8f6f4 v[62:65], v[142:149], v[66:73], v[62:65]
	v_mfma_f32_16x16x128_f8f6f4 v[54:57], v[150:157], v[66:73], v[54:57]
	s_waitcnt lgkmcnt(4)
	v_mfma_f32_16x16x128_f8f6f4 v[34:37], v[150:157], v[74:81], v[34:37]
	v_mfma_f32_16x16x128_f8f6f4 v[190:193], v[142:149], v[74:81], v[46:49]
	s_waitcnt lgkmcnt(2)
	v_mfma_f32_16x16x128_f8f6f4 v[194:197], v[142:149], v[82:89], v[26:29]
	v_mfma_f32_16x16x128_f8f6f4 v[198:201], v[150:157], v[82:89], v[18:21]
	s_waitcnt lgkmcnt(0)
	v_mfma_f32_16x16x128_f8f6f4 v[202:205], v[142:149], v[90:97], v[10:13]
	v_mfma_f32_16x16x128_f8f6f4 v[222:225], v[150:157], v[90:97], v[2:5]
	v_mfma_f32_16x16x128_f8f6f4 v[58:61], v[158:165], v[66:73], v[58:61]
	v_mfma_f32_16x16x128_f8f6f4 v[226:229], v[166:173], v[66:73], v[50:53]
	v_mfma_f32_16x16x128_f8f6f4 v[230:233], v[158:165], v[74:81], v[42:45]
	v_mfma_f32_16x16x128_f8f6f4 v[234:237], v[166:173], v[74:81], v[38:41]
	v_mfma_f32_16x16x128_f8f6f4 v[238:241], v[158:165], v[82:89], v[30:33]
	v_mfma_f32_16x16x128_f8f6f4 v[242:245], v[166:173], v[82:89], v[22:25]
	v_mfma_f32_16x16x128_f8f6f4 v[246:249], v[158:165], v[90:97], v[14:17]
	v_mfma_f32_16x16x128_f8f6f4 v[250:253], v[166:173], v[90:97], v[6:9]
	s_barrier
	ds_read_b128 v[2:5], v139
	s_nop 3
	ds_read_b128 v[6:9], v139 offset:1024
	ds_read_b128 v[38:41], v139 offset:2048
	ds_read_b128 v[42:45], v139 offset:3072
	ds_read_b128 v[142:145], v140
	ds_read_b128 v[146:149], v140 offset:1024
	ds_read_b128 v[150:153], v140 offset:2048
	ds_read_b128 v[154:157], v140 offset:3072
	s_add_i32 s72, s72, 0x40000
	s_mov_b32 m0, s28
	ds_read_b128 v[10:13], v138 offset:32768
	ds_read_b128 v[14:17], v138 offset:33792
	ds_read_b128 v[18:21], v138 offset:34816
	ds_read_b128 v[22:25], v138 offset:35840
	ds_read_b128 v[26:29], v138 offset:36864
	ds_read_b128 v[30:33], v138 offset:37888
	ds_read_b128 v[46:49], v138 offset:38912
	ds_read_b128 v[50:53], v138 offset:39936
	buffer_load_dwordx4 v131, s[8:11], s72 offen lds
	s_mov_b32 m0, s29
	s_nop 0
	buffer_load_dwordx4 v132, s[8:11], s72 offen lds
	s_waitcnt vmcnt(8)
	s_waitcnt lgkmcnt(0)
	s_barrier
	s_waitcnt lgkmcnt(6)
	v_mfma_f32_16x16x128_f8f6f4 v[126:129], v[2:9], v[10:17], v[126:129]
	v_mfma_f32_16x16x128_f8f6f4 v[122:125], v[38:45], v[10:17], v[122:125]
	s_waitcnt lgkmcnt(4)
	v_mfma_f32_16x16x128_f8f6f4 v[110:113], v[2:9], v[18:25], v[110:113]
	v_mfma_f32_16x16x128_f8f6f4 v[106:109], v[38:45], v[18:25], v[106:109]
	s_waitcnt lgkmcnt(2)
	v_mfma_f32_16x16x128_f8f6f4 v[94:97], v[2:9], v[26:33], v[206:209]
	v_mfma_f32_16x16x128_f8f6f4 v[90:93], v[38:45], v[26:33], v[210:213]
	s_waitcnt lgkmcnt(0)
	v_mfma_f32_16x16x128_f8f6f4 v[78:81], v[2:9], v[46:53], v[214:217]
	v_mfma_f32_16x16x128_f8f6f4 v[74:77], v[38:45], v[46:53], v[218:221]
	v_mfma_f32_16x16x128_f8f6f4 v[118:121], v[142:149], v[10:17], v[118:121]
	v_mfma_f32_16x16x128_f8f6f4 v[114:117], v[150:157], v[10:17], v[114:117]
	v_mfma_f32_16x16x128_f8f6f4 v[102:105], v[142:149], v[18:25], v[102:105]
	v_mfma_f32_16x16x128_f8f6f4 v[98:101], v[150:157], v[18:25], v[98:101]
	v_mfma_f32_16x16x128_f8f6f4 v[86:89], v[142:149], v[26:33], v[174:177]
	v_mfma_f32_16x16x128_f8f6f4 v[82:85], v[150:157], v[26:33], v[178:181]
	v_mfma_f32_16x16x128_f8f6f4 v[70:73], v[142:149], v[46:53], v[182:185]
	v_mfma_f32_16x16x128_f8f6f4 v[66:69], v[150:157], v[46:53], v[186:189]
	s_barrier
	s_mov_b32 m0, s33
	s_or_b32 s72, s71, 0x80
	ds_read_b128 v[158:161], v138 offset:49152
	ds_read_b128 v[162:165], v138 offset:50176
	ds_read_b128 v[166:169], v138 offset:51200
	ds_read_b128 v[170:173], v138 offset:52224
	ds_read_b128 v[174:177], v138 offset:53248
	ds_read_b128 v[178:181], v138 offset:54272
	ds_read_b128 v[182:185], v138 offset:55296
	ds_read_b128 v[186:189], v138 offset:56320
	buffer_load_dwordx4 v1, s[4:7], s72 offen lds
	s_mov_b32 m0, s34
	s_add_i32 s71, s71, 0x40080
	buffer_load_dwordx4 v130, s[4:7], s72 offen lds
	s_mov_b32 m0, s39
	s_nop 0
	buffer_load_dwordx4 v1, s[4:7], s71 offen lds
	s_mov_b32 m0, s46
	s_nop 0
	buffer_load_dwordx4 v130, s[4:7], s71 offen lds
	s_mov_b32 m0, s35
	s_nop 0
	buffer_load_dwordx4 v131, s[8:11], s70 offen lds
	s_mov_b32 m0, s38
	s_nop 0
	buffer_load_dwordx4 v132, s[8:11], s70 offen lds
	s_waitcnt vmcnt(8)
	s_waitcnt lgkmcnt(0)
	s_barrier
	s_waitcnt lgkmcnt(6)
	v_mfma_f32_16x16x128_f8f6f4 v[62:65], v[2:9], v[158:165], v[62:65]
	v_mfma_f32_16x16x128_f8f6f4 v[54:57], v[38:45], v[158:165], v[54:57]
	s_waitcnt lgkmcnt(4)
	v_mfma_f32_16x16x128_f8f6f4 v[46:49], v[2:9], v[166:173], v[190:193]
	v_mfma_f32_16x16x128_f8f6f4 v[34:37], v[38:45], v[166:173], v[34:37]
	s_waitcnt lgkmcnt(2)
	v_mfma_f32_16x16x128_f8f6f4 v[26:29], v[2:9], v[174:181], v[194:197]
	v_mfma_f32_16x16x128_f8f6f4 v[18:21], v[38:45], v[174:181], v[198:201]
	s_waitcnt lgkmcnt(0)
	v_mfma_f32_16x16x128_f8f6f4 v[10:13], v[2:9], v[182:189], v[202:205]
	v_mfma_f32_16x16x128_f8f6f4 v[2:5], v[38:45], v[182:189], v[222:225]
	v_mfma_f32_16x16x128_f8f6f4 v[58:61], v[142:149], v[158:165], v[58:61]
	v_mfma_f32_16x16x128_f8f6f4 v[50:53], v[150:157], v[158:165], v[226:229]
	v_mfma_f32_16x16x128_f8f6f4 v[42:45], v[142:149], v[166:173], v[230:233]
	v_mfma_f32_16x16x128_f8f6f4 v[38:41], v[150:157], v[166:173], v[234:237]
	v_mfma_f32_16x16x128_f8f6f4 v[30:33], v[142:149], v[174:181], v[238:241]
	v_mfma_f32_16x16x128_f8f6f4 v[22:25], v[150:157], v[174:181], v[242:245]
	v_mfma_f32_16x16x128_f8f6f4 v[14:17], v[142:149], v[182:189], v[246:249]
	v_mfma_f32_16x16x128_f8f6f4 v[6:9], v[150:157], v[182:189], v[250:253]
	s_barrier
	s_add_i32 s69, s69, 2
	s_addk_i32 s67, 0x100
	s_addk_i32 s68, 0x100
	s_cmp_gt_u32 s69, 13
	s_cbranch_scc0 .LBB0_489
	s_and_b64 vcc, exec, s[18:19]
	s_cbranch_vccz .LBB0_492
	s_barrier

.LBB0_1523:
	ds_read_b128 v[130:133], v144
	ds_read_b128 v[134:137], v144 offset:1024
	ds_read_b128 v[150:153], v144 offset:2048
	ds_read_b128 v[154:157], v144 offset:3072
	ds_read_b128 v[158:161], v145
	ds_read_b128 v[162:165], v145 offset:1024
	ds_read_b128 v[166:169], v145 offset:2048
	ds_read_b128 v[170:173], v145 offset:3072
	s_add_i32 s70, s69, -2
	s_add_i32 s71, s67, 0xfffc0080
	s_cmp_eq_u32 s53, s69
	s_cselect_b64 s[26:27], -1, 0
	s_and_b64 s[6:7], s[26:27], exec
	s_cselect_b32 s73, s66, s71
	s_cselect_b32 s72, s65, s68
	s_or_b32 s71, s73, 0x80
	s_mov_b32 m0, s56
	ds_read_b128 v[174:177], v146
	ds_read_b128 v[178:181], v146 offset:1024
	ds_read_b128 v[182:185], v146 offset:2048
	ds_read_b128 v[186:189], v146 offset:3072
	ds_read_b128 v[190:193], v146 offset:4096
	ds_read_b128 v[194:197], v146 offset:5120
	ds_read_b128 v[198:201], v146 offset:6144
	ds_read_b128 v[202:205], v146 offset:7168
	buffer_load_dwordx4 v139, s[8:11], s67 offen lds
	s_mov_b32 m0, s58
	s_nop 0
	buffer_load_dwordx4 v140, s[8:11], s67 offen lds
	s_waitcnt vmcnt(8)
	s_waitcnt lgkmcnt(0)
	s_barrier
	s_waitcnt lgkmcnt(6)
	v_mfma_f32_16x16x128_f8f6f4 v[126:129], v[130:137], v[174:181], v[126:129]
	v_mfma_f32_16x16x128_f8f6f4 v[122:125], v[150:157], v[174:181], v[122:125]
	s_waitcnt lgkmcnt(4)
	v_mfma_f32_16x16x128_f8f6f4 v[110:113], v[130:137], v[182:189], v[110:113]
	v_mfma_f32_16x16x128_f8f6f4 v[106:109], v[150:157], v[182:189], v[106:109]
	s_waitcnt lgkmcnt(2)
	v_mfma_f32_16x16x128_f8f6f4 v[206:209], v[130:137], v[190:197], v[94:97]
	v_mfma_f32_16x16x128_f8f6f4 v[210:213], v[150:157], v[190:197], v[90:93]
	s_waitcnt lgkmcnt(0)
	v_mfma_f32_16x16x128_f8f6f4 v[214:217], v[130:137], v[198:205], v[78:81]
	v_mfma_f32_16x16x128_f8f6f4 v[218:221], v[150:157], v[198:205], v[74:77]
	v_mfma_f32_16x16x128_f8f6f4 v[118:121], v[158:165], v[174:181], v[118:121]
	v_mfma_f32_16x16x128_f8f6f4 v[114:117], v[166:173], v[174:181], v[114:117]
	v_mfma_f32_16x16x128_f8f6f4 v[102:105], v[158:165], v[182:189], v[102:105]
	v_mfma_f32_16x16x128_f8f6f4 v[98:101], v[166:173], v[182:189], v[98:101]
	v_mfma_f32_16x16x128_f8f6f4 v[174:177], v[158:165], v[190:197], v[86:89]
	v_mfma_f32_16x16x128_f8f6f4 v[178:181], v[166:173], v[190:197], v[82:85]
	v_mfma_f32_16x16x128_f8f6f4 v[182:185], v[158:165], v[198:205], v[70:73]
	v_mfma_f32_16x16x128_f8f6f4 v[186:189], v[166:173], v[198:205], v[66:69]
	s_barrier
	s_mov_b32 m0, s30
	s_mov_b32 s6, s10
	s_mov_b32 s7, s11
	s_nop 1
	ds_read_b128 v[66:69], v146 offset:16384
	ds_read_b128 v[70:73], v146 offset:17408
	ds_read_b128 v[74:77], v146 offset:18432
	ds_read_b128 v[78:81], v146 offset:19456
	ds_read_b128 v[82:85], v146 offset:20480
	ds_read_b128 v[86:89], v146 offset:21504
	ds_read_b128 v[90:93], v146 offset:22528
	ds_read_b128 v[94:97], v146 offset:23552
	buffer_load_dwordx4 v1, s[4:7], s72 offen lds
	s_mov_b32 m0, s31
	s_add_i32 s74, s72, 0x40000
	buffer_load_dwordx4 v138, s[4:7], s72 offen lds
	s_mov_b32 m0, s33
	s_nop 0
	buffer_load_dwordx4 v1, s[4:7], s74 offen lds
	s_mov_b32 m0, s34
	s_nop 0
	buffer_load_dwordx4 v138, s[4:7], s74 offen lds
	s_mov_b32 m0, s29
	s_nop 0
	buffer_load_dwordx4 v139, s[8:11], s73 offen lds
	s_mov_b32 m0, s35
	s_nop 0
	buffer_load_dwordx4 v140, s[8:11], s73 offen lds
	s_waitcnt vmcnt(8)
	s_waitcnt lgkmcnt(0)
	s_barrier
	s_waitcnt lgkmcnt(6)
	v_mfma_f32_16x16x128_f8f6f4 v[62:65], v[130:137], v[66:73], v[62:65]
	v_mfma_f32_16x16x128_f8f6f4 v[58:61], v[150:157], v[66:73], v[58:61]
	s_waitcnt lgkmcnt(4)
	v_mfma_f32_16x16x128_f8f6f4 v[190:193], v[130:137], v[74:81], v[46:49]
	v_mfma_f32_16x16x128_f8f6f4 v[194:197], v[150:157], v[74:81], v[42:45]
	s_waitcnt lgkmcnt(2)
	v_mfma_f32_16x16x128_f8f6f4 v[198:201], v[130:137], v[82:89], v[30:33]
	v_mfma_f32_16x16x128_f8f6f4 v[202:205], v[150:157], v[82:89], v[26:29]
	s_waitcnt lgkmcnt(0)
	v_mfma_f32_16x16x128_f8f6f4 v[222:225], v[130:137], v[90:97], v[14:17]
	v_mfma_f32_16x16x128_f8f6f4 v[226:229], v[150:157], v[90:97], v[10:13]
	v_mfma_f32_16x16x128_f8f6f4 v[54:57], v[158:165], v[66:73], v[54:57]
	v_mfma_f32_16x16x128_f8f6f4 v[50:53], v[166:173], v[66:73], v[50:53]
	v_mfma_f32_16x16x128_f8f6f4 v[230:233], v[158:165], v[74:81], v[38:41]
	v_mfma_f32_16x16x128_f8f6f4 v[234:237], v[166:173], v[74:81], v[34:37]
	v_mfma_f32_16x16x128_f8f6f4 v[238:241], v[158:165], v[82:89], v[22:25]
	v_mfma_f32_16x16x128_f8f6f4 v[242:245], v[166:173], v[82:89], v[18:21]
	v_mfma_f32_16x16x128_f8f6f4 v[246:249], v[158:165], v[90:97], v[6:9]
	v_mfma_f32_16x16x128_f8f6f4 v[250:253], v[166:173], v[90:97], v[2:5]
	s_barrier
	s_nop 4
	ds_read_b128 v[2:5], v147
	ds_read_b128 v[6:9], v147 offset:1024
	ds_read_b128 v[18:21], v147 offset:2048
	ds_read_b128 v[22:25], v147 offset:3072
	ds_read_b128 v[130:133], v148
	ds_read_b128 v[134:137], v148 offset:1024
	ds_read_b128 v[150:153], v148 offset:2048
	ds_read_b128 v[154:157], v148 offset:3072
	s_add_i32 s73, s73, 0x40000
	s_mov_b32 m0, s38
	ds_read_b128 v[10:13], v146 offset:32768
	ds_read_b128 v[14:17], v146 offset:33792
	ds_read_b128 v[26:29], v146 offset:34816
	ds_read_b128 v[30:33], v146 offset:35840
	ds_read_b128 v[34:37], v146 offset:36864
	ds_read_b128 v[38:41], v146 offset:37888
	ds_read_b128 v[42:45], v146 offset:38912
	ds_read_b128 v[46:49], v146 offset:39936
	buffer_load_dwordx4 v139, s[8:11], s73 offen lds
	s_mov_b32 m0, s39
	s_nop 0
	buffer_load_dwordx4 v140, s[8:11], s73 offen lds
	s_waitcnt vmcnt(8)
	s_waitcnt lgkmcnt(0)
	s_barrier
	s_waitcnt lgkmcnt(6)
	v_mfma_f32_16x16x128_f8f6f4 v[126:129], v[2:9], v[10:17], v[126:129]
	v_mfma_f32_16x16x128_f8f6f4 v[122:125], v[18:25], v[10:17], v[122:125]
	s_waitcnt lgkmcnt(4)
	v_mfma_f32_16x16x128_f8f6f4 v[110:113], v[2:9], v[26:33], v[110:113]
	v_mfma_f32_16x16x128_f8f6f4 v[106:109], v[18:25], v[26:33], v[106:109]
	s_waitcnt lgkmcnt(2)
	v_mfma_f32_16x16x128_f8f6f4 v[94:97], v[2:9], v[34:41], v[206:209]
	v_mfma_f32_16x16x128_f8f6f4 v[90:93], v[18:25], v[34:41], v[210:213]
	s_waitcnt lgkmcnt(0)
	v_mfma_f32_16x16x128_f8f6f4 v[78:81], v[2:9], v[42:49], v[214:217]
	v_mfma_f32_16x16x128_f8f6f4 v[74:77], v[18:25], v[42:49], v[218:221]
	v_mfma_f32_16x16x128_f8f6f4 v[118:121], v[130:137], v[10:17], v[118:121]
	v_mfma_f32_16x16x128_f8f6f4 v[114:117], v[150:157], v[10:17], v[114:117]
	v_mfma_f32_16x16x128_f8f6f4 v[102:105], v[130:137], v[26:33], v[102:105]
	v_mfma_f32_16x16x128_f8f6f4 v[98:101], v[150:157], v[26:33], v[98:101]
	v_mfma_f32_16x16x128_f8f6f4 v[86:89], v[130:137], v[34:41], v[174:177]
	v_mfma_f32_16x16x128_f8f6f4 v[82:85], v[150:157], v[34:41], v[178:181]
	v_mfma_f32_16x16x128_f8f6f4 v[70:73], v[130:137], v[42:49], v[182:185]
	v_mfma_f32_16x16x128_f8f6f4 v[66:69], v[150:157], v[42:49], v[186:189]
	s_barrier
	s_mov_b32 m0, s47
	s_or_b32 s73, s72, 0x80
	ds_read_b128 v[34:37], v146 offset:49152
	ds_read_b128 v[38:41], v146 offset:50176
	ds_read_b128 v[158:161], v146 offset:51200
	ds_read_b128 v[162:165], v146 offset:52224
	ds_read_b128 v[166:169], v146 offset:53248
	ds_read_b128 v[170:173], v146 offset:54272
	ds_read_b128 v[174:177], v146 offset:55296
	ds_read_b128 v[178:181], v146 offset:56320
	buffer_load_dwordx4 v1, s[4:7], s73 offen lds
	s_mov_b32 m0, s48
	s_add_i32 s72, s72, 0x40080
	buffer_load_dwordx4 v138, s[4:7], s73 offen lds
	s_mov_b32 m0, s51
	s_nop 0
	buffer_load_dwordx4 v1, s[4:7], s72 offen lds
	s_mov_b32 m0, s52
	s_nop 0
	buffer_load_dwordx4 v138, s[4:7], s72 offen lds
	s_mov_b32 m0, s49
	s_nop 0
	buffer_load_dwordx4 v139, s[8:11], s71 offen lds
	s_mov_b32 m0, s50
	s_nop 0
	buffer_load_dwordx4 v140, s[8:11], s71 offen lds
	s_waitcnt vmcnt(8)
	s_waitcnt lgkmcnt(0)
	s_barrier
	s_waitcnt lgkmcnt(6)
	v_mfma_f32_16x16x128_f8f6f4 v[62:65], v[2:9], v[34:41], v[62:65]
	v_mfma_f32_16x16x128_f8f6f4 v[58:61], v[18:25], v[34:41], v[58:61]
	s_waitcnt lgkmcnt(4)
	v_mfma_f32_16x16x128_f8f6f4 v[46:49], v[2:9], v[158:165], v[190:193]
	v_mfma_f32_16x16x128_f8f6f4 v[42:45], v[18:25], v[158:165], v[194:197]
	s_waitcnt lgkmcnt(2)
	v_mfma_f32_16x16x128_f8f6f4 v[30:33], v[2:9], v[166:173], v[198:201]
	v_mfma_f32_16x16x128_f8f6f4 v[26:29], v[18:25], v[166:173], v[202:205]
	s_waitcnt lgkmcnt(0)
	v_mfma_f32_16x16x128_f8f6f4 v[14:17], v[2:9], v[174:181], v[222:225]
	v_mfma_f32_16x16x128_f8f6f4 v[10:13], v[18:25], v[174:181], v[226:229]
	v_mfma_f32_16x16x128_f8f6f4 v[54:57], v[130:137], v[34:41], v[54:57]
	v_mfma_f32_16x16x128_f8f6f4 v[50:53], v[150:157], v[34:41], v[50:53]
	v_mfma_f32_16x16x128_f8f6f4 v[38:41], v[130:137], v[158:165], v[230:233]
	v_mfma_f32_16x16x128_f8f6f4 v[34:37], v[150:157], v[158:165], v[234:237]
	v_mfma_f32_16x16x128_f8f6f4 v[22:25], v[130:137], v[166:173], v[238:241]
	v_mfma_f32_16x16x128_f8f6f4 v[18:21], v[150:157], v[166:173], v[242:245]
	v_mfma_f32_16x16x128_f8f6f4 v[6:9], v[130:137], v[174:181], v[246:249]
	v_mfma_f32_16x16x128_f8f6f4 v[2:5], v[150:157], v[174:181], v[250:253]
	s_barrier
	s_bitcmp0_b32 s70, 1
	s_cselect_b64 s[6:7], -1, 0
	s_or_b64 s[6:7], s[26:27], s[6:7]
	s_and_b64 vcc, exec, s[6:7]
	s_cbranch_vccnz .LBB0_1525
	s_lshr_b32 s6, s69, 2
	v_mov_b32_e32 v130, v143
	v_mov_b32_e32 v131, v142
	s_mulk_i32 s6, 0x42
	s_add_i32 s6, s6, s63
	v_lshlrev_b32_e32 v131, 4, v131
	s_lshl_b32 s6, s6, 3
	v_add3_u32 v130, v130, s57, v131
	s_add_i32 s6, s6, s64
	s_ashr_i32 s7, s6, 31
	v_ashrrev_i32_e32 v131, 31, v130
	v_add_u32_e32 v136, 64, v130
	s_lshl_b64 s[26:27], s[6:7], 16
	v_lshl_add_u64 v[132:133], v[130:131], 3, s[14:15]
	v_ashrrev_i32_e32 v137, 31, v136
	v_lshl_add_u64 v[134:135], v[132:133], 0, s[26:27]
	s_addk_i32 s6, 0xfdf0
	v_lshl_add_u64 v[136:137], v[136:137], 3, s[14:15]
	global_load_dwordx2 v[134:135], v[134:135], off
	s_ashr_i32 s7, s6, 31
	v_lshl_add_u64 v[150:151], v[136:137], 0, s[26:27]
	s_lshl_b64 s[6:7], s[6:7], 16
	global_load_dwordx2 v[150:151], v[150:151], off
	v_lshl_add_u64 v[132:133], v[132:133], 0, s[6:7]
	v_lshl_add_u64 v[136:137], v[136:137], 0, s[6:7]
	global_load_dwordx2 v[136:137], v[136:137], off
	v_add_u32_e32 v152, 0x80, v130
	global_load_dwordx2 v[132:133], v[132:133], off
	v_ashrrev_i32_e32 v153, 31, v152
	v_lshl_add_u64 v[152:153], v[152:153], 3, s[14:15]
	v_lshl_add_u64 v[154:155], v[152:153], 0, s[26:27]
	global_load_dwordx2 v[154:155], v[154:155], off
	v_add_u32_e32 v156, 0xc0, v130
	v_ashrrev_i32_e32 v157, 31, v156
	v_lshl_add_u64 v[156:157], v[156:157], 3, s[14:15]
	v_lshl_add_u64 v[158:159], v[156:157], 0, s[26:27]
	v_lshl_add_u64 v[152:153], v[152:153], 0, s[6:7]
	v_lshl_add_u64 v[156:157], v[156:157], 0, s[6:7]
	global_load_dwordx2 v[152:153], v[152:153], off
	s_nop 0
	global_load_dwordx2 v[158:159], v[158:159], off
	s_nop 0
	global_load_dwordx2 v[156:157], v[156:157], off
	s_waitcnt vmcnt(7)
	v_cvt_f32_ubyte0_e32 v131, v134
	v_cvt_f32_ubyte1_e32 v149, v134
	v_cvt_f32_ubyte0_e32 v160, v135
	v_cvt_f32_ubyte1_e32 v161, v135
	v_cvt_f32_ubyte2_e32 v162, v134
	v_cvt_f32_ubyte3_e32 v163, v134
	v_cvt_f32_ubyte2_e32 v168, v135
	v_cvt_f32_ubyte3_e32 v169, v135
	v_rcp_iflag_f32_e32 v134, v131
	v_rcp_iflag_f32_e32 v135, v149
	s_waitcnt vmcnt(6)
	v_cvt_f32_ubyte0_e32 v131, v150
	v_cvt_f32_ubyte1_e32 v149, v150
	v_cvt_f32_ubyte2_e32 v180, v150
	v_cvt_f32_ubyte3_e32 v150, v150
	v_rcp_iflag_f32_e32 v180, v180
	v_rcp_iflag_f32_e32 v181, v150
	s_waitcnt vmcnt(4)
	v_cvt_f32_ubyte3_e32 v165, v132
	v_cvt_f32_ubyte2_e32 v164, v132
	v_cvt_f32_ubyte1_e32 v167, v132
	v_cvt_f32_ubyte0_e32 v166, v132
	v_cvt_f32_ubyte3_e32 v171, v133
	v_cvt_f32_ubyte2_e32 v170, v133
	v_cvt_f32_ubyte1_e32 v173, v133
	v_cvt_f32_ubyte0_e32 v172, v133
	v_cvt_f32_ubyte3_e32 v133, v136
	v_cvt_f32_ubyte2_e32 v132, v136
	v_cvt_f32_ubyte1_e32 v175, v136
	v_cvt_f32_ubyte0_e32 v174, v136
	v_cvt_f32_ubyte2_e32 v136, v151
	v_rcp_iflag_f32_e32 v176, v131
	v_cvt_f32_ubyte3_e32 v131, v151
	v_cvt_f32_ubyte0_e32 v178, v151
	v_cvt_f32_ubyte1_e32 v179, v151
	v_rcp_iflag_f32_e32 v150, v136
	v_rcp_iflag_f32_e32 v151, v131
	v_pk_mul_f32 v[132:133], v[180:181], v[132:133]
	v_rcp_iflag_f32_e32 v177, v149
	v_pk_mul_f32 v[120:121], v[120:121], v[132:133]
	v_cvt_f32_ubyte3_e32 v133, v137
	v_cvt_f32_ubyte2_e32 v132, v137
	v_pk_mul_f32 v[132:133], v[150:151], v[132:133]
	v_pk_mul_f32 v[134:135], v[134:135], v[166:167]
	v_pk_mul_f32 v[116:117], v[116:117], v[132:133]
	v_add_u32_e32 v132, 0x100, v130
	v_ashrrev_i32_e32 v133, 31, v132
	v_pk_mul_f32 v[126:127], v[126:127], v[134:135]
	v_pk_mul_f32 v[134:135], v[176:177], v[174:175]
	v_lshl_add_u64 v[132:133], v[132:133], 3, s[14:15]
	v_pk_mul_f32 v[118:119], v[118:119], v[134:135]
	v_cvt_f32_ubyte1_e32 v135, v137
	v_cvt_f32_ubyte0_e32 v134, v137
	v_lshl_add_u64 v[136:137], v[132:133], 0, s[26:27]
	global_load_dwordx2 v[136:137], v[136:137], off
	v_lshl_add_u64 v[132:133], v[132:133], 0, s[6:7]
	global_load_dwordx2 v[132:133], v[132:133], off
	v_rcp_iflag_f32_e32 v178, v178
	v_rcp_iflag_f32_e32 v179, v179
	v_rcp_iflag_f32_e32 v160, v160
	v_rcp_iflag_f32_e32 v161, v161
	s_waitcnt vmcnt(5)
	v_cvt_f32_ubyte0_e32 v131, v154
	v_pk_mul_f32 v[134:135], v[178:179], v[134:135]
	v_rcp_iflag_f32_e32 v162, v162
	v_pk_mul_f32 v[114:115], v[114:115], v[134:135]
	v_rcp_iflag_f32_e32 v134, v131
	v_cvt_f32_ubyte1_e32 v131, v154
	v_rcp_iflag_f32_e32 v135, v131
	v_cvt_f32_ubyte0_e32 v131, v155
	v_rcp_iflag_f32_e32 v163, v163
	v_rcp_iflag_f32_e32 v168, v168
	v_rcp_iflag_f32_e32 v169, v169
	v_rcp_iflag_f32_e32 v150, v131
	v_cvt_f32_ubyte1_e32 v131, v155
	v_pk_mul_f32 v[160:161], v[160:161], v[172:173]
	v_rcp_iflag_f32_e32 v151, v131
	v_cvt_f32_ubyte2_e32 v131, v154
	v_pk_mul_f32 v[122:123], v[122:123], v[160:161]
	v_rcp_iflag_f32_e32 v160, v131
	v_cvt_f32_ubyte3_e32 v131, v154
	v_rcp_iflag_f32_e32 v161, v131
	v_pk_mul_f32 v[162:163], v[162:163], v[164:165]
	v_pk_mul_f32 v[164:165], v[168:169], v[170:171]
	v_pk_mul_f32 v[128:129], v[128:129], v[162:163]
	v_pk_mul_f32 v[124:125], v[124:125], v[164:165]
	s_waitcnt vmcnt(4)
	v_cvt_f32_ubyte1_e32 v165, v152
	v_cvt_f32_ubyte0_e32 v164, v152
	v_cvt_f32_ubyte3_e32 v163, v152
	v_cvt_f32_ubyte2_e32 v162, v152
	v_pk_mul_f32 v[134:135], v[134:135], v[164:165]
	v_cvt_f32_ubyte2_e32 v131, v155
	v_pk_mul_f32 v[160:161], v[160:161], v[162:163]
	v_pk_mul_f32 v[110:111], v[110:111], v[134:135]
	v_rcp_iflag_f32_e32 v134, v131
	v_cvt_f32_ubyte3_e32 v131, v155
	v_pk_mul_f32 v[112:113], v[112:113], v[160:161]
	v_rcp_iflag_f32_e32 v135, v131
	v_cvt_f32_ubyte1_e32 v161, v153
	v_cvt_f32_ubyte0_e32 v160, v153
	v_pk_mul_f32 v[150:151], v[150:151], v[160:161]
	s_waitcnt vmcnt(3)
	v_cvt_f32_ubyte0_e32 v131, v158
	v_pk_mul_f32 v[106:107], v[106:107], v[150:151]
	v_rcp_iflag_f32_e32 v150, v131
	v_cvt_f32_ubyte1_e32 v131, v158
	v_cvt_f32_ubyte3_e32 v155, v153
	v_cvt_f32_ubyte2_e32 v154, v153
	v_rcp_iflag_f32_e32 v151, v131
	v_cvt_f32_ubyte0_e32 v131, v159
	v_pk_mul_f32 v[134:135], v[134:135], v[154:155]
	v_rcp_iflag_f32_e32 v154, v131
	v_cvt_f32_ubyte1_e32 v131, v159
	v_rcp_iflag_f32_e32 v155, v131
	v_cvt_f32_ubyte2_e32 v131, v158
	v_rcp_iflag_f32_e32 v160, v131
	v_cvt_f32_ubyte3_e32 v131, v158
	s_waitcnt vmcnt(2)
	v_cvt_f32_ubyte1_e32 v165, v156
	v_cvt_f32_ubyte0_e32 v164, v156
	v_pk_mul_f32 v[108:109], v[108:109], v[134:135]
	v_add_u32_e32 v134, 0x140, v130
	v_rcp_iflag_f32_e32 v161, v131
	v_pk_mul_f32 v[150:151], v[150:151], v[164:165]
	v_cvt_f32_ubyte2_e32 v131, v159
	v_ashrrev_i32_e32 v135, 31, v134
	v_pk_mul_f32 v[102:103], v[102:103], v[150:151]
	v_rcp_iflag_f32_e32 v150, v131
	v_cvt_f32_ubyte3_e32 v131, v159
	v_lshl_add_u64 v[134:135], v[134:135], 3, s[14:15]
	v_rcp_iflag_f32_e32 v151, v131
	v_lshl_add_u64 v[152:153], v[134:135], 0, s[26:27]
	global_load_dwordx2 v[152:153], v[152:153], off
	v_cvt_f32_ubyte3_e32 v159, v157
	v_cvt_f32_ubyte2_e32 v158, v157
	v_pk_mul_f32 v[150:151], v[150:151], v[158:159]
	v_cvt_f32_ubyte3_e32 v163, v156
	v_pk_mul_f32 v[100:101], v[100:101], v[150:151]
	v_add_u32_e32 v150, 0x180, v130
	v_cvt_f32_ubyte2_e32 v162, v156
	v_ashrrev_i32_e32 v151, 31, v150
	v_pk_mul_f32 v[160:161], v[160:161], v[162:163]
	v_lshl_add_u64 v[150:151], v[150:151], 3, s[14:15]
	v_lshl_add_u64 v[134:135], v[134:135], 0, s[6:7]
	v_pk_mul_f32 v[104:105], v[104:105], v[160:161]
	v_cvt_f32_ubyte1_e32 v161, v157
	v_cvt_f32_ubyte0_e32 v160, v157
	v_lshl_add_u64 v[156:157], v[150:151], 0, s[26:27]
	v_lshl_add_u64 v[150:151], v[150:151], 0, s[6:7]
	v_pk_mul_f32 v[154:155], v[154:155], v[160:161]
	global_load_dwordx2 v[150:151], v[150:151], off
	v_pk_mul_f32 v[98:99], v[98:99], v[154:155]
	global_load_dwordx2 v[134:135], v[134:135], off
	s_waitcnt vmcnt(4)
	v_cvt_f32_ubyte0_e32 v131, v136
	v_rcp_iflag_f32_e32 v154, v131
	v_cvt_f32_ubyte1_e32 v131, v136
	v_rcp_iflag_f32_e32 v155, v131
	v_cvt_f32_ubyte0_e32 v131, v137
	v_rcp_iflag_f32_e32 v158, v131
	v_cvt_f32_ubyte1_e32 v131, v137
	v_rcp_iflag_f32_e32 v159, v131
	v_cvt_f32_ubyte2_e32 v131, v136
	global_load_dwordx2 v[156:157], v[156:157], off
	v_rcp_iflag_f32_e32 v160, v131
	v_cvt_f32_ubyte3_e32 v131, v136
	v_rcp_iflag_f32_e32 v161, v131
	v_cvt_f32_ubyte2_e32 v131, v137
	v_rcp_iflag_f32_e32 v136, v131
	v_cvt_f32_ubyte3_e32 v131, v137
	v_rcp_iflag_f32_e32 v137, v131
	s_waitcnt vmcnt(4)
	v_cvt_f32_ubyte1_e32 v165, v132
	v_cvt_f32_ubyte0_e32 v164, v132
	v_pk_mul_f32 v[154:155], v[154:155], v[164:165]
	v_cvt_f32_ubyte3_e32 v163, v132
	v_pk_mul_f32 v[94:95], v[94:95], v[154:155]
	v_cvt_f32_ubyte3_e32 v155, v133
	v_cvt_f32_ubyte2_e32 v154, v133
	v_pk_mul_f32 v[136:137], v[136:137], v[154:155]
	v_cvt_f32_ubyte2_e32 v162, v132
	v_pk_mul_f32 v[92:93], v[92:93], v[136:137]
	v_add_u32_e32 v136, 0x1c0, v130
	v_ashrrev_i32_e32 v137, 31, v136
	v_lshl_add_u64 v[136:137], v[136:137], 3, s[14:15]
	v_lshl_add_u64 v[154:155], v[136:137], 0, s[26:27]
	global_load_dwordx2 v[154:155], v[154:155], off
	v_lshl_add_u64 v[136:137], v[136:137], 0, s[6:7]
	global_load_dwordx2 v[136:137], v[136:137], off
	v_pk_mul_f32 v[160:161], v[160:161], v[162:163]
	s_waitcnt vmcnt(5)
	v_cvt_f32_ubyte0_e32 v131, v152
	v_pk_mul_f32 v[96:97], v[96:97], v[160:161]
	v_cvt_f32_ubyte1_e32 v161, v133
	v_cvt_f32_ubyte0_e32 v160, v133
	v_pk_mul_f32 v[132:133], v[158:159], v[160:161]
	s_waitcnt vmcnt(3)
	v_cvt_f32_ubyte3_e32 v163, v134
	v_pk_mul_f32 v[90:91], v[90:91], v[132:133]
	v_rcp_iflag_f32_e32 v132, v131
	v_cvt_f32_ubyte1_e32 v131, v152
	v_rcp_iflag_f32_e32 v133, v131
	v_cvt_f32_ubyte0_e32 v131, v153
	v_rcp_iflag_f32_e32 v158, v131
	v_cvt_f32_ubyte1_e32 v131, v153
	v_rcp_iflag_f32_e32 v159, v131
	v_cvt_f32_ubyte2_e32 v131, v152
	v_rcp_iflag_f32_e32 v160, v131
	v_cvt_f32_ubyte3_e32 v131, v152
	v_rcp_iflag_f32_e32 v161, v131
	v_cvt_f32_ubyte2_e32 v162, v134
	v_cvt_f32_ubyte1_e32 v165, v134
	v_cvt_f32_ubyte0_e32 v164, v134
	v_pk_mul_f32 v[132:133], v[132:133], v[164:165]
	v_pk_mul_f32 v[160:161], v[160:161], v[162:163]
	v_cvt_f32_ubyte2_e32 v131, v153
	v_pk_mul_f32 v[88:89], v[88:89], v[160:161]
	v_pk_mul_f32 v[86:87], v[86:87], v[132:133]
	v_rcp_iflag_f32_e32 v132, v131
	v_cvt_f32_ubyte3_e32 v131, v153
	v_cvt_f32_ubyte1_e32 v161, v135
	v_cvt_f32_ubyte0_e32 v160, v135
	v_rcp_iflag_f32_e32 v133, v131
	v_cvt_f32_ubyte3_e32 v153, v135
	v_cvt_f32_ubyte2_e32 v152, v135
	v_pk_mul_f32 v[134:135], v[158:159], v[160:161]
	s_waitcnt vmcnt(2)
	v_cvt_f32_ubyte0_e32 v131, v156
	v_pk_mul_f32 v[82:83], v[82:83], v[134:135]
	v_rcp_iflag_f32_e32 v134, v131
	v_cvt_f32_ubyte1_e32 v131, v156
	v_rcp_iflag_f32_e32 v135, v131
	v_cvt_f32_ubyte0_e32 v131, v157
	v_rcp_iflag_f32_e32 v158, v131
	v_cvt_f32_ubyte1_e32 v131, v157
	v_pk_mul_f32 v[132:133], v[132:133], v[152:153]
	v_rcp_iflag_f32_e32 v159, v131
	v_cvt_f32_ubyte2_e32 v131, v156
	v_pk_mul_f32 v[84:85], v[84:85], v[132:133]
	v_add_u32_e32 v132, 0x200, v130
	v_rcp_iflag_f32_e32 v160, v131
	v_cvt_f32_ubyte3_e32 v131, v156
	v_ashrrev_i32_e32 v133, 31, v132
	v_rcp_iflag_f32_e32 v161, v131
	v_lshl_add_u64 v[132:133], v[132:133], 3, s[14:15]
	v_lshl_add_u64 v[152:153], v[132:133], 0, s[26:27]
	global_load_dwordx2 v[152:153], v[152:153], off
	v_cvt_f32_ubyte3_e32 v163, v150
	v_cvt_f32_ubyte2_e32 v162, v150
	v_cvt_f32_ubyte1_e32 v165, v150
	v_cvt_f32_ubyte0_e32 v164, v150
	v_pk_mul_f32 v[134:135], v[134:135], v[164:165]
	v_pk_mul_f32 v[160:161], v[160:161], v[162:163]
	v_cvt_f32_ubyte2_e32 v131, v157
	v_pk_mul_f32 v[80:81], v[80:81], v[160:161]
	v_pk_mul_f32 v[78:79], v[78:79], v[134:135]
	v_rcp_iflag_f32_e32 v134, v131
	v_cvt_f32_ubyte3_e32 v131, v157
	v_cvt_f32_ubyte1_e32 v161, v151
	v_cvt_f32_ubyte0_e32 v160, v151
	v_rcp_iflag_f32_e32 v135, v131
	v_cvt_f32_ubyte3_e32 v157, v151
	v_cvt_f32_ubyte2_e32 v156, v151
	v_pk_mul_f32 v[150:151], v[158:159], v[160:161]
	s_waitcnt vmcnt(2)
	v_cvt_f32_ubyte0_e32 v131, v154
	v_pk_mul_f32 v[74:75], v[74:75], v[150:151]
	v_rcp_iflag_f32_e32 v150, v131
	v_cvt_f32_ubyte1_e32 v131, v154
	v_rcp_iflag_f32_e32 v151, v131
	v_cvt_f32_ubyte0_e32 v131, v155
	v_rcp_iflag_f32_e32 v158, v131
	v_cvt_f32_ubyte1_e32 v131, v155
	v_pk_mul_f32 v[134:135], v[134:135], v[156:157]
	v_rcp_iflag_f32_e32 v159, v131
	v_cvt_f32_ubyte2_e32 v131, v154
	v_lshl_add_u64 v[132:133], v[132:133], 0, s[6:7]
	v_pk_mul_f32 v[76:77], v[76:77], v[134:135]
	v_add_u32_e32 v134, 0x240, v130
	v_rcp_iflag_f32_e32 v160, v131
	v_cvt_f32_ubyte3_e32 v131, v154
	global_load_dwordx2 v[132:133], v[132:133], off
	v_ashrrev_i32_e32 v135, 31, v134
	v_rcp_iflag_f32_e32 v161, v131
	v_lshl_add_u64 v[134:135], v[134:135], 3, s[14:15]
	v_lshl_add_u64 v[156:157], v[134:135], 0, s[26:27]
	v_lshl_add_u64 v[134:135], v[134:135], 0, s[6:7]
	global_load_dwordx2 v[162:163], v[134:135], off
	s_waitcnt vmcnt(3)
	v_cvt_f32_ubyte3_e32 v135, v136
	v_cvt_f32_ubyte2_e32 v134, v136
	v_pk_mul_f32 v[134:135], v[160:161], v[134:135]
	v_cvt_f32_ubyte2_e32 v131, v155
	global_load_dwordx2 v[156:157], v[156:157], off
	v_pk_mul_f32 v[72:73], v[72:73], v[134:135]
	v_rcp_iflag_f32_e32 v134, v131
	v_cvt_f32_ubyte3_e32 v131, v155
	v_rcp_iflag_f32_e32 v135, v131
	v_cvt_f32_ubyte1_e32 v165, v136
	v_cvt_f32_ubyte0_e32 v164, v136
	v_pk_mul_f32 v[150:151], v[150:151], v[164:165]
	v_cvt_f32_ubyte1_e32 v155, v137
	v_pk_mul_f32 v[70:71], v[70:71], v[150:151]
	v_cvt_f32_ubyte3_e32 v151, v137
	v_cvt_f32_ubyte2_e32 v150, v137
	v_pk_mul_f32 v[134:135], v[134:135], v[150:151]
	v_cvt_f32_ubyte0_e32 v154, v137
	v_pk_mul_f32 v[68:69], v[68:69], v[134:135]
	v_add_u32_e32 v134, 0x280, v130
	v_ashrrev_i32_e32 v135, 31, v134
	v_lshl_add_u64 v[134:135], v[134:135], 3, s[14:15]
	v_lshl_add_u64 v[150:151], v[134:135], 0, s[26:27]
	global_load_dwordx2 v[150:151], v[150:151], off
	v_lshl_add_u64 v[134:135], v[134:135], 0, s[6:7]
	global_load_dwordx2 v[160:161], v[134:135], off
	v_pk_mul_f32 v[136:137], v[158:159], v[154:155]
	s_waitcnt vmcnt(5)
	v_cvt_f32_ubyte0_e32 v131, v152
	v_pk_mul_f32 v[66:67], v[66:67], v[136:137]
	v_rcp_iflag_f32_e32 v136, v131
	v_cvt_f32_ubyte1_e32 v131, v152
	v_rcp_iflag_f32_e32 v137, v131
	v_cvt_f32_ubyte0_e32 v131, v153
	v_rcp_iflag_f32_e32 v154, v131
	v_cvt_f32_ubyte1_e32 v131, v153
	v_rcp_iflag_f32_e32 v155, v131
	v_cvt_f32_ubyte2_e32 v131, v152
	v_rcp_iflag_f32_e32 v158, v131
	v_cvt_f32_ubyte3_e32 v131, v152
	v_rcp_iflag_f32_e32 v159, v131
	v_cvt_f32_ubyte2_e32 v131, v153
	v_add_u32_e32 v152, 0x2c0, v130
	s_waitcnt vmcnt(4)
	v_cvt_f32_ubyte3_e32 v135, v132
	v_cvt_f32_ubyte2_e32 v134, v132
	v_pk_mul_f32 v[134:135], v[158:159], v[134:135]
	v_cvt_f32_ubyte1_e32 v165, v132
	v_pk_mul_f32 v[64:65], v[64:65], v[134:135]
	v_rcp_iflag_f32_e32 v134, v131
	v_cvt_f32_ubyte3_e32 v131, v153
	v_ashrrev_i32_e32 v153, 31, v152
	v_cvt_f32_ubyte0_e32 v164, v132
	v_lshl_add_u64 v[152:153], v[152:153], 3, s[14:15]
	v_pk_mul_f32 v[136:137], v[136:137], v[164:165]
	v_rcp_iflag_f32_e32 v135, v131
	v_lshl_add_u64 v[158:159], v[152:153], 0, s[26:27]
	v_cvt_f32_ubyte1_e32 v165, v133
	v_cvt_f32_ubyte0_e32 v164, v133
	v_pk_mul_f32 v[62:63], v[62:63], v[136:137]
	v_cvt_f32_ubyte3_e32 v137, v133
	v_cvt_f32_ubyte2_e32 v136, v133
	global_load_dwordx2 v[158:159], v[158:159], off
	v_pk_mul_f32 v[132:133], v[154:155], v[164:165]
	s_waitcnt vmcnt(3)
	v_cvt_f32_ubyte0_e32 v131, v156
	v_pk_mul_f32 v[58:59], v[58:59], v[132:133]
	v_rcp_iflag_f32_e32 v132, v131
	v_cvt_f32_ubyte1_e32 v131, v156
	v_rcp_iflag_f32_e32 v133, v131
	v_cvt_f32_ubyte0_e32 v131, v157
	v_pk_mul_f32 v[134:135], v[134:135], v[136:137]
	v_rcp_iflag_f32_e32 v136, v131
	v_cvt_f32_ubyte1_e32 v131, v157
	v_rcp_iflag_f32_e32 v137, v131
	v_cvt_f32_ubyte2_e32 v131, v156
	v_rcp_iflag_f32_e32 v154, v131
	v_cvt_f32_ubyte3_e32 v131, v156
	v_rcp_iflag_f32_e32 v155, v131
	v_cvt_f32_ubyte1_e32 v165, v162
	v_cvt_f32_ubyte0_e32 v164, v162
	v_pk_mul_f32 v[132:133], v[132:133], v[164:165]
	v_cvt_f32_ubyte2_e32 v131, v157
	v_pk_mul_f32 v[60:61], v[60:61], v[134:135]
	v_lshl_add_u64 v[134:135], v[152:153], 0, s[6:7]
	v_cvt_f32_ubyte3_e32 v153, v162
	v_cvt_f32_ubyte2_e32 v152, v162
	v_pk_mul_f32 v[54:55], v[54:55], v[132:133]
	v_rcp_iflag_f32_e32 v132, v131
	v_cvt_f32_ubyte3_e32 v131, v157
	v_pk_mul_f32 v[152:153], v[154:155], v[152:153]
	v_rcp_iflag_f32_e32 v133, v131
	v_cvt_f32_ubyte1_e32 v155, v163
	v_cvt_f32_ubyte0_e32 v154, v163
	s_waitcnt vmcnt(2)
	v_cvt_f32_ubyte0_e32 v131, v150
	v_pk_mul_f32 v[136:137], v[136:137], v[154:155]
	v_rcp_iflag_f32_e32 v154, v131
	v_cvt_f32_ubyte1_e32 v131, v150
	v_rcp_iflag_f32_e32 v155, v131
	v_cvt_f32_ubyte0_e32 v131, v151
	v_rcp_iflag_f32_e32 v156, v131
	v_cvt_f32_ubyte1_e32 v131, v151
	v_pk_mul_f32 v[56:57], v[56:57], v[152:153]
	v_cvt_f32_ubyte3_e32 v153, v163
	v_cvt_f32_ubyte2_e32 v152, v163
	v_rcp_iflag_f32_e32 v157, v131
	v_cvt_f32_ubyte2_e32 v131, v150
	v_pk_mul_f32 v[132:133], v[132:133], v[152:153]
	v_rcp_iflag_f32_e32 v162, v131
	v_cvt_f32_ubyte3_e32 v131, v150
	v_pk_mul_f32 v[52:53], v[52:53], v[132:133]
	v_add_u32_e32 v132, 0x300, v130
	v_rcp_iflag_f32_e32 v163, v131
	v_cvt_f32_ubyte2_e32 v131, v151
	v_ashrrev_i32_e32 v133, 31, v132
	v_rcp_iflag_f32_e32 v150, v131
	v_cvt_f32_ubyte3_e32 v131, v151
	v_lshl_add_u64 v[152:153], v[132:133], 3, s[14:15]
	v_rcp_iflag_f32_e32 v151, v131
	v_lshl_add_u64 v[132:133], v[152:153], 0, s[26:27]
	v_pk_mul_f32 v[50:51], v[50:51], v[136:137]
	v_lshl_add_u64 v[136:137], v[152:153], 0, s[6:7]
	s_waitcnt vmcnt(1)
	v_cvt_f32_ubyte3_e32 v153, v160
	v_cvt_f32_ubyte2_e32 v152, v160
	v_pk_mul_f32 v[152:153], v[162:163], v[152:153]
	global_load_dwordx2 v[134:135], v[134:135], off
	v_pk_mul_f32 v[48:49], v[48:49], v[152:153]
	v_cvt_f32_ubyte3_e32 v153, v161
	v_cvt_f32_ubyte2_e32 v152, v161
	v_pk_mul_f32 v[150:151], v[150:151], v[152:153]
	global_load_dwordx2 v[136:137], v[136:137], off
	v_pk_mul_f32 v[44:45], v[44:45], v[150:151]
	v_add_u32_e32 v150, 0x340, v130
	v_ashrrev_i32_e32 v151, 31, v150
	v_lshl_add_u64 v[150:151], v[150:151], 3, s[14:15]
	v_lshl_add_u64 v[152:153], v[150:151], 0, s[26:27]
	global_load_dwordx2 v[152:153], v[152:153], off
	v_cvt_f32_ubyte1_e32 v165, v160
	global_load_dwordx2 v[132:133], v[132:133], off
	v_cvt_f32_ubyte0_e32 v164, v160
	v_pk_mul_f32 v[154:155], v[154:155], v[164:165]
	v_lshl_add_u64 v[150:151], v[150:151], 0, s[6:7]
	v_pk_mul_f32 v[46:47], v[46:47], v[154:155]
	v_cvt_f32_ubyte1_e32 v155, v161
	v_cvt_f32_ubyte0_e32 v154, v161
	v_pk_mul_f32 v[154:155], v[156:157], v[154:155]
	s_waitcnt vmcnt(4)
	v_cvt_f32_ubyte0_e32 v131, v158
	v_pk_mul_f32 v[42:43], v[42:43], v[154:155]
	v_rcp_iflag_f32_e32 v154, v131
	v_cvt_f32_ubyte1_e32 v131, v158
	v_rcp_iflag_f32_e32 v155, v131
	v_cvt_f32_ubyte0_e32 v131, v159
	v_rcp_iflag_f32_e32 v156, v131
	v_cvt_f32_ubyte1_e32 v131, v159
	v_rcp_iflag_f32_e32 v157, v131
	v_cvt_f32_ubyte2_e32 v131, v158
	v_rcp_iflag_f32_e32 v160, v131
	v_cvt_f32_ubyte3_e32 v131, v158
	v_rcp_iflag_f32_e32 v161, v131
	global_load_dwordx2 v[150:151], v[150:151], off
	v_cvt_f32_ubyte2_e32 v131, v159
	s_waitcnt vmcnt(4)
	v_cvt_f32_ubyte3_e32 v163, v134
	v_cvt_f32_ubyte2_e32 v162, v134
	v_cvt_f32_ubyte1_e32 v165, v134
	v_cvt_f32_ubyte0_e32 v164, v134
	v_pk_mul_f32 v[160:161], v[160:161], v[162:163]
	v_pk_mul_f32 v[154:155], v[154:155], v[164:165]
	v_pk_mul_f32 v[40:41], v[40:41], v[160:161]
	v_add_u32_e32 v160, 0x380, v130
	v_pk_mul_f32 v[38:39], v[38:39], v[154:155]
	v_rcp_iflag_f32_e32 v154, v131
	v_cvt_f32_ubyte3_e32 v131, v159
	v_ashrrev_i32_e32 v161, 31, v160
	v_rcp_iflag_f32_e32 v155, v131
	v_lshl_add_u64 v[160:161], v[160:161], 3, s[14:15]
	v_lshl_add_u64 v[162:163], v[160:161], 0, s[26:27]
	v_cvt_f32_ubyte1_e32 v165, v135
	v_cvt_f32_ubyte0_e32 v164, v135
	v_cvt_f32_ubyte3_e32 v159, v135
	v_cvt_f32_ubyte2_e32 v158, v135
	global_load_dwordx2 v[162:163], v[162:163], off
	v_pk_mul_f32 v[134:135], v[156:157], v[164:165]
	s_waitcnt vmcnt(2)
	v_cvt_f32_ubyte0_e32 v131, v132
	v_pk_mul_f32 v[34:35], v[34:35], v[134:135]
	v_rcp_iflag_f32_e32 v134, v131
	v_cvt_f32_ubyte1_e32 v131, v132
	v_pk_mul_f32 v[154:155], v[154:155], v[158:159]
	v_rcp_iflag_f32_e32 v135, v131
	v_cvt_f32_ubyte0_e32 v131, v133
	v_pk_mul_f32 v[36:37], v[36:37], v[154:155]
	v_lshl_add_u64 v[154:155], v[160:161], 0, s[6:7]
	v_rcp_iflag_f32_e32 v156, v131
	v_cvt_f32_ubyte1_e32 v131, v133
	global_load_dwordx2 v[154:155], v[154:155], off
	v_rcp_iflag_f32_e32 v157, v131
	v_cvt_f32_ubyte2_e32 v131, v132
	v_rcp_iflag_f32_e32 v158, v131
	v_cvt_f32_ubyte3_e32 v131, v132
	v_rcp_iflag_f32_e32 v159, v131
	v_add_u32_e32 v130, 0x3c0, v130
	v_cvt_f32_ubyte3_e32 v161, v136
	v_cvt_f32_ubyte2_e32 v160, v136
	v_ashrrev_i32_e32 v131, 31, v130
	v_pk_mul_f32 v[158:159], v[158:159], v[160:161]
	v_lshl_add_u64 v[130:131], v[130:131], 3, s[14:15]
	v_pk_mul_f32 v[32:33], v[32:33], v[158:159]
	v_lshl_add_u64 v[158:159], v[130:131], 0, s[26:27]
	global_load_dwordx2 v[158:159], v[158:159], off
	v_lshl_add_u64 v[130:131], v[130:131], 0, s[6:7]
	global_load_dwordx2 v[130:131], v[130:131], off
	v_cvt_f32_ubyte2_e32 v132, v133
	v_cvt_f32_ubyte3_e32 v133, v133
	v_rcp_iflag_f32_e32 v132, v132
	v_rcp_iflag_f32_e32 v133, v133
	v_cvt_f32_ubyte1_e32 v165, v136
	v_cvt_f32_ubyte0_e32 v164, v136
	v_pk_mul_f32 v[134:135], v[134:135], v[164:165]
	v_cvt_f32_ubyte1_e32 v161, v137
	v_pk_mul_f32 v[30:31], v[30:31], v[134:135]
	v_cvt_f32_ubyte3_e32 v135, v137
	v_cvt_f32_ubyte2_e32 v134, v137
	v_pk_mul_f32 v[132:133], v[132:133], v[134:135]
	v_cvt_f32_ubyte0_e32 v160, v137
	v_pk_mul_f32 v[28:29], v[28:29], v[132:133]
	v_cvt_f32_ubyte0_e32 v132, v152
	v_cvt_f32_ubyte1_e32 v133, v152
	v_rcp_iflag_f32_e32 v132, v132
	v_rcp_iflag_f32_e32 v133, v133
	v_pk_mul_f32 v[136:137], v[156:157], v[160:161]
	s_waitcnt vmcnt(4)
	v_cvt_f32_ubyte1_e32 v161, v150
	v_pk_mul_f32 v[26:27], v[26:27], v[136:137]
	v_cvt_f32_ubyte2_e32 v136, v152
	v_cvt_f32_ubyte3_e32 v137, v152
	v_cvt_f32_ubyte0_e32 v160, v150
	v_rcp_iflag_f32_e32 v136, v136
	v_rcp_iflag_f32_e32 v137, v137
	v_pk_mul_f32 v[132:133], v[132:133], v[160:161]
	v_cvt_f32_ubyte3_e32 v157, v150
	v_pk_mul_f32 v[22:23], v[22:23], v[132:133]
	v_cvt_f32_ubyte2_e32 v132, v153
	v_cvt_f32_ubyte3_e32 v133, v153
	v_rcp_iflag_f32_e32 v132, v132
	v_rcp_iflag_f32_e32 v133, v133
	v_cvt_f32_ubyte2_e32 v156, v150
	v_pk_mul_f32 v[136:137], v[136:137], v[156:157]
	v_cvt_f32_ubyte0_e32 v134, v153
	v_pk_mul_f32 v[24:25], v[24:25], v[136:137]
	v_cvt_f32_ubyte3_e32 v137, v151
	v_cvt_f32_ubyte2_e32 v136, v151
	v_cvt_f32_ubyte1_e32 v135, v153
	v_pk_mul_f32 v[132:133], v[132:133], v[136:137]
	v_rcp_iflag_f32_e32 v134, v134
	v_rcp_iflag_f32_e32 v135, v135
	v_pk_mul_f32 v[20:21], v[20:21], v[132:133]
	v_cvt_f32_ubyte1_e32 v153, v151
	v_cvt_f32_ubyte0_e32 v152, v151
	v_pk_mul_f32 v[134:135], v[134:135], v[152:153]
	s_waitcnt vmcnt(3)
	v_cvt_f32_ubyte0_e32 v132, v162
	v_cvt_f32_ubyte1_e32 v133, v162
	v_rcp_iflag_f32_e32 v132, v132
	v_rcp_iflag_f32_e32 v133, v133
	v_cvt_f32_ubyte2_e32 v136, v162
	v_cvt_f32_ubyte3_e32 v137, v162
	v_rcp_iflag_f32_e32 v136, v136
	v_rcp_iflag_f32_e32 v137, v137
	v_pk_mul_f32 v[18:19], v[18:19], v[134:135]
	v_cvt_f32_ubyte0_e32 v134, v163
	v_cvt_f32_ubyte1_e32 v135, v163
	v_rcp_iflag_f32_e32 v134, v134
	v_rcp_iflag_f32_e32 v135, v135
	s_waitcnt vmcnt(2)
	v_cvt_f32_ubyte1_e32 v153, v154
	v_cvt_f32_ubyte0_e32 v152, v154
	v_pk_mul_f32 v[132:133], v[132:133], v[152:153]
	v_cvt_f32_ubyte3_e32 v151, v154
	v_pk_mul_f32 v[14:15], v[14:15], v[132:133]
	v_cvt_f32_ubyte2_e32 v132, v163
	v_cvt_f32_ubyte3_e32 v133, v163
	v_rcp_iflag_f32_e32 v132, v132
	v_rcp_iflag_f32_e32 v133, v133
	v_cvt_f32_ubyte2_e32 v150, v154
	v_pk_mul_f32 v[136:137], v[136:137], v[150:151]
	v_cvt_f32_ubyte1_e32 v151, v155
	v_pk_mul_f32 v[16:17], v[16:17], v[136:137]
	v_cvt_f32_ubyte3_e32 v137, v155
	v_cvt_f32_ubyte2_e32 v136, v155
	v_pk_mul_f32 v[132:133], v[132:133], v[136:137]
	v_cvt_f32_ubyte0_e32 v150, v155
	v_pk_mul_f32 v[12:13], v[12:13], v[132:133]
	s_waitcnt vmcnt(1)
	v_cvt_f32_ubyte0_e32 v132, v158
	v_cvt_f32_ubyte1_e32 v133, v158
	v_rcp_iflag_f32_e32 v132, v132
	v_rcp_iflag_f32_e32 v133, v133
	v_cvt_f32_ubyte2_e32 v136, v158
	v_cvt_f32_ubyte3_e32 v137, v158
	s_waitcnt vmcnt(0)
	v_cvt_f32_ubyte1_e32 v153, v130
	v_cvt_f32_ubyte0_e32 v152, v130
	v_pk_mul_f32 v[134:135], v[134:135], v[150:151]
	v_rcp_iflag_f32_e32 v136, v136
	v_rcp_iflag_f32_e32 v137, v137
	v_cvt_f32_ubyte3_e32 v151, v130
	v_cvt_f32_ubyte2_e32 v150, v130
	v_pk_mul_f32 v[132:133], v[132:133], v[152:153]
	v_cvt_f32_ubyte2_e32 v130, v159
	v_pk_mul_f32 v[10:11], v[10:11], v[134:135]
	v_cvt_f32_ubyte0_e32 v134, v159
	v_cvt_f32_ubyte1_e32 v135, v159
	v_pk_mul_f32 v[6:7], v[6:7], v[132:133]
	v_rcp_iflag_f32_e32 v132, v130
	v_cvt_f32_ubyte3_e32 v130, v159
	v_rcp_iflag_f32_e32 v134, v134
	v_rcp_iflag_f32_e32 v135, v135
	v_rcp_iflag_f32_e32 v133, v130
	v_pk_mul_f32 v[136:137], v[136:137], v[150:151]
	v_cvt_f32_ubyte1_e32 v151, v131
	v_pk_mul_f32 v[8:9], v[8:9], v[136:137]
	v_cvt_f32_ubyte3_e32 v137, v131
	v_cvt_f32_ubyte2_e32 v136, v131
	v_cvt_f32_ubyte0_e32 v150, v131
	v_pk_mul_f32 v[130:131], v[134:135], v[150:151]
	v_pk_mul_f32 v[132:133], v[132:133], v[136:137]
	v_pk_mul_f32 v[2:3], v[2:3], v[130:131]
	v_pk_mul_f32 v[4:5], v[4:5], v[132:133]

.LBB0_1610:
	ds_read_b128 v[148:151], v143
	ds_read_b128 v[152:155], v143 offset:1024
	ds_read_b128 v[156:159], v143 offset:2048
	ds_read_b128 v[160:163], v143 offset:3072
	ds_read_b128 v[164:167], v144
	ds_read_b128 v[168:171], v144 offset:1024
	ds_read_b128 v[172:175], v144 offset:2048
	ds_read_b128 v[176:179], v144 offset:3072
	s_add_i32 s63, s60, 0xfffc0080
	s_cmp_eq_u32 s62, 12
	s_cselect_b32 s65, s25, s63
	s_cselect_b32 s64, s24, s61
	s_or_b32 s63, s65, 0x80
	s_mov_b32 m0, s51
	ds_read_b128 v[180:183], v145
	ds_read_b128 v[184:187], v145 offset:1024
	ds_read_b128 v[188:191], v145 offset:2048
	ds_read_b128 v[192:195], v145 offset:3072
	ds_read_b128 v[196:199], v145 offset:4096
	ds_read_b128 v[200:203], v145 offset:5120
	ds_read_b128 v[204:207], v145 offset:6144
	ds_read_b128 v[208:211], v145 offset:7168
	buffer_load_dwordx4 v139, s[8:11], s60 offen lds
	s_mov_b32 m0, s52
	s_nop 0
	buffer_load_dwordx4 v140, s[8:11], s60 offen lds
	s_waitcnt vmcnt(8)
	s_waitcnt lgkmcnt(0)
	s_barrier
	s_waitcnt lgkmcnt(6)
	v_mfma_f32_16x16x128_f8f6f4 v[126:129], v[148:155], v[180:187], v[126:129]
	v_mfma_f32_16x16x128_f8f6f4 v[122:125], v[156:163], v[180:187], v[122:125]
	s_waitcnt lgkmcnt(4)
	v_mfma_f32_16x16x128_f8f6f4 v[114:117], v[148:155], v[188:195], v[114:117]
	v_mfma_f32_16x16x128_f8f6f4 v[106:109], v[156:163], v[188:195], v[106:109]
	s_waitcnt lgkmcnt(2)
	v_mfma_f32_16x16x128_f8f6f4 v[98:101], v[148:155], v[196:203], v[98:101]
	v_mfma_f32_16x16x128_f8f6f4 v[134:137], v[156:163], v[196:203], v[90:93]
	s_waitcnt lgkmcnt(0)
	v_mfma_f32_16x16x128_f8f6f4 v[212:215], v[148:155], v[204:211], v[82:85]
	v_mfma_f32_16x16x128_f8f6f4 v[216:219], v[156:163], v[204:211], v[74:77]
	v_mfma_f32_16x16x128_f8f6f4 v[118:121], v[164:171], v[180:187], v[118:121]
	v_mfma_f32_16x16x128_f8f6f4 v[110:113], v[172:179], v[180:187], v[110:113]
	v_mfma_f32_16x16x128_f8f6f4 v[102:105], v[164:171], v[188:195], v[102:105]
	v_mfma_f32_16x16x128_f8f6f4 v[180:183], v[172:179], v[188:195], v[94:97]
	v_mfma_f32_16x16x128_f8f6f4 v[184:187], v[164:171], v[196:203], v[86:89]
	v_mfma_f32_16x16x128_f8f6f4 v[188:191], v[172:179], v[196:203], v[78:81]
	v_mfma_f32_16x16x128_f8f6f4 v[192:195], v[164:171], v[204:211], v[62:65]
	v_mfma_f32_16x16x128_f8f6f4 v[196:199], v[172:179], v[204:211], v[58:61]
	s_barrier
	s_mov_b32 m0, s28
	s_nop 3
	ds_read_b128 v[58:61], v145 offset:16384
	ds_read_b128 v[62:65], v145 offset:17408
	ds_read_b128 v[74:77], v145 offset:18432
	ds_read_b128 v[78:81], v145 offset:19456
	ds_read_b128 v[82:85], v145 offset:20480
	ds_read_b128 v[86:89], v145 offset:21504
	ds_read_b128 v[90:93], v145 offset:22528
	ds_read_b128 v[94:97], v145 offset:23552
	buffer_load_dwordx4 v1, s[4:7], s64 offen lds
	s_mov_b32 m0, s29
	s_add_i32 s66, s64, 0x40000
	buffer_load_dwordx4 v138, s[4:7], s64 offen lds
	s_mov_b32 m0, s30
	s_nop 0
	buffer_load_dwordx4 v1, s[4:7], s66 offen lds
	s_mov_b32 m0, s31
	s_nop 0
	buffer_load_dwordx4 v138, s[4:7], s66 offen lds
	s_mov_b32 m0, s27
	s_nop 0
	buffer_load_dwordx4 v139, s[8:11], s65 offen lds
	s_mov_b32 m0, s33
	s_nop 0
	buffer_load_dwordx4 v140, s[8:11], s65 offen lds
	s_waitcnt vmcnt(8)
	s_waitcnt lgkmcnt(0)
	s_barrier
	s_waitcnt lgkmcnt(4)
	v_mfma_f32_16x16x128_f8f6f4 v[18:21], v[156:163], v[74:81], v[18:21]
	v_mfma_f32_16x16x128_f8f6f4 v[200:203], v[148:155], v[58:65], v[46:49]
	v_mfma_f32_16x16x128_f8f6f4 v[204:207], v[156:163], v[58:65], v[42:45]
	v_mfma_f32_16x16x128_f8f6f4 v[208:211], v[148:155], v[74:81], v[30:33]
	s_waitcnt lgkmcnt(2)
	v_mfma_f32_16x16x128_f8f6f4 v[220:223], v[148:155], v[82:89], v[14:17]
	v_mfma_f32_16x16x128_f8f6f4 v[224:227], v[156:163], v[82:89], v[10:13]
	s_waitcnt lgkmcnt(0)
	v_mfma_f32_16x16x128_f8f6f4 v[228:231], v[148:155], v[90:97], v[6:9]
	v_mfma_f32_16x16x128_f8f6f4 v[232:235], v[156:163], v[90:97], v[2:5]
	v_mfma_f32_16x16x128_f8f6f4 v[66:69], v[164:171], v[58:65], v[66:69]
	v_mfma_f32_16x16x128_f8f6f4 v[70:73], v[172:179], v[58:65], v[70:73]
	v_mfma_f32_16x16x128_f8f6f4 v[54:57], v[172:179], v[74:81], v[54:57]
	v_mfma_f32_16x16x128_f8f6f4 v[236:239], v[164:171], v[74:81], v[50:53]
	v_mfma_f32_16x16x128_f8f6f4 v[240:243], v[164:171], v[82:89], v[34:37]
	v_mfma_f32_16x16x128_f8f6f4 v[244:247], v[172:179], v[82:89], v[38:41]
	v_mfma_f32_16x16x128_f8f6f4 v[248:251], v[164:171], v[90:97], v[22:25]
	v_mfma_f32_16x16x128_f8f6f4 v[252:255], v[172:179], v[90:97], v[26:29]
	s_barrier
	ds_read_b128 v[2:5], v146
	ds_read_b128 v[6:9], v146 offset:1024
	s_nop 1
	ds_read_b128 v[22:25], v146 offset:2048
	ds_read_b128 v[26:29], v146 offset:3072
	ds_read_b128 v[148:151], v147
	ds_read_b128 v[152:155], v147 offset:1024
	ds_read_b128 v[156:159], v147 offset:2048
	ds_read_b128 v[160:163], v147 offset:3072
	s_add_i32 s65, s65, 0x40000
	s_mov_b32 m0, s34
	ds_read_b128 v[10:13], v145 offset:32768
	ds_read_b128 v[14:17], v145 offset:33792
	ds_read_b128 v[30:33], v145 offset:34816
	ds_read_b128 v[34:37], v145 offset:35840
	ds_read_b128 v[38:41], v145 offset:36864
	ds_read_b128 v[42:45], v145 offset:37888
	ds_read_b128 v[46:49], v145 offset:38912
	ds_read_b128 v[50:53], v145 offset:39936
	buffer_load_dwordx4 v139, s[8:11], s65 offen lds
	s_mov_b32 m0, s35
	s_nop 0
	buffer_load_dwordx4 v140, s[8:11], s65 offen lds
	s_waitcnt vmcnt(8)
	s_waitcnt lgkmcnt(0)
	s_barrier
	s_waitcnt lgkmcnt(6)
	v_mfma_f32_16x16x128_f8f6f4 v[126:129], v[2:9], v[10:17], v[126:129]
	v_mfma_f32_16x16x128_f8f6f4 v[122:125], v[22:29], v[10:17], v[122:125]
	s_waitcnt lgkmcnt(4)
	v_mfma_f32_16x16x128_f8f6f4 v[114:117], v[2:9], v[30:37], v[114:117]
	v_mfma_f32_16x16x128_f8f6f4 v[106:109], v[22:29], v[30:37], v[106:109]
	s_waitcnt lgkmcnt(2)
	v_mfma_f32_16x16x128_f8f6f4 v[98:101], v[2:9], v[38:45], v[98:101]
	v_mfma_f32_16x16x128_f8f6f4 v[90:93], v[22:29], v[38:45], v[134:137]
	s_waitcnt lgkmcnt(0)
	v_mfma_f32_16x16x128_f8f6f4 v[82:85], v[2:9], v[46:53], v[212:215]
	v_mfma_f32_16x16x128_f8f6f4 v[74:77], v[22:29], v[46:53], v[216:219]
	v_mfma_f32_16x16x128_f8f6f4 v[118:121], v[148:155], v[10:17], v[118:121]
	v_mfma_f32_16x16x128_f8f6f4 v[110:113], v[156:163], v[10:17], v[110:113]
	v_mfma_f32_16x16x128_f8f6f4 v[102:105], v[148:155], v[30:37], v[102:105]
	v_mfma_f32_16x16x128_f8f6f4 v[94:97], v[156:163], v[30:37], v[180:183]
	v_mfma_f32_16x16x128_f8f6f4 v[86:89], v[148:155], v[38:45], v[184:187]
	v_mfma_f32_16x16x128_f8f6f4 v[78:81], v[156:163], v[38:45], v[188:191]
	v_mfma_f32_16x16x128_f8f6f4 v[62:65], v[148:155], v[46:53], v[192:195]
	v_mfma_f32_16x16x128_f8f6f4 v[58:61], v[156:163], v[46:53], v[196:199]
	s_barrier
	s_mov_b32 m0, s38
	s_or_b32 s65, s64, 0x80
	ds_read_b128 v[34:37], v145 offset:49152
	ds_read_b128 v[38:41], v145 offset:50176
	ds_read_b128 v[164:167], v145 offset:51200
	ds_read_b128 v[168:171], v145 offset:52224
	ds_read_b128 v[172:175], v145 offset:53248
	ds_read_b128 v[176:179], v145 offset:54272
	ds_read_b128 v[180:183], v145 offset:55296
	ds_read_b128 v[184:187], v145 offset:56320
	buffer_load_dwordx4 v1, s[4:7], s65 offen lds
	s_mov_b32 m0, s39
	s_add_i32 s64, s64, 0x40080
	buffer_load_dwordx4 v138, s[4:7], s65 offen lds
	s_mov_b32 m0, s48
	s_nop 0
	buffer_load_dwordx4 v1, s[4:7], s64 offen lds
	s_mov_b32 m0, s49
	s_nop 0
	buffer_load_dwordx4 v138, s[4:7], s64 offen lds
	s_mov_b32 m0, s46
	s_nop 0
	buffer_load_dwordx4 v139, s[8:11], s63 offen lds
	s_mov_b32 m0, s47
	s_nop 0
	buffer_load_dwordx4 v140, s[8:11], s63 offen lds
	s_waitcnt vmcnt(8)
	s_waitcnt lgkmcnt(0)
	s_barrier
	s_waitcnt lgkmcnt(6)
	v_mfma_f32_16x16x128_f8f6f4 v[46:49], v[2:9], v[34:41], v[200:203]
	v_mfma_f32_16x16x128_f8f6f4 v[42:45], v[22:29], v[34:41], v[204:207]
	s_waitcnt lgkmcnt(4)
	v_mfma_f32_16x16x128_f8f6f4 v[30:33], v[2:9], v[164:171], v[208:211]
	v_mfma_f32_16x16x128_f8f6f4 v[18:21], v[22:29], v[164:171], v[18:21]
	s_waitcnt lgkmcnt(2)
	v_mfma_f32_16x16x128_f8f6f4 v[14:17], v[2:9], v[172:179], v[220:223]
	v_mfma_f32_16x16x128_f8f6f4 v[10:13], v[22:29], v[172:179], v[224:227]
	s_waitcnt lgkmcnt(0)
	v_mfma_f32_16x16x128_f8f6f4 v[6:9], v[2:9], v[180:187], v[228:231]
	v_mfma_f32_16x16x128_f8f6f4 v[2:5], v[22:29], v[180:187], v[232:235]
	v_mfma_f32_16x16x128_f8f6f4 v[66:69], v[148:155], v[34:41], v[66:69]
	v_mfma_f32_16x16x128_f8f6f4 v[70:73], v[156:163], v[34:41], v[70:73]
	v_mfma_f32_16x16x128_f8f6f4 v[50:53], v[148:155], v[164:171], v[236:239]
	v_mfma_f32_16x16x128_f8f6f4 v[54:57], v[156:163], v[164:171], v[54:57]
	v_mfma_f32_16x16x128_f8f6f4 v[34:37], v[148:155], v[172:179], v[240:243]
	v_mfma_f32_16x16x128_f8f6f4 v[38:41], v[156:163], v[172:179], v[244:247]
	v_mfma_f32_16x16x128_f8f6f4 v[22:25], v[148:155], v[180:187], v[248:251]
	v_mfma_f32_16x16x128_f8f6f4 v[26:29], v[156:163], v[180:187], v[252:255]
	s_barrier
	s_add_i32 s62, s62, 2
	s_addk_i32 s60, 0x100
	s_addk_i32 s61, 0x100
	s_cmp_gt_u32 s62, 13
	s_cbranch_scc0 .LBB0_1610
	s_and_b64 vcc, exec, s[20:21]
	s_cbranch_vccz .LBB0_1613
	s_barrier

.LBB0_1856:
	s_add_i32 s81, s78, 0xffffff80
	s_cmp_eq_u32 s39, 12
	v_add_u32_e32 v2, s78, v220
	s_cselect_b64 vcc, -1, 0
	v_cndmask_b32_e32 v222, v2, v221, vcc
	ds_read_b128 v[2:5], v207
	ds_read_b128 v[6:9], v207 offset:1024
	ds_read_b128 v[10:13], v207 offset:2048
	ds_read_b128 v[14:17], v207 offset:3072
	ds_read_b128 v[18:21], v208
	ds_read_b128 v[22:25], v208 offset:1024
	ds_read_b128 v[26:29], v208 offset:2048
	ds_read_b128 v[30:33], v208 offset:3072
	s_and_b64 s[8:9], vcc, exec
	s_cselect_b32 s80, 0, s78
	s_or_b32 s79, s80, 0x80
	v_add_u32_e32 v225, 0x80, v222
	v_cndmask_b32_e32 v223, v195, v212, vcc
	v_cndmask_b32_e32 v226, v218, v213, vcc
	v_cndmask_b32_e32 v224, v217, v214, vcc
	v_cndmask_b32_e32 v227, v219, v215, vcc
	s_mov_b32 m0, s63
	ds_read_b128 v[34:37], v209
	ds_read_b128 v[38:41], v209 offset:1024
	ds_read_b128 v[42:45], v209 offset:2048
	ds_read_b128 v[46:49], v209 offset:3072
	ds_read_b128 v[50:53], v209 offset:4096
	ds_read_b128 v[54:57], v209 offset:5120
	ds_read_b128 v[58:61], v209 offset:6144
	ds_read_b128 v[62:65], v209 offset:7168
	buffer_load_dwordx4 v218, s[20:23], s81 offen lds
	s_mov_b32 m0, s65
	s_nop 0
	buffer_load_dwordx4 v219, s[20:23], s81 offen lds
	s_waitcnt vmcnt(8)
	s_waitcnt lgkmcnt(0)
	s_barrier
	s_waitcnt lgkmcnt(6)
	v_mfma_f32_16x16x128_f8f6f4 v[182:185], v[2:9], v[34:41], v[182:185]
	v_mfma_f32_16x16x128_f8f6f4 v[178:181], v[10:17], v[34:41], v[178:181]
	s_waitcnt lgkmcnt(4)
	v_mfma_f32_16x16x128_f8f6f4 v[170:173], v[2:9], v[42:49], v[170:173]
	v_mfma_f32_16x16x128_f8f6f4 v[166:169], v[10:17], v[42:49], v[166:169]
	s_waitcnt lgkmcnt(2)
	v_mfma_f32_16x16x128_f8f6f4 v[154:157], v[2:9], v[50:57], v[154:157]
	v_mfma_f32_16x16x128_f8f6f4 v[150:153], v[10:17], v[50:57], v[150:153]
	s_waitcnt lgkmcnt(0)
	v_mfma_f32_16x16x128_f8f6f4 v[138:141], v[2:9], v[58:65], v[138:141]
	v_mfma_f32_16x16x128_f8f6f4 v[134:137], v[10:17], v[58:65], v[134:137]
	v_mfma_f32_16x16x128_f8f6f4 v[190:193], v[18:25], v[34:41], v[190:193]
	v_mfma_f32_16x16x128_f8f6f4 v[186:189], v[26:33], v[34:41], v[186:189]
	v_mfma_f32_16x16x128_f8f6f4 v[174:177], v[18:25], v[42:49], v[174:177]
	v_mfma_f32_16x16x128_f8f6f4 v[162:165], v[26:33], v[42:49], v[162:165]
	v_mfma_f32_16x16x128_f8f6f4 v[158:161], v[18:25], v[50:57], v[158:161]
	v_mfma_f32_16x16x128_f8f6f4 v[146:149], v[26:33], v[50:57], v[146:149]
	v_mfma_f32_16x16x128_f8f6f4 v[142:145], v[18:25], v[58:65], v[142:145]
	v_mfma_f32_16x16x128_f8f6f4 v[130:133], v[26:33], v[58:65], v[130:133]
	s_barrier
	ds_read_b128 v[34:37], v209 offset:16384
	ds_read_b128 v[38:41], v209 offset:17408
	ds_read_b128 v[42:45], v209 offset:18432
	ds_read_b128 v[46:49], v209 offset:19456
	ds_read_b128 v[50:53], v209 offset:20480
	ds_read_b128 v[54:57], v209 offset:21504
	ds_read_b128 v[58:61], v209 offset:22528
	ds_read_b128 v[62:65], v209 offset:23552
	s_mov_b64 s[8:9], exec
	s_mov_b32 m0, s48
	v_readfirstlane_b32 s81, v222
	s_nop 4
	buffer_load_dwordx4 v200, s[16:19], s81 offen lds
	s_mov_b64 exec, s[8:9]
	s_mov_b64 s[8:9], exec
	s_mov_b32 m0, s49
	s_nop 0
	buffer_load_dwordx4 v202, s[16:19], s81 offen lds
	s_mov_b64 exec, s[8:9]
	v_add_u32_e32 v228, 0x40000, v222
	s_mov_b64 s[8:9], exec
	s_mov_b32 m0, s50
	v_readfirstlane_b32 s81, v228
	s_nop 4
	buffer_load_dwordx4 v200, s[16:19], s81 offen lds
	s_mov_b64 exec, s[8:9]
	s_mov_b64 s[8:9], exec
	s_mov_b32 m0, s51
	s_nop 0
	buffer_load_dwordx4 v202, s[16:19], s81 offen lds
	s_mov_b64 exec, s[8:9]
	s_mov_b32 m0, s47
	s_nop 0
	buffer_load_dwordx4 v223, s[20:23], s80 offen lds
	s_mov_b32 m0, s52
	s_nop 0
	buffer_load_dwordx4 v224, s[20:23], s80 offen lds
	s_waitcnt vmcnt(8)
	s_waitcnt lgkmcnt(0)
	s_barrier
	s_waitcnt lgkmcnt(6)
	v_mfma_f32_16x16x128_f8f6f4 v[118:121], v[2:9], v[34:41], v[118:121]
	v_mfma_f32_16x16x128_f8f6f4 v[114:117], v[10:17], v[34:41], v[114:117]
	s_waitcnt lgkmcnt(4)
	v_mfma_f32_16x16x128_f8f6f4 v[102:105], v[2:9], v[42:49], v[102:105]
	v_mfma_f32_16x16x128_f8f6f4 v[98:101], v[10:17], v[42:49], v[98:101]
	s_waitcnt lgkmcnt(2)
	v_mfma_f32_16x16x128_f8f6f4 v[86:89], v[2:9], v[50:57], v[86:89]
	v_mfma_f32_16x16x128_f8f6f4 v[82:85], v[10:17], v[50:57], v[82:85]
	s_waitcnt lgkmcnt(0)
	v_mfma_f32_16x16x128_f8f6f4 v[70:73], v[2:9], v[58:65], v[70:73]
	v_mfma_f32_16x16x128_f8f6f4 v[66:69], v[10:17], v[58:65], v[66:69]
	v_mfma_f32_16x16x128_f8f6f4 v[126:129], v[18:25], v[34:41], v[126:129]
	v_mfma_f32_16x16x128_f8f6f4 v[122:125], v[26:33], v[34:41], v[122:125]
	v_mfma_f32_16x16x128_f8f6f4 v[110:113], v[18:25], v[42:49], v[110:113]
	v_mfma_f32_16x16x128_f8f6f4 v[106:109], v[26:33], v[42:49], v[106:109]
	v_mfma_f32_16x16x128_f8f6f4 v[94:97], v[18:25], v[50:57], v[94:97]
	v_mfma_f32_16x16x128_f8f6f4 v[90:93], v[26:33], v[50:57], v[90:93]
	v_mfma_f32_16x16x128_f8f6f4 v[78:81], v[18:25], v[58:65], v[78:81]
	v_mfma_f32_16x16x128_f8f6f4 v[74:77], v[26:33], v[58:65], v[74:77]
	s_barrier
	v_add_u32_e32 v14, 0x18000, v206
	v_add_u32_e32 v30, 0x1c000, v206
	ds_read_b128 v[2:5], v14
	ds_read_b128 v[6:9], v14 offset:1024
	ds_read_b128 v[10:13], v14 offset:2048
	ds_read_b128 v[14:17], v14 offset:3072
	ds_read_b128 v[18:21], v30
	ds_read_b128 v[22:25], v30 offset:1024
	ds_read_b128 v[26:29], v30 offset:2048
	ds_read_b128 v[30:33], v30 offset:3072
	s_mov_b32 m0, s53
	ds_read_b128 v[34:37], v209 offset:32768
	ds_read_b128 v[38:41], v209 offset:33792
	ds_read_b128 v[42:45], v209 offset:34816
	ds_read_b128 v[46:49], v209 offset:35840
	ds_read_b128 v[50:53], v209 offset:36864
	ds_read_b128 v[54:57], v209 offset:37888
	ds_read_b128 v[58:61], v209 offset:38912
	ds_read_b128 v[62:65], v209 offset:39936
	buffer_load_dwordx4 v226, s[20:23], s80 offen lds
	s_mov_b32 m0, s56
	s_nop 0
	buffer_load_dwordx4 v227, s[20:23], s80 offen lds
	s_waitcnt vmcnt(8)
	s_waitcnt lgkmcnt(0)
	s_barrier
	s_waitcnt lgkmcnt(6)
	v_mfma_f32_16x16x128_f8f6f4 v[182:185], v[2:9], v[34:41], v[182:185]
	v_mfma_f32_16x16x128_f8f6f4 v[178:181], v[10:17], v[34:41], v[178:181]
	s_waitcnt lgkmcnt(4)
	v_mfma_f32_16x16x128_f8f6f4 v[170:173], v[2:9], v[42:49], v[170:173]
	v_mfma_f32_16x16x128_f8f6f4 v[166:169], v[10:17], v[42:49], v[166:169]
	s_waitcnt lgkmcnt(2)
	v_mfma_f32_16x16x128_f8f6f4 v[154:157], v[2:9], v[50:57], v[154:157]
	v_mfma_f32_16x16x128_f8f6f4 v[150:153], v[10:17], v[50:57], v[150:153]
	s_waitcnt lgkmcnt(0)
	v_mfma_f32_16x16x128_f8f6f4 v[138:141], v[2:9], v[58:65], v[138:141]
	v_mfma_f32_16x16x128_f8f6f4 v[134:137], v[10:17], v[58:65], v[134:137]
	v_mfma_f32_16x16x128_f8f6f4 v[190:193], v[18:25], v[34:41], v[190:193]
	v_mfma_f32_16x16x128_f8f6f4 v[186:189], v[26:33], v[34:41], v[186:189]
	v_mfma_f32_16x16x128_f8f6f4 v[174:177], v[18:25], v[42:49], v[174:177]
	v_mfma_f32_16x16x128_f8f6f4 v[162:165], v[26:33], v[42:49], v[162:165]
	v_mfma_f32_16x16x128_f8f6f4 v[158:161], v[18:25], v[50:57], v[158:161]
	v_mfma_f32_16x16x128_f8f6f4 v[146:149], v[26:33], v[50:57], v[146:149]
	v_mfma_f32_16x16x128_f8f6f4 v[142:145], v[18:25], v[58:65], v[142:145]
	v_mfma_f32_16x16x128_f8f6f4 v[130:133], v[26:33], v[58:65], v[130:133]
	s_barrier
	ds_read_b128 v[34:37], v209 offset:49152
	ds_read_b128 v[38:41], v209 offset:50176
	ds_read_b128 v[42:45], v209 offset:51200
	ds_read_b128 v[46:49], v209 offset:52224
	ds_read_b128 v[50:53], v209 offset:53248
	ds_read_b128 v[54:57], v209 offset:54272
	ds_read_b128 v[58:61], v209 offset:55296
	ds_read_b128 v[62:65], v209 offset:56320
	s_mov_b64 s[8:9], exec
	s_mov_b32 m0, s57
	v_readfirstlane_b32 s80, v225
	s_nop 4
	buffer_load_dwordx4 v200, s[16:19], s80 offen lds
	s_mov_b64 exec, s[8:9]
	s_mov_b64 s[8:9], exec
	s_mov_b32 m0, s58
	s_nop 0
	buffer_load_dwordx4 v202, s[16:19], s80 offen lds
	s_mov_b64 exec, s[8:9]
	v_add_u32_e32 v222, 0x40080, v222
	s_mov_b64 s[8:9], exec
	s_mov_b32 m0, s61
	v_readfirstlane_b32 s80, v222
	s_nop 4
	buffer_load_dwordx4 v200, s[16:19], s80 offen lds
	s_mov_b64 exec, s[8:9]
	s_mov_b64 s[8:9], exec
	s_mov_b32 m0, s62
	s_nop 0
	buffer_load_dwordx4 v202, s[16:19], s80 offen lds
	s_mov_b64 exec, s[8:9]
	s_mov_b32 m0, s59
	s_nop 0
	buffer_load_dwordx4 v223, s[20:23], s79 offen lds
	s_mov_b32 m0, s60
	s_nop 0
	buffer_load_dwordx4 v224, s[20:23], s79 offen lds
	s_waitcnt vmcnt(8)
	s_waitcnt lgkmcnt(0)
	s_barrier
	s_waitcnt lgkmcnt(6)
	v_mfma_f32_16x16x128_f8f6f4 v[118:121], v[2:9], v[34:41], v[118:121]
	v_mfma_f32_16x16x128_f8f6f4 v[114:117], v[10:17], v[34:41], v[114:117]
	s_waitcnt lgkmcnt(4)
	v_mfma_f32_16x16x128_f8f6f4 v[102:105], v[2:9], v[42:49], v[102:105]
	v_mfma_f32_16x16x128_f8f6f4 v[98:101], v[10:17], v[42:49], v[98:101]
	s_waitcnt lgkmcnt(2)
	v_mfma_f32_16x16x128_f8f6f4 v[86:89], v[2:9], v[50:57], v[86:89]
	v_mfma_f32_16x16x128_f8f6f4 v[82:85], v[10:17], v[50:57], v[82:85]
	s_waitcnt lgkmcnt(0)
	v_mfma_f32_16x16x128_f8f6f4 v[70:73], v[2:9], v[58:65], v[70:73]
	v_mfma_f32_16x16x128_f8f6f4 v[66:69], v[10:17], v[58:65], v[66:69]
	v_mfma_f32_16x16x128_f8f6f4 v[126:129], v[18:25], v[34:41], v[126:129]
	v_mfma_f32_16x16x128_f8f6f4 v[122:125], v[26:33], v[34:41], v[122:125]
	v_mfma_f32_16x16x128_f8f6f4 v[110:113], v[18:25], v[42:49], v[110:113]
	v_mfma_f32_16x16x128_f8f6f4 v[106:109], v[26:33], v[42:49], v[106:109]
	v_mfma_f32_16x16x128_f8f6f4 v[94:97], v[18:25], v[50:57], v[94:97]
	v_mfma_f32_16x16x128_f8f6f4 v[90:93], v[26:33], v[50:57], v[90:93]
	v_mfma_f32_16x16x128_f8f6f4 v[78:81], v[18:25], v[58:65], v[78:81]
	v_mfma_f32_16x16x128_f8f6f4 v[74:77], v[26:33], v[58:65], v[74:77]
	s_barrier
	s_add_i32 s39, s39, 2
	s_addk_i32 s78, 0x100
	s_cmp_gt_u32 s39, 13
	s_cbranch_scc0 .LBB0_1856
	s_and_b64 vcc, exec, s[30:31]
	s_cbranch_vccz .LBB0_1875
	s_barrier

.LBB0_1944:
	v_add_u32_e32 v14, 0x10000, v203
	v_add_u32_e32 v30, 0x14000, v203
	ds_read_b128 v[2:5], v14
	ds_read_b128 v[6:9], v14 offset:1024
	ds_read_b128 v[10:13], v14 offset:2048
	ds_read_b128 v[14:17], v14 offset:3072
	ds_read_b128 v[18:21], v30
	ds_read_b128 v[22:25], v30 offset:1024
	ds_read_b128 v[26:29], v30 offset:2048
	ds_read_b128 v[30:33], v30 offset:3072
	s_lshl_b32 s48, s95, 7
	s_add_i32 s49, s48, 0x100
	s_add_i32 s50, s49, s92
	s_and_b64 s[46:47], s[10:11], exec
	v_add_u32_e32 v34, s49, v209
	s_cselect_b32 s47, s93, s50
	v_cndmask_b32_e64 v211, v34, v210, s[10:11]
	s_or_b32 s46, s47, 0x80
	v_add_u32_e32 v212, 0x80, v211
	s_add_i32 s48, s48, s94
	s_mov_b32 m0, s77
	ds_read_b128 v[34:37], v204
	ds_read_b128 v[38:41], v204 offset:1024
	ds_read_b128 v[42:45], v204 offset:2048
	ds_read_b128 v[46:49], v204 offset:3072
	ds_read_b128 v[50:53], v204 offset:4096
	ds_read_b128 v[54:57], v204 offset:5120
	ds_read_b128 v[58:61], v204 offset:6144
	ds_read_b128 v[62:65], v204 offset:7168
	buffer_load_dwordx4 v194, s[12:15], s48 offen lds
	s_mov_b32 m0, s78
	s_nop 0
	buffer_load_dwordx4 v195, s[12:15], s48 offen lds
	s_waitcnt vmcnt(8)
	s_waitcnt lgkmcnt(0)
	s_barrier
	s_waitcnt lgkmcnt(6)
	v_mfma_f32_16x16x128_f8f6f4 v[190:193], v[2:9], v[34:41], v[190:193]
	v_mfma_f32_16x16x128_f8f6f4 v[186:189], v[10:17], v[34:41], v[186:189]
	s_waitcnt lgkmcnt(4)
	v_mfma_f32_16x16x128_f8f6f4 v[174:177], v[2:9], v[42:49], v[174:177]
	v_mfma_f32_16x16x128_f8f6f4 v[170:173], v[10:17], v[42:49], v[170:173]
	s_waitcnt lgkmcnt(2)
	v_mfma_f32_16x16x128_f8f6f4 v[158:161], v[2:9], v[50:57], v[158:161]
	v_mfma_f32_16x16x128_f8f6f4 v[154:157], v[10:17], v[50:57], v[154:157]
	s_waitcnt lgkmcnt(0)
	v_mfma_f32_16x16x128_f8f6f4 v[142:145], v[2:9], v[58:65], v[142:145]
	v_mfma_f32_16x16x128_f8f6f4 v[138:141], v[10:17], v[58:65], v[138:141]
	v_mfma_f32_16x16x128_f8f6f4 v[182:185], v[18:25], v[34:41], v[182:185]
	v_mfma_f32_16x16x128_f8f6f4 v[178:181], v[26:33], v[34:41], v[178:181]
	v_mfma_f32_16x16x128_f8f6f4 v[166:169], v[18:25], v[42:49], v[166:169]
	v_mfma_f32_16x16x128_f8f6f4 v[162:165], v[26:33], v[42:49], v[162:165]
	v_mfma_f32_16x16x128_f8f6f4 v[150:153], v[18:25], v[50:57], v[150:153]
	v_mfma_f32_16x16x128_f8f6f4 v[146:149], v[26:33], v[50:57], v[146:149]
	v_mfma_f32_16x16x128_f8f6f4 v[134:137], v[18:25], v[58:65], v[134:137]
	v_mfma_f32_16x16x128_f8f6f4 v[130:133], v[26:33], v[58:65], v[130:133]
	s_barrier
	ds_read_b128 v[34:37], v204 offset:16384
	ds_read_b128 v[38:41], v204 offset:17408
	ds_read_b128 v[42:45], v204 offset:18432
	ds_read_b128 v[46:49], v204 offset:19456
	ds_read_b128 v[50:53], v204 offset:20480
	ds_read_b128 v[54:57], v204 offset:21504
	ds_read_b128 v[58:61], v204 offset:22528
	ds_read_b128 v[62:65], v204 offset:23552
	s_mov_b64 s[10:11], exec
	s_mov_b32 m0, s60
	v_readfirstlane_b32 s48, v211
	s_nop 4
	buffer_load_dwordx4 v196, s[16:19], s48 offen lds
	s_mov_b64 exec, s[10:11]
	s_mov_b64 s[10:11], exec
	s_mov_b32 m0, s61
	s_nop 0
	buffer_load_dwordx4 v197, s[16:19], s48 offen lds
	s_mov_b64 exec, s[10:11]
	v_add_u32_e32 v213, 0x20000, v211
	s_mov_b64 s[10:11], exec
	s_mov_b32 m0, s62
	v_readfirstlane_b32 s48, v213
	s_nop 4
	buffer_load_dwordx4 v196, s[16:19], s48 offen lds
	s_mov_b64 exec, s[10:11]
	s_mov_b64 s[10:11], exec
	s_mov_b32 m0, s63
	s_nop 0
	buffer_load_dwordx4 v197, s[16:19], s48 offen lds
	s_mov_b64 exec, s[10:11]
	s_mov_b32 m0, s59
	s_nop 0
	buffer_load_dwordx4 v194, s[12:15], s47 offen lds
	s_mov_b32 m0, s64
	s_nop 0
	buffer_load_dwordx4 v195, s[12:15], s47 offen lds
	s_waitcnt vmcnt(8)
	s_waitcnt lgkmcnt(0)
	s_barrier
	s_waitcnt lgkmcnt(6)
	v_mfma_f32_16x16x128_f8f6f4 v[126:129], v[2:9], v[34:41], v[126:129]
	v_mfma_f32_16x16x128_f8f6f4 v[122:125], v[10:17], v[34:41], v[122:125]
	s_waitcnt lgkmcnt(4)
	v_mfma_f32_16x16x128_f8f6f4 v[110:113], v[2:9], v[42:49], v[110:113]
	v_mfma_f32_16x16x128_f8f6f4 v[106:109], v[10:17], v[42:49], v[106:109]
	s_waitcnt lgkmcnt(2)
	v_mfma_f32_16x16x128_f8f6f4 v[94:97], v[2:9], v[50:57], v[94:97]
	v_mfma_f32_16x16x128_f8f6f4 v[90:93], v[10:17], v[50:57], v[90:93]
	s_waitcnt lgkmcnt(0)
	v_mfma_f32_16x16x128_f8f6f4 v[78:81], v[2:9], v[58:65], v[78:81]
	v_mfma_f32_16x16x128_f8f6f4 v[74:77], v[10:17], v[58:65], v[74:77]
	v_mfma_f32_16x16x128_f8f6f4 v[118:121], v[18:25], v[34:41], v[118:121]
	v_mfma_f32_16x16x128_f8f6f4 v[114:117], v[26:33], v[34:41], v[114:117]
	v_mfma_f32_16x16x128_f8f6f4 v[102:105], v[18:25], v[42:49], v[102:105]
	v_mfma_f32_16x16x128_f8f6f4 v[98:101], v[26:33], v[42:49], v[98:101]
	v_mfma_f32_16x16x128_f8f6f4 v[86:89], v[18:25], v[50:57], v[86:89]
	v_mfma_f32_16x16x128_f8f6f4 v[82:85], v[26:33], v[50:57], v[82:85]
	v_mfma_f32_16x16x128_f8f6f4 v[70:73], v[18:25], v[58:65], v[70:73]
	v_mfma_f32_16x16x128_f8f6f4 v[66:69], v[26:33], v[58:65], v[66:69]
	s_barrier
	v_add_u32_e32 v14, 0x18000, v203
	v_add_u32_e32 v30, 0x1c000, v203
	ds_read_b128 v[2:5], v14
	ds_read_b128 v[6:9], v14 offset:1024
	ds_read_b128 v[10:13], v14 offset:2048
	ds_read_b128 v[14:17], v14 offset:3072
	ds_read_b128 v[18:21], v30
	ds_read_b128 v[22:25], v30 offset:1024
	ds_read_b128 v[26:29], v30 offset:2048
	ds_read_b128 v[30:33], v30 offset:3072
	s_add_i32 s47, s47, 0x20000
	s_mov_b32 m0, s65
	ds_read_b128 v[34:37], v204 offset:32768
	ds_read_b128 v[38:41], v204 offset:33792
	ds_read_b128 v[42:45], v204 offset:34816
	ds_read_b128 v[46:49], v204 offset:35840
	ds_read_b128 v[50:53], v204 offset:36864
	ds_read_b128 v[54:57], v204 offset:37888
	ds_read_b128 v[58:61], v204 offset:38912
	ds_read_b128 v[62:65], v204 offset:39936
	buffer_load_dwordx4 v194, s[12:15], s47 offen lds
	s_mov_b32 m0, s66
	s_nop 0
	buffer_load_dwordx4 v195, s[12:15], s47 offen lds
	s_waitcnt vmcnt(8)
	s_waitcnt lgkmcnt(0)
	s_barrier
	s_waitcnt lgkmcnt(6)
	v_mfma_f32_16x16x128_f8f6f4 v[190:193], v[2:9], v[34:41], v[190:193]
	v_mfma_f32_16x16x128_f8f6f4 v[186:189], v[10:17], v[34:41], v[186:189]
	s_waitcnt lgkmcnt(4)
	v_mfma_f32_16x16x128_f8f6f4 v[174:177], v[2:9], v[42:49], v[174:177]
	v_mfma_f32_16x16x128_f8f6f4 v[170:173], v[10:17], v[42:49], v[170:173]
	s_waitcnt lgkmcnt(2)
	v_mfma_f32_16x16x128_f8f6f4 v[158:161], v[2:9], v[50:57], v[158:161]
	v_mfma_f32_16x16x128_f8f6f4 v[154:157], v[10:17], v[50:57], v[154:157]
	s_waitcnt lgkmcnt(0)
	v_mfma_f32_16x16x128_f8f6f4 v[142:145], v[2:9], v[58:65], v[142:145]
	v_mfma_f32_16x16x128_f8f6f4 v[138:141], v[10:17], v[58:65], v[138:141]
	v_mfma_f32_16x16x128_f8f6f4 v[182:185], v[18:25], v[34:41], v[182:185]
	v_mfma_f32_16x16x128_f8f6f4 v[178:181], v[26:33], v[34:41], v[178:181]
	v_mfma_f32_16x16x128_f8f6f4 v[166:169], v[18:25], v[42:49], v[166:169]
	v_mfma_f32_16x16x128_f8f6f4 v[162:165], v[26:33], v[42:49], v[162:165]
	v_mfma_f32_16x16x128_f8f6f4 v[150:153], v[18:25], v[50:57], v[150:153]
	v_mfma_f32_16x16x128_f8f6f4 v[146:149], v[26:33], v[50:57], v[146:149]
	v_mfma_f32_16x16x128_f8f6f4 v[134:137], v[18:25], v[58:65], v[134:137]
	v_mfma_f32_16x16x128_f8f6f4 v[130:133], v[26:33], v[58:65], v[130:133]
	s_barrier
	ds_read_b128 v[34:37], v204 offset:49152
	ds_read_b128 v[38:41], v204 offset:50176
	ds_read_b128 v[42:45], v204 offset:51200
	ds_read_b128 v[46:49], v204 offset:52224
	ds_read_b128 v[50:53], v204 offset:53248
	ds_read_b128 v[54:57], v204 offset:54272
	ds_read_b128 v[58:61], v204 offset:55296
	ds_read_b128 v[62:65], v204 offset:56320
	s_mov_b64 s[10:11], exec
	s_mov_b32 m0, s70
	v_readfirstlane_b32 s47, v212
	s_nop 4
	buffer_load_dwordx4 v196, s[16:19], s47 offen lds
	s_mov_b64 exec, s[10:11]
	s_mov_b64 s[10:11], exec
	s_mov_b32 m0, s71
	s_nop 0
	buffer_load_dwordx4 v197, s[16:19], s47 offen lds
	s_mov_b64 exec, s[10:11]
	v_add_u32_e32 v211, 0x20080, v211
	s_mov_b64 s[10:11], exec
	s_mov_b32 m0, s74
	v_readfirstlane_b32 s47, v211
	s_nop 4
	buffer_load_dwordx4 v196, s[16:19], s47 offen lds
	s_mov_b64 exec, s[10:11]
	s_mov_b64 s[10:11], exec
	s_mov_b32 m0, s75
	s_nop 0
	buffer_load_dwordx4 v197, s[16:19], s47 offen lds
	s_mov_b64 exec, s[10:11]
	s_mov_b32 m0, s72
	s_nop 0
	buffer_load_dwordx4 v194, s[12:15], s46 offen lds
	s_mov_b32 m0, s73
	s_nop 0
	buffer_load_dwordx4 v195, s[12:15], s46 offen lds
	s_waitcnt vmcnt(8)
	s_waitcnt lgkmcnt(0)
	s_barrier
	s_waitcnt lgkmcnt(6)
	v_mfma_f32_16x16x128_f8f6f4 v[126:129], v[2:9], v[34:41], v[126:129]
	v_mfma_f32_16x16x128_f8f6f4 v[122:125], v[10:17], v[34:41], v[122:125]
	s_waitcnt lgkmcnt(4)
	v_mfma_f32_16x16x128_f8f6f4 v[110:113], v[2:9], v[42:49], v[110:113]
	v_mfma_f32_16x16x128_f8f6f4 v[106:109], v[10:17], v[42:49], v[106:109]
	s_waitcnt lgkmcnt(2)
	v_mfma_f32_16x16x128_f8f6f4 v[94:97], v[2:9], v[50:57], v[94:97]
	v_mfma_f32_16x16x128_f8f6f4 v[90:93], v[10:17], v[50:57], v[90:93]
	s_waitcnt lgkmcnt(0)
	v_mfma_f32_16x16x128_f8f6f4 v[78:81], v[2:9], v[58:65], v[78:81]
	v_mfma_f32_16x16x128_f8f6f4 v[74:77], v[10:17], v[58:65], v[74:77]
	v_mfma_f32_16x16x128_f8f6f4 v[118:121], v[18:25], v[34:41], v[118:121]
	v_mfma_f32_16x16x128_f8f6f4 v[114:117], v[26:33], v[34:41], v[114:117]
	v_mfma_f32_16x16x128_f8f6f4 v[102:105], v[18:25], v[42:49], v[102:105]
	v_mfma_f32_16x16x128_f8f6f4 v[98:101], v[26:33], v[42:49], v[98:101]
	v_mfma_f32_16x16x128_f8f6f4 v[86:89], v[18:25], v[50:57], v[86:89]
	v_mfma_f32_16x16x128_f8f6f4 v[82:85], v[26:33], v[50:57], v[82:85]
	v_mfma_f32_16x16x128_f8f6f4 v[70:73], v[18:25], v[58:65], v[70:73]
	v_mfma_f32_16x16x128_f8f6f4 v[66:69], v[26:33], v[58:65], v[66:69]
	s_barrier
	s_add_i32 s95, s95, 2
	s_cmp_ge_i32 s95, s67
	s_cbranch_scc0 .LBB0_1927

.LBB0_3037:
	ds_read_b128 v[130:133], v144
	ds_read_b128 v[134:137], v144 offset:1024
	ds_read_b128 v[150:153], v144 offset:2048
	ds_read_b128 v[154:157], v144 offset:3072
	ds_read_b128 v[158:161], v145
	ds_read_b128 v[162:165], v145 offset:1024
	ds_read_b128 v[166:169], v145 offset:2048
	ds_read_b128 v[170:173], v145 offset:3072
	s_add_i32 s70, s69, -2
	s_add_i32 s71, s67, 0xfffc0080
	s_cmp_eq_u32 s53, s69
	s_cselect_b64 s[26:27], -1, 0
	s_and_b64 s[6:7], s[26:27], exec
	s_cselect_b32 s73, s66, s71
	s_cselect_b32 s72, s65, s68
	s_or_b32 s71, s73, 0x80
	s_mov_b32 m0, s56
	ds_read_b128 v[174:177], v146
	ds_read_b128 v[178:181], v146 offset:1024
	ds_read_b128 v[182:185], v146 offset:2048
	ds_read_b128 v[186:189], v146 offset:3072
	ds_read_b128 v[190:193], v146 offset:4096
	ds_read_b128 v[194:197], v146 offset:5120
	ds_read_b128 v[198:201], v146 offset:6144
	ds_read_b128 v[202:205], v146 offset:7168
	buffer_load_dwordx4 v139, s[8:11], s67 offen lds
	s_mov_b32 m0, s58
	s_nop 0
	buffer_load_dwordx4 v140, s[8:11], s67 offen lds
	s_waitcnt vmcnt(8)
	s_waitcnt lgkmcnt(0)
	s_barrier
	s_waitcnt lgkmcnt(6)
	v_mfma_f32_16x16x128_f8f6f4 v[126:129], v[130:137], v[174:181], v[126:129]
	v_mfma_f32_16x16x128_f8f6f4 v[122:125], v[150:157], v[174:181], v[122:125]
	s_waitcnt lgkmcnt(4)
	v_mfma_f32_16x16x128_f8f6f4 v[110:113], v[130:137], v[182:189], v[110:113]
	v_mfma_f32_16x16x128_f8f6f4 v[106:109], v[150:157], v[182:189], v[106:109]
	s_waitcnt lgkmcnt(2)
	v_mfma_f32_16x16x128_f8f6f4 v[206:209], v[130:137], v[190:197], v[94:97]
	v_mfma_f32_16x16x128_f8f6f4 v[210:213], v[150:157], v[190:197], v[90:93]
	s_waitcnt lgkmcnt(0)
	v_mfma_f32_16x16x128_f8f6f4 v[214:217], v[130:137], v[198:205], v[78:81]
	v_mfma_f32_16x16x128_f8f6f4 v[218:221], v[150:157], v[198:205], v[74:77]
	v_mfma_f32_16x16x128_f8f6f4 v[118:121], v[158:165], v[174:181], v[118:121]
	v_mfma_f32_16x16x128_f8f6f4 v[114:117], v[166:173], v[174:181], v[114:117]
	v_mfma_f32_16x16x128_f8f6f4 v[102:105], v[158:165], v[182:189], v[102:105]
	v_mfma_f32_16x16x128_f8f6f4 v[98:101], v[166:173], v[182:189], v[98:101]
	v_mfma_f32_16x16x128_f8f6f4 v[174:177], v[158:165], v[190:197], v[86:89]
	v_mfma_f32_16x16x128_f8f6f4 v[178:181], v[166:173], v[190:197], v[82:85]
	v_mfma_f32_16x16x128_f8f6f4 v[182:185], v[158:165], v[198:205], v[70:73]
	v_mfma_f32_16x16x128_f8f6f4 v[186:189], v[166:173], v[198:205], v[66:69]
	s_barrier
	s_mov_b32 m0, s30
	s_mov_b32 s6, s10
	s_mov_b32 s7, s11
	s_nop 1
	ds_read_b128 v[66:69], v146 offset:16384
	ds_read_b128 v[70:73], v146 offset:17408
	ds_read_b128 v[74:77], v146 offset:18432
	ds_read_b128 v[78:81], v146 offset:19456
	ds_read_b128 v[82:85], v146 offset:20480
	ds_read_b128 v[86:89], v146 offset:21504
	ds_read_b128 v[90:93], v146 offset:22528
	ds_read_b128 v[94:97], v146 offset:23552
	buffer_load_dwordx4 v1, s[4:7], s72 offen lds
	s_mov_b32 m0, s31
	s_add_i32 s74, s72, 0x40000
	buffer_load_dwordx4 v138, s[4:7], s72 offen lds
	s_mov_b32 m0, s33
	s_nop 0
	buffer_load_dwordx4 v1, s[4:7], s74 offen lds
	s_mov_b32 m0, s34
	s_nop 0
	buffer_load_dwordx4 v138, s[4:7], s74 offen lds
	s_mov_b32 m0, s29
	s_nop 0
	buffer_load_dwordx4 v139, s[8:11], s73 offen lds
	s_mov_b32 m0, s35
	s_nop 0
	buffer_load_dwordx4 v140, s[8:11], s73 offen lds
	s_waitcnt vmcnt(8)
	s_waitcnt lgkmcnt(0)
	s_barrier
	s_waitcnt lgkmcnt(6)
	v_mfma_f32_16x16x128_f8f6f4 v[62:65], v[130:137], v[66:73], v[62:65]
	v_mfma_f32_16x16x128_f8f6f4 v[58:61], v[150:157], v[66:73], v[58:61]
	s_waitcnt lgkmcnt(4)
	v_mfma_f32_16x16x128_f8f6f4 v[190:193], v[130:137], v[74:81], v[46:49]
	v_mfma_f32_16x16x128_f8f6f4 v[194:197], v[150:157], v[74:81], v[42:45]
	s_waitcnt lgkmcnt(2)
	v_mfma_f32_16x16x128_f8f6f4 v[198:201], v[130:137], v[82:89], v[30:33]
	v_mfma_f32_16x16x128_f8f6f4 v[202:205], v[150:157], v[82:89], v[26:29]
	s_waitcnt lgkmcnt(0)
	v_mfma_f32_16x16x128_f8f6f4 v[222:225], v[130:137], v[90:97], v[14:17]
	v_mfma_f32_16x16x128_f8f6f4 v[226:229], v[150:157], v[90:97], v[10:13]
	v_mfma_f32_16x16x128_f8f6f4 v[54:57], v[158:165], v[66:73], v[54:57]
	v_mfma_f32_16x16x128_f8f6f4 v[50:53], v[166:173], v[66:73], v[50:53]
	v_mfma_f32_16x16x128_f8f6f4 v[230:233], v[158:165], v[74:81], v[38:41]
	v_mfma_f32_16x16x128_f8f6f4 v[234:237], v[166:173], v[74:81], v[34:37]
	v_mfma_f32_16x16x128_f8f6f4 v[238:241], v[158:165], v[82:89], v[22:25]
	v_mfma_f32_16x16x128_f8f6f4 v[242:245], v[166:173], v[82:89], v[18:21]
	v_mfma_f32_16x16x128_f8f6f4 v[246:249], v[158:165], v[90:97], v[6:9]
	v_mfma_f32_16x16x128_f8f6f4 v[250:253], v[166:173], v[90:97], v[2:5]
	s_barrier
	s_nop 4
	ds_read_b128 v[2:5], v147
	ds_read_b128 v[6:9], v147 offset:1024
	ds_read_b128 v[18:21], v147 offset:2048
	ds_read_b128 v[22:25], v147 offset:3072
	ds_read_b128 v[130:133], v148
	ds_read_b128 v[134:137], v148 offset:1024
	ds_read_b128 v[150:153], v148 offset:2048
	ds_read_b128 v[154:157], v148 offset:3072
	s_add_i32 s73, s73, 0x40000
	s_mov_b32 m0, s38
	ds_read_b128 v[10:13], v146 offset:32768
	ds_read_b128 v[14:17], v146 offset:33792
	ds_read_b128 v[26:29], v146 offset:34816
	ds_read_b128 v[30:33], v146 offset:35840
	ds_read_b128 v[34:37], v146 offset:36864
	ds_read_b128 v[38:41], v146 offset:37888
	ds_read_b128 v[42:45], v146 offset:38912
	ds_read_b128 v[46:49], v146 offset:39936
	buffer_load_dwordx4 v139, s[8:11], s73 offen lds
	s_mov_b32 m0, s39
	s_nop 0
	buffer_load_dwordx4 v140, s[8:11], s73 offen lds
	s_waitcnt vmcnt(8)
	s_waitcnt lgkmcnt(0)
	s_barrier
	s_waitcnt lgkmcnt(6)
	v_mfma_f32_16x16x128_f8f6f4 v[126:129], v[2:9], v[10:17], v[126:129]
	v_mfma_f32_16x16x128_f8f6f4 v[122:125], v[18:25], v[10:17], v[122:125]
	s_waitcnt lgkmcnt(4)
	v_mfma_f32_16x16x128_f8f6f4 v[110:113], v[2:9], v[26:33], v[110:113]
	v_mfma_f32_16x16x128_f8f6f4 v[106:109], v[18:25], v[26:33], v[106:109]
	s_waitcnt lgkmcnt(2)
	v_mfma_f32_16x16x128_f8f6f4 v[94:97], v[2:9], v[34:41], v[206:209]
	v_mfma_f32_16x16x128_f8f6f4 v[90:93], v[18:25], v[34:41], v[210:213]
	s_waitcnt lgkmcnt(0)
	v_mfma_f32_16x16x128_f8f6f4 v[78:81], v[2:9], v[42:49], v[214:217]
	v_mfma_f32_16x16x128_f8f6f4 v[74:77], v[18:25], v[42:49], v[218:221]
	v_mfma_f32_16x16x128_f8f6f4 v[118:121], v[130:137], v[10:17], v[118:121]
	v_mfma_f32_16x16x128_f8f6f4 v[114:117], v[150:157], v[10:17], v[114:117]
	v_mfma_f32_16x16x128_f8f6f4 v[102:105], v[130:137], v[26:33], v[102:105]
	v_mfma_f32_16x16x128_f8f6f4 v[98:101], v[150:157], v[26:33], v[98:101]
	v_mfma_f32_16x16x128_f8f6f4 v[86:89], v[130:137], v[34:41], v[174:177]
	v_mfma_f32_16x16x128_f8f6f4 v[82:85], v[150:157], v[34:41], v[178:181]
	v_mfma_f32_16x16x128_f8f6f4 v[70:73], v[130:137], v[42:49], v[182:185]
	v_mfma_f32_16x16x128_f8f6f4 v[66:69], v[150:157], v[42:49], v[186:189]
	s_barrier
	s_mov_b32 m0, s47
	s_or_b32 s73, s72, 0x80
	ds_read_b128 v[34:37], v146 offset:49152
	ds_read_b128 v[38:41], v146 offset:50176
	ds_read_b128 v[158:161], v146 offset:51200
	ds_read_b128 v[162:165], v146 offset:52224
	ds_read_b128 v[166:169], v146 offset:53248
	ds_read_b128 v[170:173], v146 offset:54272
	ds_read_b128 v[174:177], v146 offset:55296
	ds_read_b128 v[178:181], v146 offset:56320
	buffer_load_dwordx4 v1, s[4:7], s73 offen lds
	s_mov_b32 m0, s48
	s_add_i32 s72, s72, 0x40080
	buffer_load_dwordx4 v138, s[4:7], s73 offen lds
	s_mov_b32 m0, s51
	s_nop 0
	buffer_load_dwordx4 v1, s[4:7], s72 offen lds
	s_mov_b32 m0, s52
	s_nop 0
	buffer_load_dwordx4 v138, s[4:7], s72 offen lds
	s_mov_b32 m0, s49
	s_nop 0
	buffer_load_dwordx4 v139, s[8:11], s71 offen lds
	s_mov_b32 m0, s50
	s_nop 0
	buffer_load_dwordx4 v140, s[8:11], s71 offen lds
	s_waitcnt vmcnt(8)
	s_waitcnt lgkmcnt(0)
	s_barrier
	s_waitcnt lgkmcnt(6)
	v_mfma_f32_16x16x128_f8f6f4 v[62:65], v[2:9], v[34:41], v[62:65]
	v_mfma_f32_16x16x128_f8f6f4 v[58:61], v[18:25], v[34:41], v[58:61]
	s_waitcnt lgkmcnt(4)
	v_mfma_f32_16x16x128_f8f6f4 v[46:49], v[2:9], v[158:165], v[190:193]
	v_mfma_f32_16x16x128_f8f6f4 v[42:45], v[18:25], v[158:165], v[194:197]
	s_waitcnt lgkmcnt(2)
	v_mfma_f32_16x16x128_f8f6f4 v[30:33], v[2:9], v[166:173], v[198:201]
	v_mfma_f32_16x16x128_f8f6f4 v[26:29], v[18:25], v[166:173], v[202:205]
	s_waitcnt lgkmcnt(0)
	v_mfma_f32_16x16x128_f8f6f4 v[14:17], v[2:9], v[174:181], v[222:225]
	v_mfma_f32_16x16x128_f8f6f4 v[10:13], v[18:25], v[174:181], v[226:229]
	v_mfma_f32_16x16x128_f8f6f4 v[54:57], v[130:137], v[34:41], v[54:57]
	v_mfma_f32_16x16x128_f8f6f4 v[50:53], v[150:157], v[34:41], v[50:53]
	v_mfma_f32_16x16x128_f8f6f4 v[38:41], v[130:137], v[158:165], v[230:233]
	v_mfma_f32_16x16x128_f8f6f4 v[34:37], v[150:157], v[158:165], v[234:237]
	v_mfma_f32_16x16x128_f8f6f4 v[22:25], v[130:137], v[166:173], v[238:241]
	v_mfma_f32_16x16x128_f8f6f4 v[18:21], v[150:157], v[166:173], v[242:245]
	v_mfma_f32_16x16x128_f8f6f4 v[6:9], v[130:137], v[174:181], v[246:249]
	v_mfma_f32_16x16x128_f8f6f4 v[2:5], v[150:157], v[174:181], v[250:253]
	s_barrier
	s_bitcmp0_b32 s70, 1
	s_cselect_b64 s[6:7], -1, 0
	s_or_b64 s[6:7], s[26:27], s[6:7]
	s_and_b64 vcc, exec, s[6:7]
	s_cbranch_vccnz .LBB0_3039
	s_lshr_b32 s6, s69, 2
	v_mov_b32_e32 v130, v143
	v_mov_b32_e32 v131, v142
	s_mulk_i32 s6, 0x42
	s_add_i32 s6, s6, s63
	v_lshlrev_b32_e32 v131, 4, v131
	s_lshl_b32 s6, s6, 3
	v_add3_u32 v130, v130, s57, v131
	s_add_i32 s6, s6, s64
	s_ashr_i32 s7, s6, 31
	v_ashrrev_i32_e32 v131, 31, v130
	v_add_u32_e32 v136, 64, v130
	s_lshl_b64 s[26:27], s[6:7], 16
	v_lshl_add_u64 v[132:133], v[130:131], 3, s[16:17]
	v_ashrrev_i32_e32 v137, 31, v136
	v_lshl_add_u64 v[134:135], v[132:133], 0, s[26:27]
	s_addk_i32 s6, 0xfdf0
	v_lshl_add_u64 v[136:137], v[136:137], 3, s[16:17]
	global_load_dwordx2 v[134:135], v[134:135], off
	s_ashr_i32 s7, s6, 31
	v_lshl_add_u64 v[150:151], v[136:137], 0, s[26:27]
	s_lshl_b64 s[6:7], s[6:7], 16
	global_load_dwordx2 v[150:151], v[150:151], off
	v_lshl_add_u64 v[132:133], v[132:133], 0, s[6:7]
	v_lshl_add_u64 v[136:137], v[136:137], 0, s[6:7]
	global_load_dwordx2 v[136:137], v[136:137], off
	v_add_u32_e32 v152, 0x80, v130
	global_load_dwordx2 v[132:133], v[132:133], off
	v_ashrrev_i32_e32 v153, 31, v152
	v_lshl_add_u64 v[152:153], v[152:153], 3, s[16:17]
	v_lshl_add_u64 v[154:155], v[152:153], 0, s[26:27]
	global_load_dwordx2 v[154:155], v[154:155], off
	v_add_u32_e32 v156, 0xc0, v130
	v_ashrrev_i32_e32 v157, 31, v156
	v_lshl_add_u64 v[156:157], v[156:157], 3, s[16:17]
	v_lshl_add_u64 v[158:159], v[156:157], 0, s[26:27]
	v_lshl_add_u64 v[152:153], v[152:153], 0, s[6:7]
	v_lshl_add_u64 v[156:157], v[156:157], 0, s[6:7]
	global_load_dwordx2 v[152:153], v[152:153], off
	s_nop 0
	global_load_dwordx2 v[158:159], v[158:159], off
	s_nop 0
	global_load_dwordx2 v[156:157], v[156:157], off
	s_waitcnt vmcnt(7)
	v_cvt_f32_ubyte0_e32 v131, v134
	v_cvt_f32_ubyte1_e32 v149, v134
	v_cvt_f32_ubyte0_e32 v160, v135
	v_cvt_f32_ubyte1_e32 v161, v135
	v_cvt_f32_ubyte2_e32 v162, v134
	v_cvt_f32_ubyte3_e32 v163, v134
	v_cvt_f32_ubyte2_e32 v168, v135
	v_cvt_f32_ubyte3_e32 v169, v135
	v_rcp_iflag_f32_e32 v134, v131
	v_rcp_iflag_f32_e32 v135, v149
	s_waitcnt vmcnt(6)
	v_cvt_f32_ubyte0_e32 v131, v150
	v_cvt_f32_ubyte1_e32 v149, v150
	v_cvt_f32_ubyte2_e32 v180, v150
	v_cvt_f32_ubyte3_e32 v150, v150
	v_rcp_iflag_f32_e32 v180, v180
	v_rcp_iflag_f32_e32 v181, v150
	s_waitcnt vmcnt(4)
	v_cvt_f32_ubyte3_e32 v165, v132
	v_cvt_f32_ubyte2_e32 v164, v132
	v_cvt_f32_ubyte1_e32 v167, v132
	v_cvt_f32_ubyte0_e32 v166, v132
	v_cvt_f32_ubyte3_e32 v171, v133
	v_cvt_f32_ubyte2_e32 v170, v133
	v_cvt_f32_ubyte1_e32 v173, v133
	v_cvt_f32_ubyte0_e32 v172, v133
	v_cvt_f32_ubyte3_e32 v133, v136
	v_cvt_f32_ubyte2_e32 v132, v136
	v_cvt_f32_ubyte1_e32 v175, v136
	v_cvt_f32_ubyte0_e32 v174, v136
	v_cvt_f32_ubyte2_e32 v136, v151
	v_rcp_iflag_f32_e32 v176, v131
	v_cvt_f32_ubyte3_e32 v131, v151
	v_cvt_f32_ubyte0_e32 v178, v151
	v_cvt_f32_ubyte1_e32 v179, v151
	v_rcp_iflag_f32_e32 v150, v136
	v_rcp_iflag_f32_e32 v151, v131
	v_pk_mul_f32 v[132:133], v[180:181], v[132:133]
	v_rcp_iflag_f32_e32 v177, v149
	v_pk_mul_f32 v[120:121], v[120:121], v[132:133]
	v_cvt_f32_ubyte3_e32 v133, v137
	v_cvt_f32_ubyte2_e32 v132, v137
	v_pk_mul_f32 v[132:133], v[150:151], v[132:133]
	v_pk_mul_f32 v[134:135], v[134:135], v[166:167]
	v_pk_mul_f32 v[116:117], v[116:117], v[132:133]
	v_add_u32_e32 v132, 0x100, v130
	v_ashrrev_i32_e32 v133, 31, v132
	v_pk_mul_f32 v[126:127], v[126:127], v[134:135]
	v_pk_mul_f32 v[134:135], v[176:177], v[174:175]
	v_lshl_add_u64 v[132:133], v[132:133], 3, s[16:17]
	v_pk_mul_f32 v[118:119], v[118:119], v[134:135]
	v_cvt_f32_ubyte1_e32 v135, v137
	v_cvt_f32_ubyte0_e32 v134, v137
	v_lshl_add_u64 v[136:137], v[132:133], 0, s[26:27]
	global_load_dwordx2 v[136:137], v[136:137], off
	v_lshl_add_u64 v[132:133], v[132:133], 0, s[6:7]
	global_load_dwordx2 v[132:133], v[132:133], off
	v_rcp_iflag_f32_e32 v178, v178
	v_rcp_iflag_f32_e32 v179, v179
	v_rcp_iflag_f32_e32 v160, v160
	v_rcp_iflag_f32_e32 v161, v161
	s_waitcnt vmcnt(5)
	v_cvt_f32_ubyte0_e32 v131, v154
	v_pk_mul_f32 v[134:135], v[178:179], v[134:135]
	v_rcp_iflag_f32_e32 v162, v162
	v_pk_mul_f32 v[114:115], v[114:115], v[134:135]
	v_rcp_iflag_f32_e32 v134, v131
	v_cvt_f32_ubyte1_e32 v131, v154
	v_rcp_iflag_f32_e32 v135, v131
	v_cvt_f32_ubyte0_e32 v131, v155
	v_rcp_iflag_f32_e32 v163, v163
	v_rcp_iflag_f32_e32 v168, v168
	v_rcp_iflag_f32_e32 v169, v169
	v_rcp_iflag_f32_e32 v150, v131
	v_cvt_f32_ubyte1_e32 v131, v155
	v_pk_mul_f32 v[160:161], v[160:161], v[172:173]
	v_rcp_iflag_f32_e32 v151, v131
	v_cvt_f32_ubyte2_e32 v131, v154
	v_pk_mul_f32 v[122:123], v[122:123], v[160:161]
	v_rcp_iflag_f32_e32 v160, v131
	v_cvt_f32_ubyte3_e32 v131, v154
	v_rcp_iflag_f32_e32 v161, v131
	v_pk_mul_f32 v[162:163], v[162:163], v[164:165]
	v_pk_mul_f32 v[164:165], v[168:169], v[170:171]
	v_pk_mul_f32 v[128:129], v[128:129], v[162:163]
	v_pk_mul_f32 v[124:125], v[124:125], v[164:165]
	s_waitcnt vmcnt(4)
	v_cvt_f32_ubyte1_e32 v165, v152
	v_cvt_f32_ubyte0_e32 v164, v152
	v_cvt_f32_ubyte3_e32 v163, v152
	v_cvt_f32_ubyte2_e32 v162, v152
	v_pk_mul_f32 v[134:135], v[134:135], v[164:165]
	v_cvt_f32_ubyte2_e32 v131, v155
	v_pk_mul_f32 v[160:161], v[160:161], v[162:163]
	v_pk_mul_f32 v[110:111], v[110:111], v[134:135]
	v_rcp_iflag_f32_e32 v134, v131
	v_cvt_f32_ubyte3_e32 v131, v155
	v_pk_mul_f32 v[112:113], v[112:113], v[160:161]
	v_rcp_iflag_f32_e32 v135, v131
	v_cvt_f32_ubyte1_e32 v161, v153
	v_cvt_f32_ubyte0_e32 v160, v153
	v_pk_mul_f32 v[150:151], v[150:151], v[160:161]
	s_waitcnt vmcnt(3)
	v_cvt_f32_ubyte0_e32 v131, v158
	v_pk_mul_f32 v[106:107], v[106:107], v[150:151]
	v_rcp_iflag_f32_e32 v150, v131
	v_cvt_f32_ubyte1_e32 v131, v158
	v_cvt_f32_ubyte3_e32 v155, v153
	v_cvt_f32_ubyte2_e32 v154, v153
	v_rcp_iflag_f32_e32 v151, v131
	v_cvt_f32_ubyte0_e32 v131, v159
	v_pk_mul_f32 v[134:135], v[134:135], v[154:155]
	v_rcp_iflag_f32_e32 v154, v131
	v_cvt_f32_ubyte1_e32 v131, v159
	v_rcp_iflag_f32_e32 v155, v131
	v_cvt_f32_ubyte2_e32 v131, v158
	v_rcp_iflag_f32_e32 v160, v131
	v_cvt_f32_ubyte3_e32 v131, v158
	s_waitcnt vmcnt(2)
	v_cvt_f32_ubyte1_e32 v165, v156
	v_cvt_f32_ubyte0_e32 v164, v156
	v_pk_mul_f32 v[108:109], v[108:109], v[134:135]
	v_add_u32_e32 v134, 0x140, v130
	v_rcp_iflag_f32_e32 v161, v131
	v_pk_mul_f32 v[150:151], v[150:151], v[164:165]
	v_cvt_f32_ubyte2_e32 v131, v159
	v_ashrrev_i32_e32 v135, 31, v134
	v_pk_mul_f32 v[102:103], v[102:103], v[150:151]
	v_rcp_iflag_f32_e32 v150, v131
	v_cvt_f32_ubyte3_e32 v131, v159
	v_lshl_add_u64 v[134:135], v[134:135], 3, s[16:17]
	v_rcp_iflag_f32_e32 v151, v131
	v_lshl_add_u64 v[152:153], v[134:135], 0, s[26:27]
	global_load_dwordx2 v[152:153], v[152:153], off
	v_cvt_f32_ubyte3_e32 v159, v157
	v_cvt_f32_ubyte2_e32 v158, v157
	v_pk_mul_f32 v[150:151], v[150:151], v[158:159]
	v_cvt_f32_ubyte3_e32 v163, v156
	v_pk_mul_f32 v[100:101], v[100:101], v[150:151]
	v_add_u32_e32 v150, 0x180, v130
	v_cvt_f32_ubyte2_e32 v162, v156
	v_ashrrev_i32_e32 v151, 31, v150
	v_pk_mul_f32 v[160:161], v[160:161], v[162:163]
	v_lshl_add_u64 v[150:151], v[150:151], 3, s[16:17]
	v_lshl_add_u64 v[134:135], v[134:135], 0, s[6:7]
	v_pk_mul_f32 v[104:105], v[104:105], v[160:161]
	v_cvt_f32_ubyte1_e32 v161, v157
	v_cvt_f32_ubyte0_e32 v160, v157
	v_lshl_add_u64 v[156:157], v[150:151], 0, s[26:27]
	v_lshl_add_u64 v[150:151], v[150:151], 0, s[6:7]
	v_pk_mul_f32 v[154:155], v[154:155], v[160:161]
	global_load_dwordx2 v[150:151], v[150:151], off
	v_pk_mul_f32 v[98:99], v[98:99], v[154:155]
	global_load_dwordx2 v[134:135], v[134:135], off
	s_waitcnt vmcnt(4)
	v_cvt_f32_ubyte0_e32 v131, v136
	v_rcp_iflag_f32_e32 v154, v131
	v_cvt_f32_ubyte1_e32 v131, v136
	v_rcp_iflag_f32_e32 v155, v131
	v_cvt_f32_ubyte0_e32 v131, v137
	v_rcp_iflag_f32_e32 v158, v131
	v_cvt_f32_ubyte1_e32 v131, v137
	v_rcp_iflag_f32_e32 v159, v131
	v_cvt_f32_ubyte2_e32 v131, v136
	global_load_dwordx2 v[156:157], v[156:157], off
	v_rcp_iflag_f32_e32 v160, v131
	v_cvt_f32_ubyte3_e32 v131, v136
	v_rcp_iflag_f32_e32 v161, v131
	v_cvt_f32_ubyte2_e32 v131, v137
	v_rcp_iflag_f32_e32 v136, v131
	v_cvt_f32_ubyte3_e32 v131, v137
	v_rcp_iflag_f32_e32 v137, v131
	s_waitcnt vmcnt(4)
	v_cvt_f32_ubyte1_e32 v165, v132
	v_cvt_f32_ubyte0_e32 v164, v132
	v_pk_mul_f32 v[154:155], v[154:155], v[164:165]
	v_cvt_f32_ubyte3_e32 v163, v132
	v_pk_mul_f32 v[94:95], v[94:95], v[154:155]
	v_cvt_f32_ubyte3_e32 v155, v133
	v_cvt_f32_ubyte2_e32 v154, v133
	v_pk_mul_f32 v[136:137], v[136:137], v[154:155]
	v_cvt_f32_ubyte2_e32 v162, v132
	v_pk_mul_f32 v[92:93], v[92:93], v[136:137]
	v_add_u32_e32 v136, 0x1c0, v130
	v_ashrrev_i32_e32 v137, 31, v136
	v_lshl_add_u64 v[136:137], v[136:137], 3, s[16:17]
	v_lshl_add_u64 v[154:155], v[136:137], 0, s[26:27]
	global_load_dwordx2 v[154:155], v[154:155], off
	v_lshl_add_u64 v[136:137], v[136:137], 0, s[6:7]
	global_load_dwordx2 v[136:137], v[136:137], off
	v_pk_mul_f32 v[160:161], v[160:161], v[162:163]
	s_waitcnt vmcnt(5)
	v_cvt_f32_ubyte0_e32 v131, v152
	v_pk_mul_f32 v[96:97], v[96:97], v[160:161]
	v_cvt_f32_ubyte1_e32 v161, v133
	v_cvt_f32_ubyte0_e32 v160, v133
	v_pk_mul_f32 v[132:133], v[158:159], v[160:161]
	s_waitcnt vmcnt(3)
	v_cvt_f32_ubyte3_e32 v163, v134
	v_pk_mul_f32 v[90:91], v[90:91], v[132:133]
	v_rcp_iflag_f32_e32 v132, v131
	v_cvt_f32_ubyte1_e32 v131, v152
	v_rcp_iflag_f32_e32 v133, v131
	v_cvt_f32_ubyte0_e32 v131, v153
	v_rcp_iflag_f32_e32 v158, v131
	v_cvt_f32_ubyte1_e32 v131, v153
	v_rcp_iflag_f32_e32 v159, v131
	v_cvt_f32_ubyte2_e32 v131, v152
	v_rcp_iflag_f32_e32 v160, v131
	v_cvt_f32_ubyte3_e32 v131, v152
	v_rcp_iflag_f32_e32 v161, v131
	v_cvt_f32_ubyte2_e32 v162, v134
	v_cvt_f32_ubyte1_e32 v165, v134
	v_cvt_f32_ubyte0_e32 v164, v134
	v_pk_mul_f32 v[132:133], v[132:133], v[164:165]
	v_pk_mul_f32 v[160:161], v[160:161], v[162:163]
	v_cvt_f32_ubyte2_e32 v131, v153
	v_pk_mul_f32 v[88:89], v[88:89], v[160:161]
	v_pk_mul_f32 v[86:87], v[86:87], v[132:133]
	v_rcp_iflag_f32_e32 v132, v131
	v_cvt_f32_ubyte3_e32 v131, v153
	v_cvt_f32_ubyte1_e32 v161, v135
	v_cvt_f32_ubyte0_e32 v160, v135
	v_rcp_iflag_f32_e32 v133, v131
	v_cvt_f32_ubyte3_e32 v153, v135
	v_cvt_f32_ubyte2_e32 v152, v135
	v_pk_mul_f32 v[134:135], v[158:159], v[160:161]
	s_waitcnt vmcnt(2)
	v_cvt_f32_ubyte0_e32 v131, v156
	v_pk_mul_f32 v[82:83], v[82:83], v[134:135]
	v_rcp_iflag_f32_e32 v134, v131
	v_cvt_f32_ubyte1_e32 v131, v156
	v_rcp_iflag_f32_e32 v135, v131
	v_cvt_f32_ubyte0_e32 v131, v157
	v_rcp_iflag_f32_e32 v158, v131
	v_cvt_f32_ubyte1_e32 v131, v157
	v_pk_mul_f32 v[132:133], v[132:133], v[152:153]
	v_rcp_iflag_f32_e32 v159, v131
	v_cvt_f32_ubyte2_e32 v131, v156
	v_pk_mul_f32 v[84:85], v[84:85], v[132:133]
	v_add_u32_e32 v132, 0x200, v130
	v_rcp_iflag_f32_e32 v160, v131
	v_cvt_f32_ubyte3_e32 v131, v156
	v_ashrrev_i32_e32 v133, 31, v132
	v_rcp_iflag_f32_e32 v161, v131
	v_lshl_add_u64 v[132:133], v[132:133], 3, s[16:17]
	v_lshl_add_u64 v[152:153], v[132:133], 0, s[26:27]
	global_load_dwordx2 v[152:153], v[152:153], off
	v_cvt_f32_ubyte3_e32 v163, v150
	v_cvt_f32_ubyte2_e32 v162, v150
	v_cvt_f32_ubyte1_e32 v165, v150
	v_cvt_f32_ubyte0_e32 v164, v150
	v_pk_mul_f32 v[134:135], v[134:135], v[164:165]
	v_pk_mul_f32 v[160:161], v[160:161], v[162:163]
	v_cvt_f32_ubyte2_e32 v131, v157
	v_pk_mul_f32 v[80:81], v[80:81], v[160:161]
	v_pk_mul_f32 v[78:79], v[78:79], v[134:135]
	v_rcp_iflag_f32_e32 v134, v131
	v_cvt_f32_ubyte3_e32 v131, v157
	v_cvt_f32_ubyte1_e32 v161, v151
	v_cvt_f32_ubyte0_e32 v160, v151
	v_rcp_iflag_f32_e32 v135, v131
	v_cvt_f32_ubyte3_e32 v157, v151
	v_cvt_f32_ubyte2_e32 v156, v151
	v_pk_mul_f32 v[150:151], v[158:159], v[160:161]
	s_waitcnt vmcnt(2)
	v_cvt_f32_ubyte0_e32 v131, v154
	v_pk_mul_f32 v[74:75], v[74:75], v[150:151]
	v_rcp_iflag_f32_e32 v150, v131
	v_cvt_f32_ubyte1_e32 v131, v154
	v_rcp_iflag_f32_e32 v151, v131
	v_cvt_f32_ubyte0_e32 v131, v155
	v_rcp_iflag_f32_e32 v158, v131
	v_cvt_f32_ubyte1_e32 v131, v155
	v_pk_mul_f32 v[134:135], v[134:135], v[156:157]
	v_rcp_iflag_f32_e32 v159, v131
	v_cvt_f32_ubyte2_e32 v131, v154
	v_lshl_add_u64 v[132:133], v[132:133], 0, s[6:7]
	v_pk_mul_f32 v[76:77], v[76:77], v[134:135]
	v_add_u32_e32 v134, 0x240, v130
	v_rcp_iflag_f32_e32 v160, v131
	v_cvt_f32_ubyte3_e32 v131, v154
	global_load_dwordx2 v[132:133], v[132:133], off
	v_ashrrev_i32_e32 v135, 31, v134
	v_rcp_iflag_f32_e32 v161, v131
	v_lshl_add_u64 v[134:135], v[134:135], 3, s[16:17]
	v_lshl_add_u64 v[156:157], v[134:135], 0, s[26:27]
	v_lshl_add_u64 v[134:135], v[134:135], 0, s[6:7]
	global_load_dwordx2 v[162:163], v[134:135], off
	s_waitcnt vmcnt(3)
	v_cvt_f32_ubyte3_e32 v135, v136
	v_cvt_f32_ubyte2_e32 v134, v136
	v_pk_mul_f32 v[134:135], v[160:161], v[134:135]
	v_cvt_f32_ubyte2_e32 v131, v155
	global_load_dwordx2 v[156:157], v[156:157], off
	v_pk_mul_f32 v[72:73], v[72:73], v[134:135]
	v_rcp_iflag_f32_e32 v134, v131
	v_cvt_f32_ubyte3_e32 v131, v155
	v_rcp_iflag_f32_e32 v135, v131
	v_cvt_f32_ubyte1_e32 v165, v136
	v_cvt_f32_ubyte0_e32 v164, v136
	v_pk_mul_f32 v[150:151], v[150:151], v[164:165]
	v_cvt_f32_ubyte1_e32 v155, v137
	v_pk_mul_f32 v[70:71], v[70:71], v[150:151]
	v_cvt_f32_ubyte3_e32 v151, v137
	v_cvt_f32_ubyte2_e32 v150, v137
	v_pk_mul_f32 v[134:135], v[134:135], v[150:151]
	v_cvt_f32_ubyte0_e32 v154, v137
	v_pk_mul_f32 v[68:69], v[68:69], v[134:135]
	v_add_u32_e32 v134, 0x280, v130
	v_ashrrev_i32_e32 v135, 31, v134
	v_lshl_add_u64 v[134:135], v[134:135], 3, s[16:17]
	v_lshl_add_u64 v[150:151], v[134:135], 0, s[26:27]
	global_load_dwordx2 v[150:151], v[150:151], off
	v_lshl_add_u64 v[134:135], v[134:135], 0, s[6:7]
	global_load_dwordx2 v[160:161], v[134:135], off
	v_pk_mul_f32 v[136:137], v[158:159], v[154:155]
	s_waitcnt vmcnt(5)
	v_cvt_f32_ubyte0_e32 v131, v152
	v_pk_mul_f32 v[66:67], v[66:67], v[136:137]
	v_rcp_iflag_f32_e32 v136, v131
	v_cvt_f32_ubyte1_e32 v131, v152
	v_rcp_iflag_f32_e32 v137, v131
	v_cvt_f32_ubyte0_e32 v131, v153
	v_rcp_iflag_f32_e32 v154, v131
	v_cvt_f32_ubyte1_e32 v131, v153
	v_rcp_iflag_f32_e32 v155, v131
	v_cvt_f32_ubyte2_e32 v131, v152
	v_rcp_iflag_f32_e32 v158, v131
	v_cvt_f32_ubyte3_e32 v131, v152
	v_rcp_iflag_f32_e32 v159, v131
	v_cvt_f32_ubyte2_e32 v131, v153
	v_add_u32_e32 v152, 0x2c0, v130
	s_waitcnt vmcnt(4)
	v_cvt_f32_ubyte3_e32 v135, v132
	v_cvt_f32_ubyte2_e32 v134, v132
	v_pk_mul_f32 v[134:135], v[158:159], v[134:135]
	v_cvt_f32_ubyte1_e32 v165, v132
	v_pk_mul_f32 v[64:65], v[64:65], v[134:135]
	v_rcp_iflag_f32_e32 v134, v131
	v_cvt_f32_ubyte3_e32 v131, v153
	v_ashrrev_i32_e32 v153, 31, v152
	v_cvt_f32_ubyte0_e32 v164, v132
	v_lshl_add_u64 v[152:153], v[152:153], 3, s[16:17]
	v_pk_mul_f32 v[136:137], v[136:137], v[164:165]
	v_rcp_iflag_f32_e32 v135, v131
	v_lshl_add_u64 v[158:159], v[152:153], 0, s[26:27]
	v_cvt_f32_ubyte1_e32 v165, v133
	v_cvt_f32_ubyte0_e32 v164, v133
	v_pk_mul_f32 v[62:63], v[62:63], v[136:137]
	v_cvt_f32_ubyte3_e32 v137, v133
	v_cvt_f32_ubyte2_e32 v136, v133
	global_load_dwordx2 v[158:159], v[158:159], off
	v_pk_mul_f32 v[132:133], v[154:155], v[164:165]
	s_waitcnt vmcnt(3)
	v_cvt_f32_ubyte0_e32 v131, v156
	v_pk_mul_f32 v[58:59], v[58:59], v[132:133]
	v_rcp_iflag_f32_e32 v132, v131
	v_cvt_f32_ubyte1_e32 v131, v156
	v_rcp_iflag_f32_e32 v133, v131
	v_cvt_f32_ubyte0_e32 v131, v157
	v_pk_mul_f32 v[134:135], v[134:135], v[136:137]
	v_rcp_iflag_f32_e32 v136, v131
	v_cvt_f32_ubyte1_e32 v131, v157
	v_rcp_iflag_f32_e32 v137, v131
	v_cvt_f32_ubyte2_e32 v131, v156
	v_rcp_iflag_f32_e32 v154, v131
	v_cvt_f32_ubyte3_e32 v131, v156
	v_rcp_iflag_f32_e32 v155, v131
	v_cvt_f32_ubyte1_e32 v165, v162
	v_cvt_f32_ubyte0_e32 v164, v162
	v_pk_mul_f32 v[132:133], v[132:133], v[164:165]
	v_cvt_f32_ubyte2_e32 v131, v157
	v_pk_mul_f32 v[60:61], v[60:61], v[134:135]
	v_lshl_add_u64 v[134:135], v[152:153], 0, s[6:7]
	v_cvt_f32_ubyte3_e32 v153, v162
	v_cvt_f32_ubyte2_e32 v152, v162
	v_pk_mul_f32 v[54:55], v[54:55], v[132:133]
	v_rcp_iflag_f32_e32 v132, v131
	v_cvt_f32_ubyte3_e32 v131, v157
	v_pk_mul_f32 v[152:153], v[154:155], v[152:153]
	v_rcp_iflag_f32_e32 v133, v131
	v_cvt_f32_ubyte1_e32 v155, v163
	v_cvt_f32_ubyte0_e32 v154, v163
	s_waitcnt vmcnt(2)
	v_cvt_f32_ubyte0_e32 v131, v150
	v_pk_mul_f32 v[136:137], v[136:137], v[154:155]
	v_rcp_iflag_f32_e32 v154, v131
	v_cvt_f32_ubyte1_e32 v131, v150
	v_rcp_iflag_f32_e32 v155, v131
	v_cvt_f32_ubyte0_e32 v131, v151
	v_rcp_iflag_f32_e32 v156, v131
	v_cvt_f32_ubyte1_e32 v131, v151
	v_pk_mul_f32 v[56:57], v[56:57], v[152:153]
	v_cvt_f32_ubyte3_e32 v153, v163
	v_cvt_f32_ubyte2_e32 v152, v163
	v_rcp_iflag_f32_e32 v157, v131
	v_cvt_f32_ubyte2_e32 v131, v150
	v_pk_mul_f32 v[132:133], v[132:133], v[152:153]
	v_rcp_iflag_f32_e32 v162, v131
	v_cvt_f32_ubyte3_e32 v131, v150
	v_pk_mul_f32 v[52:53], v[52:53], v[132:133]
	v_add_u32_e32 v132, 0x300, v130
	v_rcp_iflag_f32_e32 v163, v131
	v_cvt_f32_ubyte2_e32 v131, v151
	v_ashrrev_i32_e32 v133, 31, v132
	v_rcp_iflag_f32_e32 v150, v131
	v_cvt_f32_ubyte3_e32 v131, v151
	v_lshl_add_u64 v[152:153], v[132:133], 3, s[16:17]
	v_rcp_iflag_f32_e32 v151, v131
	v_lshl_add_u64 v[132:133], v[152:153], 0, s[26:27]
	v_pk_mul_f32 v[50:51], v[50:51], v[136:137]
	v_lshl_add_u64 v[136:137], v[152:153], 0, s[6:7]
	s_waitcnt vmcnt(1)
	v_cvt_f32_ubyte3_e32 v153, v160
	v_cvt_f32_ubyte2_e32 v152, v160
	v_pk_mul_f32 v[152:153], v[162:163], v[152:153]
	global_load_dwordx2 v[134:135], v[134:135], off
	v_pk_mul_f32 v[48:49], v[48:49], v[152:153]
	v_cvt_f32_ubyte3_e32 v153, v161
	v_cvt_f32_ubyte2_e32 v152, v161
	v_pk_mul_f32 v[150:151], v[150:151], v[152:153]
	global_load_dwordx2 v[136:137], v[136:137], off
	v_pk_mul_f32 v[44:45], v[44:45], v[150:151]
	v_add_u32_e32 v150, 0x340, v130
	v_ashrrev_i32_e32 v151, 31, v150
	v_lshl_add_u64 v[150:151], v[150:151], 3, s[16:17]
	v_lshl_add_u64 v[152:153], v[150:151], 0, s[26:27]
	global_load_dwordx2 v[152:153], v[152:153], off
	v_cvt_f32_ubyte1_e32 v165, v160
	global_load_dwordx2 v[132:133], v[132:133], off
	v_cvt_f32_ubyte0_e32 v164, v160
	v_pk_mul_f32 v[154:155], v[154:155], v[164:165]
	v_lshl_add_u64 v[150:151], v[150:151], 0, s[6:7]
	v_pk_mul_f32 v[46:47], v[46:47], v[154:155]
	v_cvt_f32_ubyte1_e32 v155, v161
	v_cvt_f32_ubyte0_e32 v154, v161
	v_pk_mul_f32 v[154:155], v[156:157], v[154:155]
	s_waitcnt vmcnt(4)
	v_cvt_f32_ubyte0_e32 v131, v158
	v_pk_mul_f32 v[42:43], v[42:43], v[154:155]
	v_rcp_iflag_f32_e32 v154, v131
	v_cvt_f32_ubyte1_e32 v131, v158
	v_rcp_iflag_f32_e32 v155, v131
	v_cvt_f32_ubyte0_e32 v131, v159
	v_rcp_iflag_f32_e32 v156, v131
	v_cvt_f32_ubyte1_e32 v131, v159
	v_rcp_iflag_f32_e32 v157, v131
	v_cvt_f32_ubyte2_e32 v131, v158
	v_rcp_iflag_f32_e32 v160, v131
	v_cvt_f32_ubyte3_e32 v131, v158
	v_rcp_iflag_f32_e32 v161, v131
	global_load_dwordx2 v[150:151], v[150:151], off
	v_cvt_f32_ubyte2_e32 v131, v159
	s_waitcnt vmcnt(4)
	v_cvt_f32_ubyte3_e32 v163, v134
	v_cvt_f32_ubyte2_e32 v162, v134
	v_cvt_f32_ubyte1_e32 v165, v134
	v_cvt_f32_ubyte0_e32 v164, v134
	v_pk_mul_f32 v[160:161], v[160:161], v[162:163]
	v_pk_mul_f32 v[154:155], v[154:155], v[164:165]
	v_pk_mul_f32 v[40:41], v[40:41], v[160:161]
	v_add_u32_e32 v160, 0x380, v130
	v_pk_mul_f32 v[38:39], v[38:39], v[154:155]
	v_rcp_iflag_f32_e32 v154, v131
	v_cvt_f32_ubyte3_e32 v131, v159
	v_ashrrev_i32_e32 v161, 31, v160
	v_rcp_iflag_f32_e32 v155, v131
	v_lshl_add_u64 v[160:161], v[160:161], 3, s[16:17]
	v_lshl_add_u64 v[162:163], v[160:161], 0, s[26:27]
	v_cvt_f32_ubyte1_e32 v165, v135
	v_cvt_f32_ubyte0_e32 v164, v135
	v_cvt_f32_ubyte3_e32 v159, v135
	v_cvt_f32_ubyte2_e32 v158, v135
	global_load_dwordx2 v[162:163], v[162:163], off
	v_pk_mul_f32 v[134:135], v[156:157], v[164:165]
	s_waitcnt vmcnt(2)
	v_cvt_f32_ubyte0_e32 v131, v132
	v_pk_mul_f32 v[34:35], v[34:35], v[134:135]
	v_rcp_iflag_f32_e32 v134, v131
	v_cvt_f32_ubyte1_e32 v131, v132
	v_pk_mul_f32 v[154:155], v[154:155], v[158:159]
	v_rcp_iflag_f32_e32 v135, v131
	v_cvt_f32_ubyte0_e32 v131, v133
	v_pk_mul_f32 v[36:37], v[36:37], v[154:155]
	v_lshl_add_u64 v[154:155], v[160:161], 0, s[6:7]
	v_rcp_iflag_f32_e32 v156, v131
	v_cvt_f32_ubyte1_e32 v131, v133
	global_load_dwordx2 v[154:155], v[154:155], off
	v_rcp_iflag_f32_e32 v157, v131
	v_cvt_f32_ubyte2_e32 v131, v132
	v_rcp_iflag_f32_e32 v158, v131
	v_cvt_f32_ubyte3_e32 v131, v132
	v_rcp_iflag_f32_e32 v159, v131
	v_add_u32_e32 v130, 0x3c0, v130
	v_cvt_f32_ubyte3_e32 v161, v136
	v_cvt_f32_ubyte2_e32 v160, v136
	v_ashrrev_i32_e32 v131, 31, v130
	v_pk_mul_f32 v[158:159], v[158:159], v[160:161]
	v_lshl_add_u64 v[130:131], v[130:131], 3, s[16:17]
	v_pk_mul_f32 v[32:33], v[32:33], v[158:159]
	v_lshl_add_u64 v[158:159], v[130:131], 0, s[26:27]
	global_load_dwordx2 v[158:159], v[158:159], off
	v_lshl_add_u64 v[130:131], v[130:131], 0, s[6:7]
	global_load_dwordx2 v[130:131], v[130:131], off
	v_cvt_f32_ubyte2_e32 v132, v133
	v_cvt_f32_ubyte3_e32 v133, v133
	v_rcp_iflag_f32_e32 v132, v132
	v_rcp_iflag_f32_e32 v133, v133
	v_cvt_f32_ubyte1_e32 v165, v136
	v_cvt_f32_ubyte0_e32 v164, v136
	v_pk_mul_f32 v[134:135], v[134:135], v[164:165]
	v_cvt_f32_ubyte1_e32 v161, v137
	v_pk_mul_f32 v[30:31], v[30:31], v[134:135]
	v_cvt_f32_ubyte3_e32 v135, v137
	v_cvt_f32_ubyte2_e32 v134, v137
	v_pk_mul_f32 v[132:133], v[132:133], v[134:135]
	v_cvt_f32_ubyte0_e32 v160, v137
	v_pk_mul_f32 v[28:29], v[28:29], v[132:133]
	v_cvt_f32_ubyte0_e32 v132, v152
	v_cvt_f32_ubyte1_e32 v133, v152
	v_rcp_iflag_f32_e32 v132, v132
	v_rcp_iflag_f32_e32 v133, v133
	v_pk_mul_f32 v[136:137], v[156:157], v[160:161]
	s_waitcnt vmcnt(4)
	v_cvt_f32_ubyte1_e32 v161, v150
	v_pk_mul_f32 v[26:27], v[26:27], v[136:137]
	v_cvt_f32_ubyte2_e32 v136, v152
	v_cvt_f32_ubyte3_e32 v137, v152
	v_cvt_f32_ubyte0_e32 v160, v150
	v_rcp_iflag_f32_e32 v136, v136
	v_rcp_iflag_f32_e32 v137, v137
	v_pk_mul_f32 v[132:133], v[132:133], v[160:161]
	v_cvt_f32_ubyte3_e32 v157, v150
	v_pk_mul_f32 v[22:23], v[22:23], v[132:133]
	v_cvt_f32_ubyte2_e32 v132, v153
	v_cvt_f32_ubyte3_e32 v133, v153
	v_rcp_iflag_f32_e32 v132, v132
	v_rcp_iflag_f32_e32 v133, v133
	v_cvt_f32_ubyte2_e32 v156, v150
	v_pk_mul_f32 v[136:137], v[136:137], v[156:157]
	v_cvt_f32_ubyte0_e32 v134, v153
	v_pk_mul_f32 v[24:25], v[24:25], v[136:137]
	v_cvt_f32_ubyte3_e32 v137, v151
	v_cvt_f32_ubyte2_e32 v136, v151
	v_cvt_f32_ubyte1_e32 v135, v153
	v_pk_mul_f32 v[132:133], v[132:133], v[136:137]
	v_rcp_iflag_f32_e32 v134, v134
	v_rcp_iflag_f32_e32 v135, v135
	v_pk_mul_f32 v[20:21], v[20:21], v[132:133]
	v_cvt_f32_ubyte1_e32 v153, v151
	v_cvt_f32_ubyte0_e32 v152, v151
	v_pk_mul_f32 v[134:135], v[134:135], v[152:153]
	s_waitcnt vmcnt(3)
	v_cvt_f32_ubyte0_e32 v132, v162
	v_cvt_f32_ubyte1_e32 v133, v162
	v_rcp_iflag_f32_e32 v132, v132
	v_rcp_iflag_f32_e32 v133, v133
	v_cvt_f32_ubyte2_e32 v136, v162
	v_cvt_f32_ubyte3_e32 v137, v162
	v_rcp_iflag_f32_e32 v136, v136
	v_rcp_iflag_f32_e32 v137, v137
	v_pk_mul_f32 v[18:19], v[18:19], v[134:135]
	v_cvt_f32_ubyte0_e32 v134, v163
	v_cvt_f32_ubyte1_e32 v135, v163
	v_rcp_iflag_f32_e32 v134, v134
	v_rcp_iflag_f32_e32 v135, v135
	s_waitcnt vmcnt(2)
	v_cvt_f32_ubyte1_e32 v153, v154
	v_cvt_f32_ubyte0_e32 v152, v154
	v_pk_mul_f32 v[132:133], v[132:133], v[152:153]
	v_cvt_f32_ubyte3_e32 v151, v154
	v_pk_mul_f32 v[14:15], v[14:15], v[132:133]
	v_cvt_f32_ubyte2_e32 v132, v163
	v_cvt_f32_ubyte3_e32 v133, v163
	v_rcp_iflag_f32_e32 v132, v132
	v_rcp_iflag_f32_e32 v133, v133
	v_cvt_f32_ubyte2_e32 v150, v154
	v_pk_mul_f32 v[136:137], v[136:137], v[150:151]
	v_cvt_f32_ubyte1_e32 v151, v155
	v_pk_mul_f32 v[16:17], v[16:17], v[136:137]
	v_cvt_f32_ubyte3_e32 v137, v155
	v_cvt_f32_ubyte2_e32 v136, v155
	v_pk_mul_f32 v[132:133], v[132:133], v[136:137]
	v_cvt_f32_ubyte0_e32 v150, v155
	v_pk_mul_f32 v[12:13], v[12:13], v[132:133]
	s_waitcnt vmcnt(1)
	v_cvt_f32_ubyte0_e32 v132, v158
	v_cvt_f32_ubyte1_e32 v133, v158
	v_rcp_iflag_f32_e32 v132, v132
	v_rcp_iflag_f32_e32 v133, v133
	v_cvt_f32_ubyte2_e32 v136, v158
	v_cvt_f32_ubyte3_e32 v137, v158
	s_waitcnt vmcnt(0)
	v_cvt_f32_ubyte1_e32 v153, v130
	v_cvt_f32_ubyte0_e32 v152, v130
	v_pk_mul_f32 v[134:135], v[134:135], v[150:151]
	v_rcp_iflag_f32_e32 v136, v136
	v_rcp_iflag_f32_e32 v137, v137
	v_cvt_f32_ubyte3_e32 v151, v130
	v_cvt_f32_ubyte2_e32 v150, v130
	v_pk_mul_f32 v[132:133], v[132:133], v[152:153]
	v_cvt_f32_ubyte2_e32 v130, v159
	v_pk_mul_f32 v[10:11], v[10:11], v[134:135]
	v_cvt_f32_ubyte0_e32 v134, v159
	v_cvt_f32_ubyte1_e32 v135, v159
	v_pk_mul_f32 v[6:7], v[6:7], v[132:133]
	v_rcp_iflag_f32_e32 v132, v130
	v_cvt_f32_ubyte3_e32 v130, v159
	v_rcp_iflag_f32_e32 v134, v134
	v_rcp_iflag_f32_e32 v135, v135
	v_rcp_iflag_f32_e32 v133, v130
	v_pk_mul_f32 v[136:137], v[136:137], v[150:151]
	v_cvt_f32_ubyte1_e32 v151, v131
	v_pk_mul_f32 v[8:9], v[8:9], v[136:137]
	v_cvt_f32_ubyte3_e32 v137, v131
	v_cvt_f32_ubyte2_e32 v136, v131
	v_cvt_f32_ubyte0_e32 v150, v131
	v_pk_mul_f32 v[130:131], v[134:135], v[150:151]
	v_pk_mul_f32 v[132:133], v[132:133], v[136:137]
	v_pk_mul_f32 v[2:3], v[2:3], v[130:131]
	v_pk_mul_f32 v[4:5], v[4:5], v[132:133]

.LBB0_3119:
	ds_read_b128 v[148:151], v143
	ds_read_b128 v[152:155], v143 offset:1024
	ds_read_b128 v[156:159], v143 offset:2048
	ds_read_b128 v[160:163], v143 offset:3072
	ds_read_b128 v[164:167], v144
	ds_read_b128 v[168:171], v144 offset:1024
	ds_read_b128 v[172:175], v144 offset:2048
	ds_read_b128 v[176:179], v144 offset:3072
	s_add_i32 s6, s60, 0xfffc0080
	s_cmp_eq_u32 s62, 12
	s_cselect_b32 s65, s59, s6
	s_cselect_b32 s64, s58, s61
	s_or_b32 s63, s65, 0x80
	s_mov_b32 m0, s49
	ds_read_b128 v[180:183], v145
	ds_read_b128 v[184:187], v145 offset:1024
	ds_read_b128 v[188:191], v145 offset:2048
	ds_read_b128 v[192:195], v145 offset:3072
	ds_read_b128 v[196:199], v145 offset:4096
	ds_read_b128 v[200:203], v145 offset:5120
	ds_read_b128 v[204:207], v145 offset:6144
	ds_read_b128 v[208:211], v145 offset:7168
	buffer_load_dwordx4 v139, s[8:11], s60 offen lds
	s_mov_b32 m0, s50
	s_nop 0
	buffer_load_dwordx4 v140, s[8:11], s60 offen lds
	s_waitcnt vmcnt(8)
	s_waitcnt lgkmcnt(0)
	s_barrier
	s_waitcnt lgkmcnt(6)
	v_mfma_f32_16x16x128_f8f6f4 v[126:129], v[148:155], v[180:187], v[126:129]
	v_mfma_f32_16x16x128_f8f6f4 v[122:125], v[156:163], v[180:187], v[122:125]
	s_waitcnt lgkmcnt(4)
	v_mfma_f32_16x16x128_f8f6f4 v[114:117], v[148:155], v[188:195], v[114:117]
	v_mfma_f32_16x16x128_f8f6f4 v[106:109], v[156:163], v[188:195], v[106:109]
	s_waitcnt lgkmcnt(2)
	v_mfma_f32_16x16x128_f8f6f4 v[98:101], v[148:155], v[196:203], v[98:101]
	v_mfma_f32_16x16x128_f8f6f4 v[134:137], v[156:163], v[196:203], v[90:93]
	s_waitcnt lgkmcnt(0)
	v_mfma_f32_16x16x128_f8f6f4 v[212:215], v[148:155], v[204:211], v[82:85]
	v_mfma_f32_16x16x128_f8f6f4 v[216:219], v[156:163], v[204:211], v[74:77]
	v_mfma_f32_16x16x128_f8f6f4 v[118:121], v[164:171], v[180:187], v[118:121]
	v_mfma_f32_16x16x128_f8f6f4 v[110:113], v[172:179], v[180:187], v[110:113]
	v_mfma_f32_16x16x128_f8f6f4 v[102:105], v[164:171], v[188:195], v[102:105]
	v_mfma_f32_16x16x128_f8f6f4 v[180:183], v[172:179], v[188:195], v[94:97]
	v_mfma_f32_16x16x128_f8f6f4 v[184:187], v[164:171], v[196:203], v[86:89]
	v_mfma_f32_16x16x128_f8f6f4 v[188:191], v[172:179], v[196:203], v[78:81]
	v_mfma_f32_16x16x128_f8f6f4 v[192:195], v[164:171], v[204:211], v[62:65]
	v_mfma_f32_16x16x128_f8f6f4 v[196:199], v[172:179], v[204:211], v[58:61]
	s_barrier
	s_mov_b32 m0, s26
	s_mov_b32 s6, s10
	s_mov_b32 s7, s11
	s_nop 1
	ds_read_b128 v[58:61], v145 offset:16384
	ds_read_b128 v[62:65], v145 offset:17408
	ds_read_b128 v[74:77], v145 offset:18432
	ds_read_b128 v[78:81], v145 offset:19456
	ds_read_b128 v[82:85], v145 offset:20480
	ds_read_b128 v[86:89], v145 offset:21504
	ds_read_b128 v[90:93], v145 offset:22528
	ds_read_b128 v[94:97], v145 offset:23552
	buffer_load_dwordx4 v1, s[4:7], s64 offen lds
	s_mov_b32 m0, s27
	s_add_i32 s66, s64, 0x40000
	buffer_load_dwordx4 v138, s[4:7], s64 offen lds
	s_mov_b32 m0, s28
	s_nop 0
	buffer_load_dwordx4 v1, s[4:7], s66 offen lds
	s_mov_b32 m0, s29
	s_nop 0
	buffer_load_dwordx4 v138, s[4:7], s66 offen lds
	s_mov_b32 m0, s25
	s_nop 0
	buffer_load_dwordx4 v139, s[8:11], s65 offen lds
	s_mov_b32 m0, s30
	s_nop 0
	buffer_load_dwordx4 v140, s[8:11], s65 offen lds
	s_waitcnt vmcnt(8)
	s_waitcnt lgkmcnt(0)
	s_barrier
	s_waitcnt lgkmcnt(4)
	v_mfma_f32_16x16x128_f8f6f4 v[18:21], v[156:163], v[74:81], v[18:21]
	v_mfma_f32_16x16x128_f8f6f4 v[200:203], v[148:155], v[58:65], v[46:49]
	v_mfma_f32_16x16x128_f8f6f4 v[204:207], v[156:163], v[58:65], v[42:45]
	v_mfma_f32_16x16x128_f8f6f4 v[208:211], v[148:155], v[74:81], v[30:33]
	s_waitcnt lgkmcnt(2)
	v_mfma_f32_16x16x128_f8f6f4 v[220:223], v[148:155], v[82:89], v[14:17]
	v_mfma_f32_16x16x128_f8f6f4 v[224:227], v[156:163], v[82:89], v[10:13]
	s_waitcnt lgkmcnt(0)
	v_mfma_f32_16x16x128_f8f6f4 v[228:231], v[148:155], v[90:97], v[6:9]
	v_mfma_f32_16x16x128_f8f6f4 v[232:235], v[156:163], v[90:97], v[2:5]
	v_mfma_f32_16x16x128_f8f6f4 v[66:69], v[164:171], v[58:65], v[66:69]
	v_mfma_f32_16x16x128_f8f6f4 v[70:73], v[172:179], v[58:65], v[70:73]
	v_mfma_f32_16x16x128_f8f6f4 v[54:57], v[172:179], v[74:81], v[54:57]
	v_mfma_f32_16x16x128_f8f6f4 v[236:239], v[164:171], v[74:81], v[50:53]
	v_mfma_f32_16x16x128_f8f6f4 v[240:243], v[164:171], v[82:89], v[34:37]
	v_mfma_f32_16x16x128_f8f6f4 v[244:247], v[172:179], v[82:89], v[38:41]
	v_mfma_f32_16x16x128_f8f6f4 v[248:251], v[164:171], v[90:97], v[22:25]
	v_mfma_f32_16x16x128_f8f6f4 v[252:255], v[172:179], v[90:97], v[26:29]
	s_barrier
	ds_read_b128 v[2:5], v146
	ds_read_b128 v[6:9], v146 offset:1024
	s_nop 1
	ds_read_b128 v[22:25], v146 offset:2048
	ds_read_b128 v[26:29], v146 offset:3072
	ds_read_b128 v[148:151], v147
	ds_read_b128 v[152:155], v147 offset:1024
	ds_read_b128 v[156:159], v147 offset:2048
	ds_read_b128 v[160:163], v147 offset:3072
	s_add_i32 s65, s65, 0x40000
	s_mov_b32 m0, s31
	ds_read_b128 v[10:13], v145 offset:32768
	ds_read_b128 v[14:17], v145 offset:33792
	ds_read_b128 v[30:33], v145 offset:34816
	ds_read_b128 v[34:37], v145 offset:35840
	ds_read_b128 v[38:41], v145 offset:36864
	ds_read_b128 v[42:45], v145 offset:37888
	ds_read_b128 v[46:49], v145 offset:38912
	ds_read_b128 v[50:53], v145 offset:39936
	buffer_load_dwordx4 v139, s[8:11], s65 offen lds
	s_mov_b32 m0, s33
	s_nop 0
	buffer_load_dwordx4 v140, s[8:11], s65 offen lds
	s_waitcnt vmcnt(8)
	s_waitcnt lgkmcnt(0)
	s_barrier
	s_waitcnt lgkmcnt(6)
	v_mfma_f32_16x16x128_f8f6f4 v[126:129], v[2:9], v[10:17], v[126:129]
	v_mfma_f32_16x16x128_f8f6f4 v[122:125], v[22:29], v[10:17], v[122:125]
	s_waitcnt lgkmcnt(4)
	v_mfma_f32_16x16x128_f8f6f4 v[114:117], v[2:9], v[30:37], v[114:117]
	v_mfma_f32_16x16x128_f8f6f4 v[106:109], v[22:29], v[30:37], v[106:109]
	s_waitcnt lgkmcnt(2)
	v_mfma_f32_16x16x128_f8f6f4 v[98:101], v[2:9], v[38:45], v[98:101]
	v_mfma_f32_16x16x128_f8f6f4 v[90:93], v[22:29], v[38:45], v[134:137]
	s_waitcnt lgkmcnt(0)
	v_mfma_f32_16x16x128_f8f6f4 v[82:85], v[2:9], v[46:53], v[212:215]
	v_mfma_f32_16x16x128_f8f6f4 v[74:77], v[22:29], v[46:53], v[216:219]
	v_mfma_f32_16x16x128_f8f6f4 v[118:121], v[148:155], v[10:17], v[118:121]
	v_mfma_f32_16x16x128_f8f6f4 v[110:113], v[156:163], v[10:17], v[110:113]
	v_mfma_f32_16x16x128_f8f6f4 v[102:105], v[148:155], v[30:37], v[102:105]
	v_mfma_f32_16x16x128_f8f6f4 v[94:97], v[156:163], v[30:37], v[180:183]
	v_mfma_f32_16x16x128_f8f6f4 v[86:89], v[148:155], v[38:45], v[184:187]
	v_mfma_f32_16x16x128_f8f6f4 v[78:81], v[156:163], v[38:45], v[188:191]
	v_mfma_f32_16x16x128_f8f6f4 v[62:65], v[148:155], v[46:53], v[192:195]
	v_mfma_f32_16x16x128_f8f6f4 v[58:61], v[156:163], v[46:53], v[196:199]
	s_barrier
	s_mov_b32 m0, s34
	s_or_b32 s65, s64, 0x80
	ds_read_b128 v[34:37], v145 offset:49152
	ds_read_b128 v[38:41], v145 offset:50176
	ds_read_b128 v[164:167], v145 offset:51200
	ds_read_b128 v[168:171], v145 offset:52224
	ds_read_b128 v[172:175], v145 offset:53248
	ds_read_b128 v[176:179], v145 offset:54272
	ds_read_b128 v[180:183], v145 offset:55296
	ds_read_b128 v[184:187], v145 offset:56320
	buffer_load_dwordx4 v1, s[4:7], s65 offen lds
	s_mov_b32 m0, s35
	s_add_i32 s64, s64, 0x40080
	buffer_load_dwordx4 v138, s[4:7], s65 offen lds
	s_mov_b32 m0, s46
	s_nop 0
	buffer_load_dwordx4 v1, s[4:7], s64 offen lds
	s_mov_b32 m0, s47
	s_nop 0
	buffer_load_dwordx4 v138, s[4:7], s64 offen lds
	s_mov_b32 m0, s38
	s_nop 0
	buffer_load_dwordx4 v139, s[8:11], s63 offen lds
	s_mov_b32 m0, s39
	s_nop 0
	buffer_load_dwordx4 v140, s[8:11], s63 offen lds
	s_waitcnt vmcnt(8)
	s_waitcnt lgkmcnt(0)
	s_barrier
	s_waitcnt lgkmcnt(6)
	v_mfma_f32_16x16x128_f8f6f4 v[46:49], v[2:9], v[34:41], v[200:203]
	v_mfma_f32_16x16x128_f8f6f4 v[42:45], v[22:29], v[34:41], v[204:207]
	s_waitcnt lgkmcnt(4)
	v_mfma_f32_16x16x128_f8f6f4 v[30:33], v[2:9], v[164:171], v[208:211]
	v_mfma_f32_16x16x128_f8f6f4 v[18:21], v[22:29], v[164:171], v[18:21]
	s_waitcnt lgkmcnt(2)
	v_mfma_f32_16x16x128_f8f6f4 v[14:17], v[2:9], v[172:179], v[220:223]
	v_mfma_f32_16x16x128_f8f6f4 v[10:13], v[22:29], v[172:179], v[224:227]
	s_waitcnt lgkmcnt(0)
	v_mfma_f32_16x16x128_f8f6f4 v[6:9], v[2:9], v[180:187], v[228:231]
	v_mfma_f32_16x16x128_f8f6f4 v[2:5], v[22:29], v[180:187], v[232:235]
	v_mfma_f32_16x16x128_f8f6f4 v[66:69], v[148:155], v[34:41], v[66:69]
	v_mfma_f32_16x16x128_f8f6f4 v[70:73], v[156:163], v[34:41], v[70:73]
	v_mfma_f32_16x16x128_f8f6f4 v[50:53], v[148:155], v[164:171], v[236:239]
	v_mfma_f32_16x16x128_f8f6f4 v[54:57], v[156:163], v[164:171], v[54:57]
	v_mfma_f32_16x16x128_f8f6f4 v[34:37], v[148:155], v[172:179], v[240:243]
	v_mfma_f32_16x16x128_f8f6f4 v[38:41], v[156:163], v[172:179], v[244:247]
	v_mfma_f32_16x16x128_f8f6f4 v[22:25], v[148:155], v[180:187], v[248:251]
	v_mfma_f32_16x16x128_f8f6f4 v[26:29], v[156:163], v[180:187], v[252:255]
	s_barrier
	s_add_i32 s62, s62, 2
	s_addk_i32 s60, 0x100
	s_addk_i32 s61, 0x100
	s_cmp_gt_u32 s62, 13
	s_cbranch_scc0 .LBB0_3119
	s_and_b64 vcc, exec, s[20:21]
	s_cbranch_vccz .LBB0_3122
	s_barrier
